# PEER retrieval scores: the eight key-fragment LDS reads of a 32-key block issued together with counted lgkmcnt per MFMA (12 of 16 blocks; the compiler had batched the other 4)
# speedup vs baseline: 1.0051x; 1.0051x over previous
; #define LAS __attribute__((address_space(3)))
; __device__ __forceinline__ void phase_topk(Frame& F, const bf16_t* QP, const bf16_t* K1B, const bf16_t* K2B, unsigned short* EID, float* GATE) {
;     ...
;             { const int tnx = tile + nbh * NWAVES, tl = half ? (tnx < TOK / 32 ? tnx : tile) : tile;
;               const bf16_t* qrow = QP + (size_t)(tl * 32 + r32) * 2048 + h * 256 + (half ? 0 : 128) + 8 * hi;
; #pragma unroll
;               for (int kk = 0; kk < 8; ++kk) qn[kk] = *(const bf16x8*)(qrow + 16 * kk); }
;             unsigned K[64];
; #pragma unroll
;             for (int nb = 0; nb < 4; ++nb) { f32x16 acc = f32x16{};
;                 LAS const unsigned char* kb = F.lds + half * TK_KSET + (nb * 32 + r32) * TK_KSTRIDE + 16 * hi; asm volatile("" : "+v"(kb));
; #pragma unroll
;                 for (int kk = 0; kk < 8; ++kk) acc = __builtin_amdgcn_mfma_f32_32x32x16_bf16(*(LAS const bf16x8*)(kb + 32 * kk), qf[kk], acc, 0, 0, 0);
; #pragma unroll
;                 for (int r = 0; r < 16; ++r) {
;                     const unsigned x = __float_as_uint(acc[r]), o = x ^ ((unsigned)((int)x >> 31) | 0x80000000u); const int j = r >> 2;
;                     const unsigned pack = (unsigned)(127 - (nb * 32 + 0 + 8 * j)) | ((unsigned)(127 - (nb * 32 + 1 + 8 * j)) << 8) | ((unsigned)(127 - (nb * 32 + 2 + 8 * j)) << 16) | ((unsigned)(127 - (nb * 32 + 3 + 8 * j)) << 24);
;                     K[nb * 16 + r] = __builtin_amdgcn_perm(o, pack, 0x07060500u | (unsigned)(r & 3)); }
;                 __builtin_amdgcn_sched_barrier(0); }
.LBB0_822:
	v_ashrrev_i32_e32 v81, 31, v80
	v_lshlrev_b64 v[0:1], 12, v[80:81]
	v_mov_b32_e32 v105, v89
	v_lshl_add_u64 v[0:1], v[86:87], 0, v[0:1]
	global_load_dwordx4 v[76:79], v[0:1], off offset:256
	global_load_dwordx4 v[72:75], v[0:1], off offset:288
	global_load_dwordx4 v[68:71], v[0:1], off offset:320
	global_load_dwordx4 v[64:67], v[0:1], off offset:352
	global_load_dwordx4 v[60:63], v[0:1], off offset:384
	global_load_dwordx4 v[56:59], v[0:1], off offset:416
	global_load_dwordx4 v[52:55], v[0:1], off offset:448
	global_load_dwordx4 v[48:51], v[0:1], off offset:480
	v_mov_b32_e32 v114, v91
	ds_read_b128 v[0:3], v114
	ds_read_b128 v[106:109], v114 offset:32
	ds_read_b128 v[110:113], v114 offset:64
	ds_read_b128 v[186:189], v114 offset:96
	ds_read_b128 v[190:193], v114 offset:128
	ds_read_b128 v[194:197], v114 offset:160
	ds_read_b128 v[198:201], v114 offset:192
	ds_read_b128 v[202:205], v114 offset:224
	s_waitcnt vmcnt(8) lgkmcnt(7)
	v_mfma_f32_32x32x16_bf16 v[0:15], v[0:3], v[44:47], 0
	s_add_i32 s31, s33, s8
	s_cmpk_lt_i32 s31, 0x400
	s_cselect_b64 s[4:5], -1, 0
	s_and_b64 s[34:35], s[4:5], exec
	s_cselect_b32 s33, s31, s33
	s_waitcnt lgkmcnt(6)
	v_mfma_f32_32x32x16_bf16 v[0:15], v[106:109], v[40:43], v[0:15]
	s_waitcnt lgkmcnt(5)
	v_mfma_f32_32x32x16_bf16 v[0:15], v[110:113], v[36:39], v[0:15]
	s_waitcnt lgkmcnt(4)
	v_mfma_f32_32x32x16_bf16 v[0:15], v[186:189], v[32:35], v[0:15]
	s_waitcnt lgkmcnt(3)
	v_mfma_f32_32x32x16_bf16 v[0:15], v[190:193], v[28:31], v[0:15]
	s_waitcnt lgkmcnt(2)
	v_mfma_f32_32x32x16_bf16 v[0:15], v[194:197], v[24:27], v[0:15]
	s_waitcnt lgkmcnt(1)
	v_mfma_f32_32x32x16_bf16 v[0:15], v[198:201], v[20:23], v[0:15]
	s_waitcnt lgkmcnt(0)
	v_mfma_f32_32x32x16_bf16 v[0:15], v[202:205], v[16:19], v[0:15]
	s_nop 11
	v_ashrrev_i32_e32 v106, 31, v0
	v_ashrrev_i32_e32 v114, 31, v8
	v_bitop3_b32 v0, v106, v0, s11 bitop3:0x36
	v_ashrrev_i32_e32 v107, 31, v1
	v_ashrrev_i32_e32 v108, 31, v2
	v_ashrrev_i32_e32 v109, 31, v3
	v_ashrrev_i32_e32 v110, 31, v4
	v_ashrrev_i32_e32 v111, 31, v5
	v_ashrrev_i32_e32 v112, 31, v6
	v_ashrrev_i32_e32 v113, 31, v7
	v_ashrrev_i32_e32 v115, 31, v9
	v_ashrrev_i32_e32 v116, 31, v10
	v_ashrrev_i32_e32 v117, 31, v11
	v_ashrrev_i32_e32 v118, 31, v12
	v_ashrrev_i32_e32 v119, 31, v13
	v_ashrrev_i32_e32 v120, 31, v14
	v_bitop3_b32 v8, v114, v8, s11 bitop3:0x36
	v_perm_b32 v114, v0, s12, v100
	v_ashrrev_i32_e32 v0, 31, v15
	v_bitop3_b32 v1, v107, v1, s11 bitop3:0x36
	v_bitop3_b32 v2, v108, v2, s11 bitop3:0x36
	v_bitop3_b32 v3, v109, v3, s11 bitop3:0x36
	v_bitop3_b32 v4, v110, v4, s11 bitop3:0x36
	v_bitop3_b32 v5, v111, v5, s11 bitop3:0x36
	v_bitop3_b32 v6, v112, v6, s11 bitop3:0x36
	v_bitop3_b32 v7, v113, v7, s11 bitop3:0x36
	v_bitop3_b32 v9, v115, v9, s11 bitop3:0x36
	v_bitop3_b32 v10, v116, v10, s11 bitop3:0x36
	v_bitop3_b32 v11, v117, v11, s11 bitop3:0x36
	v_bitop3_b32 v12, v118, v12, s11 bitop3:0x36
	v_bitop3_b32 v13, v119, v13, s11 bitop3:0x36
	v_bitop3_b32 v14, v120, v14, s11 bitop3:0x36
	v_bitop3_b32 v0, v0, v15, s11 bitop3:0x36
	v_perm_b32 v115, v1, s12, v101
	v_perm_b32 v116, v2, s12, v102
	v_perm_b32 v117, v3, s12, v103
	v_perm_b32 v118, v4, s13, v100
	v_perm_b32 v119, v5, s13, v101
	v_perm_b32 v120, v6, s13, v102
	v_perm_b32 v121, v7, s13, v103
	v_perm_b32 v122, v8, s14, v100
	v_perm_b32 v123, v9, s14, v101
	v_perm_b32 v124, v10, s14, v102
	v_perm_b32 v125, v11, s14, v103
	v_perm_b32 v126, v12, s15, v100
	v_perm_b32 v127, v13, s15, v101
	v_perm_b32 v128, v14, s15, v102
	v_perm_b32 v129, v0, s15, v103
	v_mov_b32_e32 v130, v92
	ds_read_b128 v[0:3], v130
	ds_read_b128 v[106:109], v130 offset:32
	ds_read_b128 v[110:113], v130 offset:64
	ds_read_b128 v[186:189], v130 offset:96
	ds_read_b128 v[190:193], v130 offset:128
	ds_read_b128 v[194:197], v130 offset:160
	ds_read_b128 v[198:201], v130 offset:192
	ds_read_b128 v[202:205], v130 offset:224
	s_waitcnt lgkmcnt(7)
	v_mfma_f32_32x32x16_bf16 v[0:15], v[0:3], v[44:47], 0
	s_waitcnt lgkmcnt(6)
	v_mfma_f32_32x32x16_bf16 v[0:15], v[106:109], v[40:43], v[0:15]
	s_waitcnt lgkmcnt(5)
	v_mfma_f32_32x32x16_bf16 v[0:15], v[110:113], v[36:39], v[0:15]
	s_waitcnt lgkmcnt(4)
	v_mfma_f32_32x32x16_bf16 v[0:15], v[186:189], v[32:35], v[0:15]
	s_waitcnt lgkmcnt(3)
	v_mfma_f32_32x32x16_bf16 v[0:15], v[190:193], v[28:31], v[0:15]
	s_waitcnt lgkmcnt(2)
	v_mfma_f32_32x32x16_bf16 v[0:15], v[194:197], v[24:27], v[0:15]
	s_waitcnt lgkmcnt(1)
	v_mfma_f32_32x32x16_bf16 v[0:15], v[198:201], v[20:23], v[0:15]
	s_waitcnt lgkmcnt(0)
	v_mfma_f32_32x32x16_bf16 v[0:15], v[202:205], v[16:19], v[0:15]
	s_nop 11
	v_ashrrev_i32_e32 v106, 31, v0
	v_ashrrev_i32_e32 v107, 31, v1
	v_ashrrev_i32_e32 v108, 31, v2
	v_ashrrev_i32_e32 v109, 31, v3
	v_ashrrev_i32_e32 v110, 31, v4
	v_ashrrev_i32_e32 v111, 31, v5
	v_ashrrev_i32_e32 v112, 31, v6
	v_ashrrev_i32_e32 v113, 31, v7
	v_ashrrev_i32_e32 v130, 31, v8
	v_ashrrev_i32_e32 v131, 31, v9
	v_ashrrev_i32_e32 v132, 31, v10
	v_ashrrev_i32_e32 v133, 31, v11
	v_ashrrev_i32_e32 v134, 31, v12
	v_ashrrev_i32_e32 v135, 31, v13
	v_ashrrev_i32_e32 v136, 31, v14
	v_ashrrev_i32_e32 v137, 31, v15
	v_bitop3_b32 v0, v106, v0, s11 bitop3:0x36
	v_bitop3_b32 v1, v107, v1, s11 bitop3:0x36
	v_bitop3_b32 v2, v108, v2, s11 bitop3:0x36
	v_bitop3_b32 v3, v109, v3, s11 bitop3:0x36
	v_bitop3_b32 v4, v110, v4, s11 bitop3:0x36
	v_bitop3_b32 v5, v111, v5, s11 bitop3:0x36
	v_bitop3_b32 v6, v112, v6, s11 bitop3:0x36
	v_bitop3_b32 v7, v113, v7, s11 bitop3:0x36
	v_bitop3_b32 v8, v130, v8, s11 bitop3:0x36
	v_bitop3_b32 v9, v131, v9, s11 bitop3:0x36
	v_bitop3_b32 v10, v132, v10, s11 bitop3:0x36
	v_bitop3_b32 v11, v133, v11, s11 bitop3:0x36
	v_bitop3_b32 v12, v134, v12, s11 bitop3:0x36
	v_bitop3_b32 v13, v135, v13, s11 bitop3:0x36
	v_bitop3_b32 v14, v136, v14, s11 bitop3:0x36
	v_bitop3_b32 v15, v137, v15, s11 bitop3:0x36
	v_perm_b32 v130, v0, s16, v100
	v_perm_b32 v131, v1, s16, v101
	v_perm_b32 v132, v2, s16, v102
	v_perm_b32 v133, v3, s16, v103
	v_perm_b32 v134, v4, s17, v100
	v_perm_b32 v135, v5, s17, v101
	v_perm_b32 v136, v6, s17, v102
	v_perm_b32 v137, v7, s17, v103
	v_perm_b32 v138, v8, s18, v100
	v_perm_b32 v139, v9, s18, v101
	v_perm_b32 v140, v10, s18, v102
	v_perm_b32 v141, v11, s18, v103
	v_perm_b32 v142, v12, s19, v100
	v_perm_b32 v143, v13, s19, v101
	v_perm_b32 v144, v14, s19, v102
	v_perm_b32 v145, v15, s19, v103
	v_mov_b32_e32 v146, v93
	ds_read_b128 v[0:3], v146
	ds_read_b128 v[106:109], v146 offset:32
	ds_read_b128 v[110:113], v146 offset:64
	ds_read_b128 v[186:189], v146 offset:96
	ds_read_b128 v[190:193], v146 offset:128
	ds_read_b128 v[194:197], v146 offset:160
	ds_read_b128 v[198:201], v146 offset:192
	ds_read_b128 v[202:205], v146 offset:224
	s_waitcnt lgkmcnt(7)
; #define LAS __attribute__((address_space(3)))
; template <int OFF, int TOT> DEVFN void sort16_desc(unsigned (&a)[TOT]) {
; #pragma unroll
;     for (int q = 0; q < OE16_N; ++q) { const int i = OFF + OE16[q][0], l = OFF + OE16[q][1]; const unsigned x = a[i], y = a[l]; a[i] = x > y ? x : y; a[l] = x > y ? y : x; }
; }
; __device__ __forceinline__ void phase_topk(Frame& F, const bf16_t* QP, const bf16_t* K1B, const bf16_t* K2B, unsigned short* EID, float* GATE) {
;     ...
;             for (int nb = 0; nb < 4; ++nb) { f32x16 acc = f32x16{};
;                 LAS const unsigned char* kb = F.lds + half * TK_KSET + (nb * 32 + r32) * TK_KSTRIDE + 16 * hi; asm volatile("" : "+v"(kb));
; #pragma unroll
;                 for (int kk = 0; kk < 8; ++kk) acc = __builtin_amdgcn_mfma_f32_32x32x16_bf16(*(LAS const bf16x8*)(kb + 32 * kk), qf[kk], acc, 0, 0, 0);
; #pragma unroll
;                 for (int r = 0; r < 16; ++r) {
;                     const unsigned x = __float_as_uint(acc[r]), o = x ^ ((unsigned)((int)x >> 31) | 0x80000000u); const int j = r >> 2;
;                     const unsigned pack = (unsigned)(127 - (nb * 32 + 0 + 8 * j)) | ((unsigned)(127 - (nb * 32 + 1 + 8 * j)) << 8) | ((unsigned)(127 - (nb * 32 + 2 + 8 * j)) << 16) | ((unsigned)(127 - (nb * 32 + 3 + 8 * j)) << 24);
;                     K[nb * 16 + r] = __builtin_amdgcn_perm(o, pack, 0x07060500u | (unsigned)(r & 3)); }
;                 __builtin_amdgcn_sched_barrier(0); }
	v_mfma_f32_32x32x16_bf16 v[0:15], v[0:3], v[44:47], 0
	s_waitcnt lgkmcnt(6)
	v_mfma_f32_32x32x16_bf16 v[0:15], v[106:109], v[40:43], v[0:15]
	s_waitcnt lgkmcnt(5)
	v_mfma_f32_32x32x16_bf16 v[0:15], v[110:113], v[36:39], v[0:15]
	s_waitcnt lgkmcnt(4)
	v_mfma_f32_32x32x16_bf16 v[0:15], v[186:189], v[32:35], v[0:15]
	s_waitcnt lgkmcnt(3)
	v_mfma_f32_32x32x16_bf16 v[0:15], v[190:193], v[28:31], v[0:15]
	s_waitcnt lgkmcnt(2)
	v_mfma_f32_32x32x16_bf16 v[0:15], v[194:197], v[24:27], v[0:15]
	s_waitcnt lgkmcnt(1)
	v_mfma_f32_32x32x16_bf16 v[0:15], v[198:201], v[20:23], v[0:15]
	s_waitcnt lgkmcnt(0)
	v_mfma_f32_32x32x16_bf16 v[0:15], v[202:205], v[16:19], v[0:15]
	s_nop 11
	v_ashrrev_i32_e32 v106, 31, v0
	v_ashrrev_i32_e32 v107, 31, v1
	v_ashrrev_i32_e32 v108, 31, v2
	v_ashrrev_i32_e32 v109, 31, v3
	v_ashrrev_i32_e32 v110, 31, v4
	v_ashrrev_i32_e32 v111, 31, v5
	v_ashrrev_i32_e32 v112, 31, v6
	v_ashrrev_i32_e32 v113, 31, v7
	v_ashrrev_i32_e32 v146, 31, v8
	v_ashrrev_i32_e32 v147, 31, v9
	v_ashrrev_i32_e32 v148, 31, v10
	v_ashrrev_i32_e32 v149, 31, v11
	v_ashrrev_i32_e32 v150, 31, v12
	v_ashrrev_i32_e32 v151, 31, v13
	v_ashrrev_i32_e32 v152, 31, v14
	v_ashrrev_i32_e32 v153, 31, v15
	v_bitop3_b32 v0, v106, v0, s11 bitop3:0x36
	v_bitop3_b32 v1, v107, v1, s11 bitop3:0x36
	v_bitop3_b32 v2, v108, v2, s11 bitop3:0x36
	v_bitop3_b32 v3, v109, v3, s11 bitop3:0x36
	v_bitop3_b32 v4, v110, v4, s11 bitop3:0x36
	v_bitop3_b32 v5, v111, v5, s11 bitop3:0x36
	v_bitop3_b32 v6, v112, v6, s11 bitop3:0x36
	v_bitop3_b32 v7, v113, v7, s11 bitop3:0x36
	v_bitop3_b32 v8, v146, v8, s11 bitop3:0x36
	v_bitop3_b32 v9, v147, v9, s11 bitop3:0x36
	v_bitop3_b32 v10, v148, v10, s11 bitop3:0x36
	v_bitop3_b32 v11, v149, v11, s11 bitop3:0x36
	v_bitop3_b32 v12, v150, v12, s11 bitop3:0x36
	v_bitop3_b32 v13, v151, v13, s11 bitop3:0x36
	v_bitop3_b32 v14, v152, v14, s11 bitop3:0x36
	v_bitop3_b32 v15, v153, v15, s11 bitop3:0x36
	v_perm_b32 v110, v0, s20, v100
	v_perm_b32 v111, v1, s20, v101
	v_perm_b32 v112, v2, s20, v102
	v_perm_b32 v113, v3, s20, v103
	v_perm_b32 v146, v4, s21, v100
	v_perm_b32 v147, v5, s21, v101
	v_perm_b32 v148, v6, s21, v102
	v_perm_b32 v149, v7, s21, v103
	v_perm_b32 v150, v8, s22, v100
	v_perm_b32 v151, v9, s22, v101
	v_perm_b32 v152, v10, s22, v102
	v_perm_b32 v153, v11, s22, v103
	v_perm_b32 v154, v12, s23, v100
	v_perm_b32 v155, v13, s23, v101
	v_perm_b32 v156, v14, s23, v102
	v_perm_b32 v157, v15, s23, v103
	v_mov_b32_e32 v158, v94
	ds_read_b128 v[0:3], v158
	ds_read_b128 v[106:109], v158 offset:32
	s_waitcnt lgkmcnt(1)
	v_mfma_f32_32x32x16_bf16 v[0:15], v[0:3], v[44:47], 0
	s_waitcnt lgkmcnt(0)
	v_mfma_f32_32x32x16_bf16 v[0:15], v[106:109], v[40:43], v[0:15]
	ds_read_b128 v[40:43], v158 offset:64
	ds_read_b128 v[44:47], v158 offset:96
	s_waitcnt lgkmcnt(1)
	v_mfma_f32_32x32x16_bf16 v[0:15], v[40:43], v[36:39], v[0:15]
	s_waitcnt lgkmcnt(0)
	v_mfma_f32_32x32x16_bf16 v[0:15], v[44:47], v[32:35], v[0:15]
	ds_read_b128 v[32:35], v158 offset:128
	ds_read_b128 v[36:39], v158 offset:160
	s_waitcnt lgkmcnt(1)
	v_mfma_f32_32x32x16_bf16 v[0:15], v[32:35], v[28:31], v[0:15]
	s_waitcnt lgkmcnt(0)
	v_mfma_f32_32x32x16_bf16 v[0:15], v[36:39], v[24:27], v[0:15]
	ds_read_b128 v[24:27], v158 offset:192
	ds_read_b128 v[28:31], v158 offset:224
	s_waitcnt lgkmcnt(1)
	v_mfma_f32_32x32x16_bf16 v[0:15], v[24:27], v[20:23], v[0:15]
	s_waitcnt lgkmcnt(0)
	v_mfma_f32_32x32x16_bf16 v[0:15], v[28:31], v[16:19], v[0:15]
	s_nop 11
	v_ashrrev_i32_e32 v16, 31, v0
	v_ashrrev_i32_e32 v17, 31, v1
	v_ashrrev_i32_e32 v18, 31, v2
	v_ashrrev_i32_e32 v19, 31, v3
	v_ashrrev_i32_e32 v20, 31, v4
	v_ashrrev_i32_e32 v21, 31, v5
	v_ashrrev_i32_e32 v22, 31, v6
	v_ashrrev_i32_e32 v23, 31, v7
	v_ashrrev_i32_e32 v24, 31, v8
	v_ashrrev_i32_e32 v25, 31, v9
	v_ashrrev_i32_e32 v26, 31, v10
	v_ashrrev_i32_e32 v27, 31, v11
	v_ashrrev_i32_e32 v28, 31, v12
	v_ashrrev_i32_e32 v29, 31, v13
	v_ashrrev_i32_e32 v30, 31, v14
	v_ashrrev_i32_e32 v31, 31, v15
	v_bitop3_b32 v0, v16, v0, s11 bitop3:0x36
	v_bitop3_b32 v1, v17, v1, s11 bitop3:0x36
	v_bitop3_b32 v2, v18, v2, s11 bitop3:0x36
	v_bitop3_b32 v3, v19, v3, s11 bitop3:0x36
	v_bitop3_b32 v4, v20, v4, s11 bitop3:0x36
	v_bitop3_b32 v5, v21, v5, s11 bitop3:0x36
	v_bitop3_b32 v6, v22, v6, s11 bitop3:0x36
	v_bitop3_b32 v7, v23, v7, s11 bitop3:0x36
	v_bitop3_b32 v8, v24, v8, s11 bitop3:0x36
	v_bitop3_b32 v9, v25, v9, s11 bitop3:0x36
	v_bitop3_b32 v10, v26, v10, s11 bitop3:0x36
	v_bitop3_b32 v11, v27, v11, s11 bitop3:0x36
	v_bitop3_b32 v12, v28, v12, s11 bitop3:0x36
	v_bitop3_b32 v13, v29, v13, s11 bitop3:0x36
	v_bitop3_b32 v14, v30, v14, s11 bitop3:0x36
	v_bitop3_b32 v15, v31, v15, s11 bitop3:0x36
	v_perm_b32 v0, v0, s24, v100
	v_perm_b32 v1, v1, s24, v101
	v_perm_b32 v2, v2, s24, v102
	v_perm_b32 v3, v3, s24, v103
	v_perm_b32 v4, v4, s25, v100
	v_perm_b32 v5, v5, s25, v101
	v_perm_b32 v6, v6, s25, v102
	v_perm_b32 v7, v7, s25, v103
	v_perm_b32 v8, v8, s26, v100
	v_perm_b32 v9, v9, s26, v101
	v_perm_b32 v10, v10, s26, v102
	v_perm_b32 v11, v11, s26, v103
	v_perm_b32 v12, v12, s27, v100
	v_perm_b32 v13, v13, s27, v101
	v_perm_b32 v14, v14, s27, v102
	v_perm_b32 v15, v15, s27, v103
	v_max_u32_e32 v16, v114, v115
	v_min_u32_e32 v17, v114, v115
	v_max_u32_e32 v18, v116, v117
	v_min_u32_e32 v19, v116, v117
	v_max_u32_e32 v20, v16, v18
	v_min_u32_e32 v16, v16, v18
	v_max_u32_e32 v18, v17, v19
	v_min_u32_e32 v17, v17, v19
	v_max_u32_e32 v19, v18, v16
	v_min_u32_e32 v16, v18, v16
	v_max_u32_e32 v18, v118, v119
	v_min_u32_e32 v21, v118, v119
	v_max_u32_e32 v22, v120, v121
	v_min_u32_e32 v23, v120, v121
	v_max_u32_e32 v24, v18, v22
	v_min_u32_e32 v18, v18, v22
	v_max_u32_e32 v22, v21, v23
; template <int OFF, int TOT> DEVFN void sort16_desc(unsigned (&a)[TOT]) {
; #pragma unroll
;     for (int q = 0; q < OE16_N; ++q) { const int i = OFF + OE16[q][0], l = OFF + OE16[q][1]; const unsigned x = a[i], y = a[l]; a[i] = x > y ? x : y; a[l] = x > y ? y : x; }
; }
; DEVFN void top16of64(unsigned (&a)[64]) {
;     sort16_desc<0, 64>(a); sort16_desc<16, 64>(a); sort16_desc<32, 64>(a); sort16_desc<48, 64>(a);
;     merge_top16<0, 16, 64>(a); merge_top16<32, 48, 64>(a); merge_top16<0, 32, 64>(a);
	v_min_u32_e32 v21, v21, v23
	v_max_u32_e32 v23, v22, v18
	v_min_u32_e32 v18, v22, v18
	v_max_u32_e32 v22, v20, v24
	v_min_u32_e32 v20, v20, v24
	v_max_u32_e32 v24, v16, v18
	v_min_u32_e32 v16, v16, v18
	v_max_u32_e32 v18, v24, v20
	v_min_u32_e32 v20, v24, v20
	v_max_u32_e32 v24, v19, v23
	v_min_u32_e32 v19, v19, v23
	v_max_u32_e32 v23, v17, v21
	v_min_u32_e32 v17, v17, v21
	v_max_u32_e32 v21, v23, v19
	v_min_u32_e32 v19, v23, v19
	v_max_u32_e32 v23, v24, v18
	v_min_u32_e32 v18, v24, v18
	v_max_u32_e32 v24, v21, v20
	v_min_u32_e32 v20, v21, v20
	v_max_u32_e32 v21, v19, v16
	v_min_u32_e32 v16, v19, v16
	v_max_u32_e32 v19, v122, v123
	v_min_u32_e32 v25, v122, v123
	v_max_u32_e32 v26, v124, v125
	v_min_u32_e32 v27, v124, v125
	v_max_u32_e32 v28, v19, v26
	v_min_u32_e32 v19, v19, v26
	v_max_u32_e32 v26, v25, v27
	v_min_u32_e32 v25, v25, v27
	v_max_u32_e32 v27, v26, v19
	v_min_u32_e32 v19, v26, v19
	v_max_u32_e32 v26, v126, v127
	v_min_u32_e32 v29, v126, v127
	v_max_u32_e32 v126, v110, v111
	v_min_u32_e32 v110, v110, v111
	v_max_u32_e32 v111, v112, v113
	v_min_u32_e32 v112, v112, v113
	v_max_u32_e32 v113, v126, v111
	v_min_u32_e32 v111, v126, v111
	v_max_u32_e32 v126, v110, v112
	v_max_u32_e32 v40, v130, v131
	v_min_u32_e32 v41, v130, v131
	v_max_u32_e32 v42, v132, v133
	v_min_u32_e32 v43, v132, v133
	v_min_u32_e32 v110, v110, v112
	v_max_u32_e32 v112, v126, v111
	v_min_u32_e32 v111, v126, v111
	v_max_u32_e32 v126, v146, v147
	v_min_u32_e32 v127, v146, v147
	v_max_u32_e32 v146, v0, v1
	v_min_u32_e32 v0, v0, v1
	v_max_u32_e32 v1, v2, v3
	v_min_u32_e32 v2, v2, v3
	v_max_u32_e32 v44, v40, v42
	v_min_u32_e32 v40, v40, v42
	v_max_u32_e32 v42, v41, v43
	v_max_u32_e32 v3, v146, v1
	v_min_u32_e32 v1, v146, v1
	v_max_u32_e32 v146, v0, v2
	v_max_u32_e32 v30, v128, v129
	v_min_u32_e32 v31, v128, v129
	v_min_u32_e32 v41, v41, v43
	v_max_u32_e32 v43, v42, v40
	v_min_u32_e32 v40, v42, v40
	v_max_u32_e32 v42, v134, v135
	v_min_u32_e32 v45, v134, v135
	v_max_u32_e32 v46, v136, v137
	v_min_u32_e32 v47, v136, v137
	v_max_u32_e32 v128, v148, v149
	v_min_u32_e32 v129, v148, v149
	v_min_u32_e32 v0, v0, v2
	v_max_u32_e32 v2, v146, v1
	v_min_u32_e32 v1, v146, v1
	v_max_u32_e32 v146, v4, v5
	v_min_u32_e32 v4, v4, v5
	v_max_u32_e32 v5, v6, v7
	v_min_u32_e32 v6, v6, v7
	v_max_u32_e32 v106, v42, v46
	v_min_u32_e32 v42, v42, v46
	v_max_u32_e32 v46, v45, v47
	v_max_u32_e32 v130, v126, v128
	v_min_u32_e32 v126, v126, v128
	v_max_u32_e32 v128, v127, v129
	v_max_u32_e32 v7, v146, v5
	v_min_u32_e32 v5, v146, v5
	v_max_u32_e32 v146, v4, v6
	v_min_u32_e32 v45, v45, v47
	v_max_u32_e32 v47, v46, v42
	v_min_u32_e32 v42, v46, v42
	v_min_u32_e32 v127, v127, v129
	v_max_u32_e32 v129, v128, v126
	v_min_u32_e32 v126, v128, v126
	v_min_u32_e32 v4, v4, v6
	v_max_u32_e32 v6, v146, v5
	v_min_u32_e32 v5, v146, v5
	v_max_u32_e32 v46, v44, v106
	v_min_u32_e32 v44, v44, v106
	v_max_u32_e32 v106, v40, v42
	v_max_u32_e32 v128, v113, v130
	v_min_u32_e32 v113, v113, v130
	v_max_u32_e32 v130, v111, v126
	v_max_u32_e32 v146, v3, v7
	v_min_u32_e32 v3, v3, v7
	v_max_u32_e32 v7, v1, v5
	v_min_u32_e32 v40, v40, v42
	v_max_u32_e32 v42, v106, v44
	v_min_u32_e32 v44, v106, v44
	v_max_u32_e32 v106, v43, v47
	v_min_u32_e32 v43, v43, v47
	v_max_u32_e32 v47, v41, v45
	v_min_u32_e32 v111, v111, v126
	v_max_u32_e32 v126, v130, v113
	v_min_u32_e32 v113, v130, v113
	v_max_u32_e32 v130, v112, v129
	v_min_u32_e32 v112, v112, v129
	v_max_u32_e32 v129, v110, v127
	v_min_u32_e32 v1, v1, v5
	v_max_u32_e32 v5, v7, v3
	v_min_u32_e32 v3, v7, v3
	v_max_u32_e32 v7, v2, v6
	v_min_u32_e32 v2, v2, v6
	v_max_u32_e32 v6, v0, v4
	v_min_u32_e32 v41, v41, v45
	v_max_u32_e32 v45, v47, v43
	v_min_u32_e32 v43, v47, v43
	v_min_u32_e32 v110, v110, v127
	v_max_u32_e32 v127, v129, v112
	v_min_u32_e32 v112, v129, v112
	v_min_u32_e32 v0, v0, v4
	v_max_u32_e32 v4, v6, v2
	v_min_u32_e32 v2, v6, v2
	v_max_u32_e32 v47, v106, v42
	v_min_u32_e32 v42, v106, v42
	v_max_u32_e32 v106, v45, v44
	v_min_u32_e32 v44, v45, v44
	v_max_u32_e32 v45, v43, v40
	v_min_u32_e32 v40, v43, v40
	v_max_u32_e32 v43, v138, v139
	v_min_u32_e32 v107, v138, v139
	v_max_u32_e32 v108, v140, v141
	v_min_u32_e32 v109, v140, v141
	v_max_u32_e32 v129, v130, v126
	v_min_u32_e32 v126, v130, v126
	v_max_u32_e32 v130, v127, v113
	v_min_u32_e32 v113, v127, v113
	v_max_u32_e32 v127, v112, v111
	v_min_u32_e32 v111, v112, v111
	v_max_u32_e32 v112, v150, v151
	v_min_u32_e32 v131, v150, v151
	v_max_u32_e32 v132, v152, v153
	v_min_u32_e32 v133, v152, v153
	v_max_u32_e32 v6, v7, v5
	v_min_u32_e32 v5, v7, v5
	v_max_u32_e32 v7, v4, v3
	v_min_u32_e32 v3, v4, v3
	v_max_u32_e32 v4, v2, v1
	v_min_u32_e32 v1, v2, v1
	v_max_u32_e32 v2, v8, v9
	v_min_u32_e32 v8, v8, v9
	v_max_u32_e32 v9, v10, v11
	v_min_u32_e32 v10, v10, v11
	v_max_u32_e32 v114, v43, v108
	v_min_u32_e32 v43, v43, v108
	v_max_u32_e32 v108, v107, v109
	v_max_u32_e32 v134, v112, v132
	v_min_u32_e32 v112, v112, v132
	v_max_u32_e32 v132, v131, v133
	v_max_u32_e32 v11, v2, v9
	v_min_u32_e32 v2, v2, v9
	v_max_u32_e32 v9, v8, v10
	v_min_u32_e32 v107, v107, v109
	v_max_u32_e32 v109, v108, v43
	v_min_u32_e32 v43, v108, v43
	v_max_u32_e32 v108, v142, v143
	v_min_u32_e32 v115, v142, v143
	v_max_u32_e32 v116, v144, v145
	v_min_u32_e32 v117, v144, v145
	v_min_u32_e32 v131, v131, v133
	v_max_u32_e32 v133, v132, v112
	v_min_u32_e32 v112, v132, v112
	v_max_u32_e32 v132, v154, v155
	v_min_u32_e32 v135, v154, v155
	v_max_u32_e32 v136, v156, v157
	v_min_u32_e32 v137, v156, v157
	v_min_u32_e32 v8, v8, v10
	v_max_u32_e32 v10, v9, v2
	v_min_u32_e32 v2, v9, v2
	v_max_u32_e32 v9, v12, v13
	v_min_u32_e32 v12, v12, v13
	v_max_u32_e32 v13, v14, v15
; template <int OFF, int TOT> DEVFN void sort16_desc(unsigned (&a)[TOT]) {
; #pragma unroll
;     for (int q = 0; q < OE16_N; ++q) { const int i = OFF + OE16[q][0], l = OFF + OE16[q][1]; const unsigned x = a[i], y = a[l]; a[i] = x > y ? x : y; a[l] = x > y ? y : x; }
; }
; DEVFN void top16of64(unsigned (&a)[64]) {
;     sort16_desc<0, 64>(a); sort16_desc<16, 64>(a); sort16_desc<32, 64>(a); sort16_desc<48, 64>(a);
;     merge_top16<0, 16, 64>(a); merge_top16<32, 48, 64>(a); merge_top16<0, 32, 64>(a);
	v_min_u32_e32 v14, v14, v15
	v_max_u32_e32 v32, v26, v30
	v_min_u32_e32 v26, v26, v30
	v_max_u32_e32 v30, v29, v31
	v_max_u32_e32 v118, v108, v116
	v_min_u32_e32 v108, v108, v116
	v_max_u32_e32 v116, v115, v117
	v_max_u32_e32 v138, v132, v136
	v_min_u32_e32 v132, v132, v136
	v_max_u32_e32 v136, v135, v137
	v_max_u32_e32 v15, v9, v13
	v_min_u32_e32 v9, v9, v13
	v_max_u32_e32 v13, v12, v14
	v_min_u32_e32 v29, v29, v31
	v_max_u32_e32 v31, v30, v26
	v_min_u32_e32 v26, v30, v26
	v_min_u32_e32 v115, v115, v117
	v_max_u32_e32 v117, v116, v108
	v_min_u32_e32 v108, v116, v108
	v_min_u32_e32 v135, v135, v137
	v_max_u32_e32 v137, v136, v132
	v_min_u32_e32 v132, v136, v132
	v_min_u32_e32 v12, v12, v14
	v_max_u32_e32 v14, v13, v9
	v_min_u32_e32 v9, v13, v9
	v_max_u32_e32 v30, v28, v32
	v_min_u32_e32 v28, v28, v32
	v_max_u32_e32 v32, v19, v26
	v_max_u32_e32 v116, v114, v118
	v_min_u32_e32 v114, v114, v118
	v_max_u32_e32 v118, v43, v108
	v_max_u32_e32 v136, v134, v138
	v_min_u32_e32 v134, v134, v138
	v_max_u32_e32 v138, v112, v132
	v_max_u32_e32 v13, v11, v15
	v_min_u32_e32 v11, v11, v15
	v_max_u32_e32 v15, v2, v9
	v_min_u32_e32 v19, v19, v26
	v_max_u32_e32 v26, v32, v28
	v_min_u32_e32 v28, v32, v28
	v_max_u32_e32 v32, v27, v31
	v_min_u32_e32 v27, v27, v31
	v_max_u32_e32 v31, v25, v29
	v_min_u32_e32 v43, v43, v108
	v_max_u32_e32 v108, v118, v114
	v_min_u32_e32 v114, v118, v114
	v_max_u32_e32 v118, v109, v117
	v_min_u32_e32 v109, v109, v117
	v_max_u32_e32 v117, v107, v115
	v_min_u32_e32 v112, v112, v132
	v_max_u32_e32 v132, v138, v134
	v_min_u32_e32 v134, v138, v134
	v_max_u32_e32 v138, v133, v137
	v_min_u32_e32 v133, v133, v137
	v_max_u32_e32 v137, v131, v135
	v_min_u32_e32 v2, v2, v9
	v_max_u32_e32 v9, v15, v11
	v_min_u32_e32 v11, v15, v11
	v_max_u32_e32 v15, v10, v14
	v_min_u32_e32 v10, v10, v14
	v_max_u32_e32 v14, v8, v12
	v_min_u32_e32 v25, v25, v29
	v_max_u32_e32 v29, v31, v27
	v_min_u32_e32 v107, v107, v115
	v_max_u32_e32 v115, v117, v109
	v_min_u32_e32 v131, v131, v135
	v_max_u32_e32 v135, v137, v133
	v_min_u32_e32 v8, v8, v12
	v_max_u32_e32 v12, v14, v10
	v_min_u32_e32 v27, v31, v27
	v_max_u32_e32 v31, v32, v26
	v_min_u32_e32 v26, v32, v26
	v_max_u32_e32 v32, v29, v28
	v_min_u32_e32 v28, v29, v28
	v_min_u32_e32 v109, v117, v109
	v_max_u32_e32 v117, v118, v108
	v_min_u32_e32 v108, v118, v108
	v_max_u32_e32 v118, v115, v114
	v_min_u32_e32 v114, v115, v114
	v_min_u32_e32 v133, v137, v133
	v_max_u32_e32 v137, v138, v132
	v_min_u32_e32 v132, v138, v132
	v_max_u32_e32 v138, v135, v134
	v_min_u32_e32 v134, v135, v134
	v_min_u32_e32 v10, v14, v10
	v_max_u32_e32 v14, v15, v9
	v_min_u32_e32 v9, v15, v9
	v_max_u32_e32 v15, v12, v11
	v_min_u32_e32 v11, v12, v11
	v_max_u32_e32 v29, v27, v19
	v_min_u32_e32 v19, v27, v19
	v_min_u32_e32 v27, v22, v30
	v_max_u32_e32 v33, v20, v28
	v_max_u32_e32 v115, v109, v43
	v_min_u32_e32 v43, v109, v43
	v_min_u32_e32 v109, v46, v116
	v_max_u32_e32 v119, v44, v114
	v_max_u32_e32 v135, v133, v112
	v_min_u32_e32 v112, v133, v112
	v_min_u32_e32 v133, v128, v136
	v_max_u32_e32 v139, v113, v134
	v_max_u32_e32 v12, v10, v2
	v_min_u32_e32 v2, v10, v2
	v_min_u32_e32 v10, v146, v13
	v_max_u32_e32 v147, v3, v11
	v_min_u32_e32 v20, v20, v28
	v_max_u32_e32 v28, v33, v27
	v_min_u32_e32 v27, v33, v27
	v_max_u32_e32 v33, v18, v26
	v_min_u32_e32 v18, v18, v26
	v_max_u32_e32 v26, v16, v19
	v_min_u32_e32 v44, v44, v114
	v_max_u32_e32 v114, v119, v109
	v_min_u32_e32 v109, v119, v109
	v_max_u32_e32 v119, v42, v108
	v_min_u32_e32 v42, v42, v108
	v_max_u32_e32 v108, v40, v43
	v_min_u32_e32 v113, v113, v134
	v_max_u32_e32 v134, v139, v133
	v_min_u32_e32 v133, v139, v133
	v_max_u32_e32 v139, v126, v132
	v_min_u32_e32 v126, v126, v132
	v_max_u32_e32 v132, v111, v112
	v_min_u32_e32 v3, v3, v11
	v_max_u32_e32 v11, v147, v10
	v_min_u32_e32 v10, v147, v10
	v_max_u32_e32 v147, v5, v9
	v_min_u32_e32 v5, v5, v9
	v_max_u32_e32 v9, v1, v2
	v_min_u32_e32 v16, v16, v19
	v_max_u32_e32 v19, v26, v18
	v_min_u32_e32 v18, v26, v18
	v_min_u32_e32 v40, v40, v43
	v_max_u32_e32 v43, v108, v42
	v_min_u32_e32 v42, v108, v42
	v_min_u32_e32 v111, v111, v112
	v_max_u32_e32 v112, v132, v126
	v_min_u32_e32 v126, v132, v126
	v_min_u32_e32 v1, v1, v2
	v_max_u32_e32 v2, v9, v5
	v_min_u32_e32 v5, v9, v5
	v_max_u32_e32 v26, v33, v28
	v_min_u32_e32 v28, v33, v28
	v_max_u32_e32 v33, v19, v27
	v_min_u32_e32 v19, v19, v27
	v_max_u32_e32 v27, v18, v20
	v_min_u32_e32 v18, v18, v20
	v_max_u32_e32 v20, v23, v31
	v_min_u32_e32 v23, v23, v31
	v_max_u32_e32 v31, v21, v29
	v_max_u32_e32 v108, v119, v114
	v_min_u32_e32 v114, v119, v114
	v_max_u32_e32 v119, v43, v109
	v_min_u32_e32 v43, v43, v109
	v_max_u32_e32 v109, v42, v44
	v_min_u32_e32 v42, v42, v44
	v_max_u32_e32 v44, v47, v117
	v_min_u32_e32 v47, v47, v117
	v_max_u32_e32 v117, v45, v115
	v_max_u32_e32 v132, v139, v134
	v_min_u32_e32 v134, v139, v134
	v_max_u32_e32 v139, v112, v133
	v_min_u32_e32 v112, v112, v133
	v_max_u32_e32 v133, v126, v113
	v_min_u32_e32 v113, v126, v113
	v_max_u32_e32 v126, v129, v137
	v_min_u32_e32 v129, v129, v137
	v_max_u32_e32 v137, v127, v135
	v_max_u32_e32 v9, v147, v11
	v_min_u32_e32 v11, v147, v11
	v_max_u32_e32 v147, v2, v10
	v_min_u32_e32 v2, v2, v10
	v_max_u32_e32 v10, v5, v3
	v_min_u32_e32 v3, v5, v3
	v_max_u32_e32 v5, v6, v14
	v_min_u32_e32 v6, v6, v14
	v_max_u32_e32 v14, v4, v12
	v_min_u32_e32 v21, v21, v29
	v_max_u32_e32 v29, v31, v23
	v_min_u32_e32 v23, v31, v23
	v_max_u32_e32 v31, v24, v32
	v_min_u32_e32 v24, v24, v32
	v_max_u32_e32 v32, v17, v25
	v_min_u32_e32 v45, v45, v115
	v_max_u32_e32 v115, v117, v47
	v_min_u32_e32 v47, v117, v47
	v_max_u32_e32 v117, v106, v118
	v_min_u32_e32 v106, v106, v118
; template <int A, int B, int TOT> DEVFN void merge_top16(unsigned (&a)[TOT]) {
; #pragma unroll
;     for (int i = 0; i < 16; ++i) { const unsigned x = a[A + i], y = a[B + 15 - i]; a[A + i] = x > y ? x : y; }
;     bitonic_merge16_desc<A, TOT>(a);
; }
; DEVFN void top16of64(unsigned (&a)[64]) {
;     sort16_desc<0, 64>(a); sort16_desc<16, 64>(a); sort16_desc<32, 64>(a); sort16_desc<48, 64>(a);
;     merge_top16<0, 16, 64>(a); merge_top16<32, 48, 64>(a); merge_top16<0, 32, 64>(a);
	v_max_u32_e32 v118, v41, v107
	v_min_u32_e32 v127, v127, v135
	v_max_u32_e32 v135, v137, v129
	v_min_u32_e32 v129, v137, v129
	v_max_u32_e32 v137, v130, v138
	v_min_u32_e32 v130, v130, v138
	v_max_u32_e32 v138, v110, v131
	v_min_u32_e32 v4, v4, v12
	v_max_u32_e32 v12, v14, v6
	v_min_u32_e32 v6, v14, v6
	v_max_u32_e32 v14, v7, v15
	v_min_u32_e32 v7, v7, v15
	v_max_u32_e32 v15, v0, v8
	v_min_u32_e32 v17, v17, v25
	v_max_u32_e32 v25, v32, v24
	v_min_u32_e32 v24, v32, v24
	v_min_u32_e32 v41, v41, v107
	v_max_u32_e32 v107, v118, v106
	v_min_u32_e32 v106, v118, v106
	v_min_u32_e32 v110, v110, v131
	v_max_u32_e32 v131, v138, v130
	v_min_u32_e32 v130, v138, v130
	v_min_u32_e32 v0, v0, v8
	v_max_u32_e32 v8, v15, v7
	v_min_u32_e32 v7, v15, v7
	v_max_u32_e32 v32, v31, v29
	v_min_u32_e32 v29, v31, v29
	v_max_u32_e32 v31, v25, v23
	v_min_u32_e32 v23, v25, v23
	v_max_u32_e32 v25, v24, v21
	v_min_u32_e32 v21, v24, v21
	v_max_u32_e32 v118, v117, v115
	v_min_u32_e32 v115, v117, v115
	v_max_u32_e32 v117, v107, v47
	v_min_u32_e32 v47, v107, v47
	v_max_u32_e32 v107, v106, v45
	v_min_u32_e32 v45, v106, v45
	v_max_u32_e32 v138, v137, v135
	v_min_u32_e32 v135, v137, v135
	v_max_u32_e32 v137, v131, v129
	v_min_u32_e32 v129, v131, v129
	v_max_u32_e32 v131, v130, v127
	v_min_u32_e32 v127, v130, v127
	v_max_u32_e32 v15, v14, v12
	v_min_u32_e32 v12, v14, v12
	v_max_u32_e32 v14, v8, v6
	v_min_u32_e32 v6, v8, v6
	v_max_u32_e32 v8, v7, v4
	v_min_u32_e32 v4, v7, v4
	v_min_u32_e32 v24, v20, v26
	v_min_u32_e32 v34, v32, v28
	v_min_u32_e32 v35, v29, v33
	v_min_u32_e32 v36, v31, v19
	v_min_u32_e32 v37, v23, v27
	v_min_u32_e32 v38, v25, v18
	v_min_u32_e32 v39, v21, v16
	v_min_u32_e32 v106, v44, v108
	v_min_u32_e32 v120, v118, v114
	v_min_u32_e32 v121, v115, v119
	v_min_u32_e32 v122, v117, v43
	v_min_u32_e32 v123, v47, v109
	v_min_u32_e32 v124, v107, v42
	v_min_u32_e32 v125, v45, v40
	v_min_u32_e32 v130, v126, v132
	v_min_u32_e32 v140, v138, v134
	v_min_u32_e32 v141, v135, v139
	v_min_u32_e32 v142, v137, v112
	v_min_u32_e32 v143, v129, v133
	v_min_u32_e32 v144, v131, v113
	v_min_u32_e32 v145, v127, v111
	v_min_u32_e32 v7, v5, v9
	v_min_u32_e32 v148, v15, v11
	v_min_u32_e32 v149, v12, v147
	v_min_u32_e32 v150, v14, v2
	v_min_u32_e32 v151, v6, v10
	v_min_u32_e32 v152, v8, v3
	v_min_u32_e32 v153, v4, v1
	v_max3_u32 v22, v22, v30, v41
	v_max3_u32 v20, v20, v26, v125
	v_max3_u32 v24, v24, v45, v40
	v_max3_u32 v26, v32, v28, v124
	v_max3_u32 v28, v34, v107, v42
	v_max3_u32 v29, v29, v33, v123
	v_max3_u32 v30, v35, v47, v109
	v_max3_u32 v19, v31, v19, v122
	v_max3_u32 v31, v36, v117, v43
	v_max3_u32 v23, v23, v27, v121
	v_max3_u32 v27, v37, v115, v119
	v_max3_u32 v18, v25, v18, v120
	v_max3_u32 v25, v38, v118, v114
	v_max3_u32 v16, v21, v16, v106
	v_max3_u32 v21, v39, v44, v108
	v_max3_u32 v17, v17, v46, v116
	v_max3_u32 v0, v128, v136, v0
	v_max3_u32 v40, v126, v132, v153
	v_max3_u32 v1, v130, v4, v1
	v_max3_u32 v4, v138, v134, v152
	v_max3_u32 v3, v140, v8, v3
	v_max3_u32 v8, v135, v139, v151
	v_max3_u32 v6, v141, v6, v10
	v_max3_u32 v10, v137, v112, v150
	v_max3_u32 v2, v142, v14, v2
	v_max3_u32 v14, v129, v133, v149
	v_max3_u32 v12, v143, v12, v147
	v_max3_u32 v41, v131, v113, v148
	v_max3_u32 v11, v144, v15, v11
	v_max3_u32 v7, v127, v111, v7
	v_max3_u32 v5, v145, v5, v9
	v_max3_u32 v9, v110, v146, v13
	v_max_u32_e32 v32, v22, v31
	v_min_u32_e32 v22, v22, v31
	v_max_u32_e32 v31, v20, v23
	v_min_u32_e32 v20, v20, v23
	v_max_u32_e32 v23, v24, v27
	v_min_u32_e32 v24, v24, v27
	v_max_u32_e32 v27, v26, v18
	v_min_u32_e32 v18, v26, v18
	v_max_u32_e32 v26, v28, v25
	v_min_u32_e32 v25, v28, v25
	v_max_u32_e32 v28, v29, v16
	v_min_u32_e32 v16, v29, v16
	v_max_u32_e32 v29, v30, v21
	v_min_u32_e32 v21, v30, v21
	v_max_u32_e32 v30, v19, v17
	v_min_u32_e32 v17, v19, v17
	v_max_u32_e32 v13, v0, v2
	v_min_u32_e32 v0, v0, v2
	v_max_u32_e32 v2, v40, v14
	v_min_u32_e32 v14, v40, v14
	v_max_u32_e32 v15, v1, v12
	v_min_u32_e32 v1, v1, v12
	v_max_u32_e32 v12, v4, v41
	v_min_u32_e32 v4, v4, v41
	v_max_u32_e32 v40, v3, v11
	v_min_u32_e32 v3, v3, v11
	v_max_u32_e32 v11, v8, v7
	v_min_u32_e32 v7, v8, v7
	v_max_u32_e32 v8, v6, v5
	v_min_u32_e32 v5, v6, v5
	v_max_u32_e32 v6, v10, v9
	v_min_u32_e32 v9, v10, v9
	v_max_u32_e32 v19, v32, v26
	v_min_u32_e32 v26, v32, v26
	v_max_u32_e32 v32, v31, v28
	v_min_u32_e32 v28, v31, v28
	v_max_u32_e32 v31, v23, v29
	v_min_u32_e32 v23, v23, v29
	v_max_u32_e32 v29, v27, v30
	v_min_u32_e32 v27, v27, v30
	v_max_u32_e32 v30, v22, v25
	v_min_u32_e32 v22, v22, v25
	v_max_u32_e32 v25, v20, v16
	v_min_u32_e32 v16, v20, v16
	v_max_u32_e32 v20, v24, v21
	v_min_u32_e32 v21, v24, v21
	v_max_u32_e32 v24, v18, v17
	v_min_u32_e32 v17, v18, v17
	v_max_u32_e32 v10, v13, v40
	v_min_u32_e32 v13, v13, v40
	v_max_u32_e32 v40, v2, v11
	v_min_u32_e32 v2, v2, v11
	v_max_u32_e32 v11, v15, v8
	v_min_u32_e32 v8, v15, v8
	v_max_u32_e32 v15, v12, v6
	v_min_u32_e32 v6, v12, v6
	v_max_u32_e32 v12, v0, v3
	v_min_u32_e32 v0, v0, v3
	v_max_u32_e32 v3, v14, v7
	v_min_u32_e32 v7, v14, v7
	v_max_u32_e32 v14, v1, v5
	v_min_u32_e32 v1, v1, v5
	v_max_u32_e32 v5, v4, v9
	v_min_u32_e32 v4, v4, v9
	v_max_u32_e32 v18, v19, v31
	v_min_u32_e32 v19, v19, v31
	v_max_u32_e32 v31, v32, v29
	v_min_u32_e32 v29, v32, v29
	v_max_u32_e32 v32, v26, v23
	v_min_u32_e32 v23, v26, v23
	v_max_u32_e32 v26, v28, v27
	v_min_u32_e32 v27, v28, v27
	v_max_u32_e32 v28, v30, v20
	v_min_u32_e32 v20, v30, v20
	v_max_u32_e32 v30, v25, v24
	v_min_u32_e32 v24, v25, v24
	v_max_u32_e32 v25, v22, v21
	v_min_u32_e32 v21, v22, v21
	v_max_u32_e32 v22, v16, v17
	v_min_u32_e32 v16, v16, v17
	v_max_u32_e32 v9, v10, v11
	v_min_u32_e32 v10, v10, v11
; template <int OFF, int TOT> DEVFN void bitonic_merge16_desc(unsigned (&a)[TOT]) {
; #pragma unroll
;     for (int j = 8; j > 0; j >>= 1)
; #pragma unroll
;         for (int i = 0; i < 16; ++i) { const int l = i ^ j; if (l > i) { const unsigned x = a[OFF + i], y = a[OFF + l]; a[OFF + i] = x > y ? x : y; a[OFF + l] = x > y ? y : x; } }
; }
; template <int A, int B, int TOT> DEVFN void merge_top16(unsigned (&a)[TOT]) {
; #pragma unroll
;     for (int i = 0; i < 16; ++i) { const unsigned x = a[A + i], y = a[B + 15 - i]; a[A + i] = x > y ? x : y; }
;     bitonic_merge16_desc<A, TOT>(a);
; }
; DEVFN void top16of64(unsigned (&a)[64]) {
;     sort16_desc<0, 64>(a); sort16_desc<16, 64>(a); sort16_desc<32, 64>(a); sort16_desc<48, 64>(a);
;     merge_top16<0, 16, 64>(a); merge_top16<32, 48, 64>(a); merge_top16<0, 32, 64>(a);
; __device__ __forceinline__ void phase_topk(Frame& F, const bf16_t* QP, const bf16_t* K1B, const bf16_t* K2B, unsigned short* EID, float* GATE) {
;     ...
;             for (int i = 0; i < 16; ++i) K[i] ^= h4;
;             unsigned C[16];
; #pragma unroll
;             for (int i = 0; i < 16; ++i) { const unsigned y = (unsigned)__shfl_xor((int)K[15 - i], 32); C[i] = K[i] > y ? K[i] : y; }
;             bitonic_merge16_desc<0, 16>(C);
	v_max_u32_e32 v11, v40, v15
	v_min_u32_e32 v15, v40, v15
	v_max_u32_e32 v40, v13, v8
	v_min_u32_e32 v8, v13, v8
	v_max_u32_e32 v13, v2, v6
	v_min_u32_e32 v2, v2, v6
	v_max_u32_e32 v6, v12, v14
	v_min_u32_e32 v12, v12, v14
	v_max_u32_e32 v14, v3, v5
	v_min_u32_e32 v3, v3, v5
	v_max_u32_e32 v5, v0, v1
	v_min_u32_e32 v0, v0, v1
	v_max_u32_e32 v1, v7, v4
	v_min_u32_e32 v4, v7, v4
	v_min_u32_e32 v17, v18, v31
	v_min_u32_e32 v33, v19, v29
	v_min_u32_e32 v34, v32, v26
	v_min_u32_e32 v35, v23, v27
	v_min_u32_e32 v36, v28, v30
	v_min_u32_e32 v37, v20, v24
	v_min_u32_e32 v38, v25, v22
	v_min_u32_e32 v39, v21, v16
	v_min_u32_e32 v7, v9, v11
	v_min_u32_e32 v41, v10, v15
	v_min_u32_e32 v42, v40, v13
	v_min_u32_e32 v43, v8, v2
	v_min_u32_e32 v44, v6, v14
	v_min_u32_e32 v45, v12, v3
	v_min_u32_e32 v46, v5, v1
	v_min_u32_e32 v47, v0, v4
	v_max3_u32 v18, v18, v31, v47
	v_max3_u32 v0, v17, v0, v4
	v_max3_u32 v4, v19, v29, v46
	v_max3_u32 v1, v33, v5, v1
	v_max3_u32 v5, v32, v26, v45
	v_max3_u32 v3, v34, v12, v3
	v_max3_u32 v12, v23, v27, v44
	v_max3_u32 v6, v35, v6, v14
	v_max3_u32 v14, v28, v30, v43
	v_max3_u32 v2, v36, v8, v2
	v_max3_u32 v8, v20, v24, v42
	v_max3_u32 v13, v37, v40, v13
	v_max3_u32 v17, v25, v22, v41
	v_max3_u32 v10, v38, v10, v15
	v_max3_u32 v7, v21, v16, v7
	v_max3_u32 v9, v39, v9, v11
	v_max_u32_e32 v11, v18, v14
	v_max_u32_e32 v15, v0, v2
	v_min_u32_e32 v0, v0, v2
	v_max_u32_e32 v2, v4, v8
	v_min_u32_e32 v4, v4, v8
	v_max_u32_e32 v8, v1, v13
	v_min_u32_e32 v1, v1, v13
	v_max_u32_e32 v13, v5, v17
	v_max_u32_e32 v16, v3, v10
	v_min_u32_e32 v3, v3, v10
	v_max_u32_e32 v10, v12, v7
	v_min_u32_e32 v7, v12, v7
	v_max_u32_e32 v12, v6, v9
	v_min_u32_e32 v14, v18, v14
	v_min_u32_e32 v5, v5, v17
	v_min_u32_e32 v6, v6, v9
	v_max_u32_e32 v9, v11, v13
	v_min_u32_e32 v11, v11, v13
	v_max_u32_e32 v13, v15, v16
	v_min_u32_e32 v15, v15, v16
	v_max_u32_e32 v16, v2, v10
	v_min_u32_e32 v2, v2, v10
	v_max_u32_e32 v10, v8, v12
	v_min_u32_e32 v8, v8, v12
	v_max_u32_e32 v12, v14, v5
	v_min_u32_e32 v5, v14, v5
	v_max_u32_e32 v14, v0, v3
	v_min_u32_e32 v0, v0, v3
	v_max_u32_e32 v3, v4, v7
	v_min_u32_e32 v4, v4, v7
	v_max_u32_e32 v7, v1, v6
	v_min_u32_e32 v1, v1, v6
	v_max_u32_e32 v6, v9, v16
	v_min_u32_e32 v9, v9, v16
	v_max_u32_e32 v16, v13, v10
	v_min_u32_e32 v10, v13, v10
	v_max_u32_e32 v13, v11, v2
	v_min_u32_e32 v2, v11, v2
	v_max_u32_e32 v11, v15, v8
	v_min_u32_e32 v8, v15, v8
	v_max_u32_e32 v15, v12, v3
	v_min_u32_e32 v3, v12, v3
	v_max_u32_e32 v12, v14, v7
	v_min_u32_e32 v7, v14, v7
	v_max_u32_e32 v14, v5, v4
	v_min_u32_e32 v4, v5, v4
	v_max_u32_e32 v5, v0, v1
	v_min_u32_e32 v0, v0, v1
	v_max_u32_e32 v1, v6, v16
	v_min_u32_e32 v6, v6, v16
	v_max_u32_e32 v16, v9, v10
	v_min_u32_e32 v9, v9, v10
	v_max_u32_e32 v10, v13, v11
	v_min_u32_e32 v11, v13, v11
	v_max_u32_e32 v13, v2, v8
	v_min_u32_e32 v2, v2, v8
	v_max_u32_e32 v8, v15, v12
	v_min_u32_e32 v12, v15, v12
	v_max_u32_e32 v15, v3, v7
	v_min_u32_e32 v3, v3, v7
	v_max_u32_e32 v7, v14, v5
	v_min_u32_e32 v5, v14, v5
	v_max_u32_e32 v14, v4, v0
	v_min_u32_e32 v0, v4, v0
	v_and_b32_e32 v17, 64, v99
	v_xor_b32_e32 v4, v6, v105
	v_xor_b32_e32 v6, v16, v105
	v_xor_b32_e32 v16, 32, v99
	v_add_u32_e32 v17, 64, v17
	v_cmp_lt_i32_e32 vcc, v16, v17
	v_xor_b32_e32 v15, v15, v105
	v_xor_b32_e32 v0, v0, v105
	v_cndmask_b32_e32 v16, v99, v16, vcc
	v_lshlrev_b32_e32 v119, 2, v16
	v_xor_b32_e32 v3, v3, v105
	v_xor_b32_e32 v7, v7, v105
	v_xor_b32_e32 v5, v5, v105
	v_xor_b32_e32 v14, v14, v105
	ds_bpermute_b32 v16, v119, v0
	ds_bpermute_b32 v17, v119, v14
	ds_bpermute_b32 v18, v119, v5
	ds_bpermute_b32 v19, v119, v7
	ds_bpermute_b32 v20, v119, v3
	ds_bpermute_b32 v21, v119, v15
	v_xor_b32_e32 v1, v1, v105
	v_xor_b32_e32 v9, v9, v105
	v_xor_b32_e32 v10, v10, v105
	v_xor_b32_e32 v11, v11, v105
	v_xor_b32_e32 v13, v13, v105
	v_xor_b32_e32 v2, v2, v105
	v_xor_b32_e32 v8, v8, v105
	v_xor_b32_e32 v12, v12, v105
	s_waitcnt lgkmcnt(5)
	v_max_u32_e32 v16, v1, v16
	s_waitcnt lgkmcnt(4)
	v_max_u32_e32 v17, v4, v17
	s_waitcnt lgkmcnt(3)
	v_max_u32_e32 v18, v6, v18
	s_waitcnt lgkmcnt(2)
	v_max_u32_e32 v19, v9, v19
	s_waitcnt lgkmcnt(1)
	v_max_u32_e32 v20, v10, v20
	s_waitcnt lgkmcnt(0)
	v_max_u32_e32 v21, v11, v21
	ds_bpermute_b32 v22, v119, v12
	ds_bpermute_b32 v23, v119, v8
	ds_bpermute_b32 v24, v119, v2
	ds_bpermute_b32 v25, v119, v13
	ds_bpermute_b32 v11, v119, v11
	ds_bpermute_b32 v10, v119, v10
	ds_bpermute_b32 v9, v119, v9
	ds_bpermute_b32 v6, v119, v6
	ds_bpermute_b32 v4, v119, v4
	ds_bpermute_b32 v1, v119, v1
	s_waitcnt lgkmcnt(9)
	v_max_u32_e32 v13, v13, v22
	s_waitcnt lgkmcnt(8)
	v_max_u32_e32 v2, v2, v23
	s_waitcnt lgkmcnt(7)
	v_max_u32_e32 v8, v8, v24
	s_waitcnt lgkmcnt(6)
	v_max_u32_e32 v12, v12, v25
	s_waitcnt lgkmcnt(5)
	v_max_u32_e32 v11, v15, v11
	s_waitcnt lgkmcnt(4)
	v_max_u32_e32 v3, v3, v10
	s_waitcnt lgkmcnt(3)
	v_max_u32_e32 v7, v7, v9
	s_waitcnt lgkmcnt(2)
	v_max_u32_e32 v5, v5, v6
	s_waitcnt lgkmcnt(1)
	v_max_u32_e32 v4, v14, v4
	s_waitcnt lgkmcnt(0)
; #define LAS __attribute__((address_space(3)))
; __device__ __forceinline__ void phase_topk(Frame& F, const bf16_t* QP, const bf16_t* K1B, const bf16_t* K2B, unsigned short* EID, float* GATE) {
;     ...
;             { const int tnx = tile + nbh * NWAVES, tl = half ? (tnx < TOK / 32 ? tnx : tile) : tile;
;               const bf16_t* qrow = QP + (size_t)(tl * 32 + r32) * 2048 + h * 256 + (half ? 0 : 128) + 8 * hi;
; #pragma unroll
;               for (int kk = 0; kk < 8; ++kk) qn[kk] = *(const bf16x8*)(qrow + 16 * kk); }
;             unsigned K[64];
; #pragma unroll
;             for (int nb = 0; nb < 4; ++nb) { f32x16 acc = f32x16{};
;                 LAS const unsigned char* kb = F.lds + half * TK_KSET + (nb * 32 + r32) * TK_KSTRIDE + 16 * hi; asm volatile("" : "+v"(kb));
; #pragma unroll
;                 for (int kk = 0; kk < 8; ++kk) acc = __builtin_amdgcn_mfma_f32_32x32x16_bf16(*(LAS const bf16x8*)(kb + 32 * kk), qf[kk], acc, 0, 0, 0);
; #pragma unroll
;                 for (int r = 0; r < 16; ++r) {
;                     const unsigned x = __float_as_uint(acc[r]), o = x ^ ((unsigned)((int)x >> 31) | 0x80000000u); const int j = r >> 2;
;                     const unsigned pack = (unsigned)(127 - (nb * 32 + 0 + 8 * j)) | ((unsigned)(127 - (nb * 32 + 1 + 8 * j)) << 8) | ((unsigned)(127 - (nb * 32 + 2 + 8 * j)) << 16) | ((unsigned)(127 - (nb * 32 + 3 + 8 * j)) << 24);
;                     K[nb * 16 + r] = __builtin_amdgcn_perm(o, pack, 0x07060500u | (unsigned)(r & 3)); }
;                 __builtin_amdgcn_sched_barrier(0); }
;     ...
;             for (int i = 0; i < 16; ++i) { const unsigned y = (unsigned)__shfl_xor((int)K[15 - i], 32); C[i] = K[i] > y ? K[i] : y; }
;             bitonic_merge16_desc<0, 16>(C);
; #pragma unroll
;             for (int i = 0; i < 16; ++i) { if (half == 0) V1[i] = C[i]; else V2[i] = C[i]; }
	v_max_u32_e32 v0, v0, v1
	v_max_u32_e32 v1, v16, v8
	v_min_u32_e32 v6, v16, v8
	v_max_u32_e32 v8, v17, v12
	v_min_u32_e32 v9, v17, v12
	v_max_u32_e32 v10, v18, v11
	v_min_u32_e32 v11, v18, v11
	v_max_u32_e32 v12, v19, v3
	v_min_u32_e32 v3, v19, v3
	v_max_u32_e32 v14, v20, v7
	v_min_u32_e32 v7, v20, v7
	v_max_u32_e32 v15, v21, v5
	v_min_u32_e32 v5, v21, v5
	v_max_u32_e32 v16, v13, v4
	v_min_u32_e32 v4, v13, v4
	v_max_u32_e32 v13, v2, v0
	v_min_u32_e32 v0, v2, v0
	v_max_u32_e32 v2, v1, v14
	v_min_u32_e32 v1, v1, v14
	v_max_u32_e32 v14, v8, v15
	v_min_u32_e32 v8, v8, v15
	v_max_u32_e32 v15, v10, v16
	v_min_u32_e32 v10, v10, v16
	v_max_u32_e32 v16, v12, v13
	v_min_u32_e32 v12, v12, v13
	v_max_u32_e32 v13, v6, v7
	v_min_u32_e32 v6, v6, v7
	v_max_u32_e32 v7, v9, v5
	v_min_u32_e32 v5, v9, v5
	v_max_u32_e32 v9, v11, v4
	v_min_u32_e32 v4, v11, v4
	v_max_u32_e32 v11, v3, v0
	v_min_u32_e32 v0, v3, v0
	v_max_u32_e32 v3, v2, v15
	v_min_u32_e32 v2, v2, v15
	v_max_u32_e32 v15, v14, v16
	v_min_u32_e32 v14, v14, v16
	v_max_u32_e32 v16, v1, v10
	v_min_u32_e32 v1, v1, v10
	v_max_u32_e32 v10, v8, v12
	v_min_u32_e32 v8, v8, v12
	v_max_u32_e32 v12, v13, v9
	v_min_u32_e32 v9, v13, v9
	v_max_u32_e32 v13, v7, v11
	v_min_u32_e32 v7, v7, v11
	v_max_u32_e32 v11, v6, v4
	v_min_u32_e32 v4, v6, v4
	v_max_u32_e32 v6, v5, v0
	v_min_u32_e32 v0, v5, v0
	v_max_u32_e32 v122, v3, v15
	v_min_u32_e32 v121, v3, v15
	v_max_u32_e32 v120, v2, v14
	v_min_u32_e32 v118, v2, v14
	v_max_u32_e32 v117, v16, v10
	v_min_u32_e32 v116, v16, v10
	v_max_u32_e32 v115, v1, v8
	v_min_u32_e32 v114, v1, v8
	v_max_u32_e32 v113, v12, v13
	v_min_u32_e32 v112, v12, v13
	v_max_u32_e32 v111, v9, v7
	v_min_u32_e32 v110, v9, v7
	v_max_u32_e32 v109, v11, v6
	v_min_u32_e32 v108, v11, v6
	v_max_u32_e32 v107, v4, v0
	v_min_u32_e32 v106, v4, v0
	v_lshl_or_b32 v0, s33, 5, v88
	v_ashrrev_i32_e32 v1, 31, v0
	v_lshlrev_b64 v[0:1], 12, v[0:1]
	v_lshl_add_u64 v[0:1], v[86:87], 0, v[0:1]
	global_load_dwordx4 v[44:47], v[0:1], off
	global_load_dwordx4 v[40:43], v[0:1], off offset:32
	global_load_dwordx4 v[36:39], v[0:1], off offset:64
	global_load_dwordx4 v[32:35], v[0:1], off offset:96
	global_load_dwordx4 v[28:31], v[0:1], off offset:128
	global_load_dwordx4 v[24:27], v[0:1], off offset:160
	global_load_dwordx4 v[20:23], v[0:1], off offset:192
	global_load_dwordx4 v[16:19], v[0:1], off offset:224
	v_mov_b32_e32 v123, v95
	ds_read_b128 v[0:3], v123
	ds_read_b128 v[124:127], v123 offset:32
	ds_read_b128 v[128:131], v123 offset:64
	ds_read_b128 v[186:189], v123 offset:96
	ds_read_b128 v[190:193], v123 offset:128
	ds_read_b128 v[194:197], v123 offset:160
	ds_read_b128 v[198:201], v123 offset:192
	ds_read_b128 v[202:205], v123 offset:224
	s_waitcnt vmcnt(15) lgkmcnt(7)
	v_mfma_f32_32x32x16_bf16 v[0:15], v[0:3], v[76:79], 0
	s_waitcnt vmcnt(14) lgkmcnt(6)
	v_mfma_f32_32x32x16_bf16 v[0:15], v[124:127], v[72:75], v[0:15]
	s_waitcnt vmcnt(13) lgkmcnt(5)
	v_mfma_f32_32x32x16_bf16 v[0:15], v[128:131], v[68:71], v[0:15]
	s_waitcnt vmcnt(12) lgkmcnt(4)
	v_mfma_f32_32x32x16_bf16 v[0:15], v[186:189], v[64:67], v[0:15]
	s_waitcnt vmcnt(11) lgkmcnt(3)
	v_mfma_f32_32x32x16_bf16 v[0:15], v[190:193], v[60:63], v[0:15]
	s_waitcnt vmcnt(10) lgkmcnt(2)
	v_mfma_f32_32x32x16_bf16 v[0:15], v[194:197], v[56:59], v[0:15]
	s_waitcnt vmcnt(9) lgkmcnt(1)
	v_mfma_f32_32x32x16_bf16 v[0:15], v[198:201], v[52:55], v[0:15]
	s_waitcnt vmcnt(8) lgkmcnt(0)
	v_mfma_f32_32x32x16_bf16 v[0:15], v[202:205], v[48:51], v[0:15]
	s_nop 11
	v_ashrrev_i32_e32 v123, 31, v0
	v_bitop3_b32 v0, v123, v0, s11 bitop3:0x36
	v_ashrrev_i32_e32 v124, 31, v1
	v_ashrrev_i32_e32 v125, 31, v2
	v_ashrrev_i32_e32 v126, 31, v3
	v_ashrrev_i32_e32 v127, 31, v4
	v_ashrrev_i32_e32 v128, 31, v5
	v_ashrrev_i32_e32 v129, 31, v6
	v_ashrrev_i32_e32 v130, 31, v7
	v_ashrrev_i32_e32 v131, 31, v8
	v_ashrrev_i32_e32 v132, 31, v9
	v_ashrrev_i32_e32 v133, 31, v10
	v_ashrrev_i32_e32 v134, 31, v11
	v_ashrrev_i32_e32 v135, 31, v12
	v_ashrrev_i32_e32 v136, 31, v13
	v_ashrrev_i32_e32 v137, 31, v14
	v_perm_b32 v123, v0, s12, v100
	v_ashrrev_i32_e32 v0, 31, v15
	v_bitop3_b32 v1, v124, v1, s11 bitop3:0x36
	v_bitop3_b32 v2, v125, v2, s11 bitop3:0x36
	v_bitop3_b32 v3, v126, v3, s11 bitop3:0x36
	v_bitop3_b32 v4, v127, v4, s11 bitop3:0x36
	v_bitop3_b32 v5, v128, v5, s11 bitop3:0x36
	v_bitop3_b32 v6, v129, v6, s11 bitop3:0x36
	v_bitop3_b32 v7, v130, v7, s11 bitop3:0x36
	v_bitop3_b32 v8, v131, v8, s11 bitop3:0x36
	v_bitop3_b32 v9, v132, v9, s11 bitop3:0x36
	v_bitop3_b32 v10, v133, v10, s11 bitop3:0x36
	v_bitop3_b32 v11, v134, v11, s11 bitop3:0x36
	v_bitop3_b32 v12, v135, v12, s11 bitop3:0x36
	v_bitop3_b32 v13, v136, v13, s11 bitop3:0x36
	v_bitop3_b32 v14, v137, v14, s11 bitop3:0x36
	v_bitop3_b32 v0, v0, v15, s11 bitop3:0x36
	v_perm_b32 v132, v1, s12, v101
	v_perm_b32 v133, v2, s12, v102
	v_perm_b32 v134, v3, s12, v103
	v_perm_b32 v135, v4, s13, v100
	v_perm_b32 v136, v5, s13, v101
	v_perm_b32 v137, v6, s13, v102
	v_perm_b32 v138, v7, s13, v103
	v_perm_b32 v139, v8, s14, v100
	v_perm_b32 v140, v9, s14, v101
	v_perm_b32 v141, v10, s14, v102
	v_perm_b32 v142, v11, s14, v103
	v_perm_b32 v143, v12, s15, v100
	v_perm_b32 v144, v13, s15, v101
	v_perm_b32 v145, v14, s15, v102
	v_perm_b32 v146, v0, s15, v103
	v_mov_b32_e32 v147, v96
	ds_read_b128 v[0:3], v147
	ds_read_b128 v[124:127], v147 offset:32
	ds_read_b128 v[128:131], v147 offset:64
	ds_read_b128 v[186:189], v147 offset:96
	ds_read_b128 v[190:193], v147 offset:128
	ds_read_b128 v[194:197], v147 offset:160
	ds_read_b128 v[198:201], v147 offset:192
	ds_read_b128 v[202:205], v147 offset:224
	s_waitcnt lgkmcnt(7)
	v_mfma_f32_32x32x16_bf16 v[0:15], v[0:3], v[76:79], 0
	s_waitcnt lgkmcnt(6)
; #define LAS __attribute__((address_space(3)))
; __device__ __forceinline__ void phase_topk(Frame& F, const bf16_t* QP, const bf16_t* K1B, const bf16_t* K2B, unsigned short* EID, float* GATE) {
;     ...
;             for (int nb = 0; nb < 4; ++nb) { f32x16 acc = f32x16{};
;                 LAS const unsigned char* kb = F.lds + half * TK_KSET + (nb * 32 + r32) * TK_KSTRIDE + 16 * hi; asm volatile("" : "+v"(kb));
; #pragma unroll
;                 for (int kk = 0; kk < 8; ++kk) acc = __builtin_amdgcn_mfma_f32_32x32x16_bf16(*(LAS const bf16x8*)(kb + 32 * kk), qf[kk], acc, 0, 0, 0);
; #pragma unroll
;                 for (int r = 0; r < 16; ++r) {
;                     const unsigned x = __float_as_uint(acc[r]), o = x ^ ((unsigned)((int)x >> 31) | 0x80000000u); const int j = r >> 2;
;                     const unsigned pack = (unsigned)(127 - (nb * 32 + 0 + 8 * j)) | ((unsigned)(127 - (nb * 32 + 1 + 8 * j)) << 8) | ((unsigned)(127 - (nb * 32 + 2 + 8 * j)) << 16) | ((unsigned)(127 - (nb * 32 + 3 + 8 * j)) << 24);
;                     K[nb * 16 + r] = __builtin_amdgcn_perm(o, pack, 0x07060500u | (unsigned)(r & 3)); }
;                 __builtin_amdgcn_sched_barrier(0); }
	v_mfma_f32_32x32x16_bf16 v[0:15], v[124:127], v[72:75], v[0:15]
	s_waitcnt lgkmcnt(5)
	v_mfma_f32_32x32x16_bf16 v[0:15], v[128:131], v[68:71], v[0:15]
	s_waitcnt lgkmcnt(4)
	v_mfma_f32_32x32x16_bf16 v[0:15], v[186:189], v[64:67], v[0:15]
	s_waitcnt lgkmcnt(3)
	v_mfma_f32_32x32x16_bf16 v[0:15], v[190:193], v[60:63], v[0:15]
	s_waitcnt lgkmcnt(2)
	v_mfma_f32_32x32x16_bf16 v[0:15], v[194:197], v[56:59], v[0:15]
	s_waitcnt lgkmcnt(1)
	v_mfma_f32_32x32x16_bf16 v[0:15], v[198:201], v[52:55], v[0:15]
	s_waitcnt lgkmcnt(0)
	v_mfma_f32_32x32x16_bf16 v[0:15], v[202:205], v[48:51], v[0:15]
	s_nop 11
	v_ashrrev_i32_e32 v124, 31, v0
	v_ashrrev_i32_e32 v125, 31, v1
	v_ashrrev_i32_e32 v126, 31, v2
	v_ashrrev_i32_e32 v127, 31, v3
	v_ashrrev_i32_e32 v128, 31, v4
	v_ashrrev_i32_e32 v129, 31, v5
	v_ashrrev_i32_e32 v130, 31, v6
	v_ashrrev_i32_e32 v131, 31, v7
	v_ashrrev_i32_e32 v147, 31, v8
	v_ashrrev_i32_e32 v148, 31, v9
	v_ashrrev_i32_e32 v149, 31, v10
	v_ashrrev_i32_e32 v150, 31, v11
	v_ashrrev_i32_e32 v151, 31, v12
	v_ashrrev_i32_e32 v152, 31, v13
	v_ashrrev_i32_e32 v153, 31, v14
	v_ashrrev_i32_e32 v154, 31, v15
	v_bitop3_b32 v0, v124, v0, s11 bitop3:0x36
	v_bitop3_b32 v1, v125, v1, s11 bitop3:0x36
	v_bitop3_b32 v2, v126, v2, s11 bitop3:0x36
	v_bitop3_b32 v3, v127, v3, s11 bitop3:0x36
	v_bitop3_b32 v4, v128, v4, s11 bitop3:0x36
	v_bitop3_b32 v5, v129, v5, s11 bitop3:0x36
	v_bitop3_b32 v6, v130, v6, s11 bitop3:0x36
	v_bitop3_b32 v7, v131, v7, s11 bitop3:0x36
	v_bitop3_b32 v8, v147, v8, s11 bitop3:0x36
	v_bitop3_b32 v9, v148, v9, s11 bitop3:0x36
	v_bitop3_b32 v10, v149, v10, s11 bitop3:0x36
	v_bitop3_b32 v11, v150, v11, s11 bitop3:0x36
	v_bitop3_b32 v12, v151, v12, s11 bitop3:0x36
	v_bitop3_b32 v13, v152, v13, s11 bitop3:0x36
	v_bitop3_b32 v14, v153, v14, s11 bitop3:0x36
	v_bitop3_b32 v15, v154, v15, s11 bitop3:0x36
	v_perm_b32 v147, v0, s16, v100
	v_perm_b32 v148, v1, s16, v101
	v_perm_b32 v149, v2, s16, v102
	v_perm_b32 v150, v3, s16, v103
	v_perm_b32 v151, v4, s17, v100
	v_perm_b32 v152, v5, s17, v101
	v_perm_b32 v153, v6, s17, v102
	v_perm_b32 v154, v7, s17, v103
	v_perm_b32 v155, v8, s18, v100
	v_perm_b32 v156, v9, s18, v101
	v_perm_b32 v157, v10, s18, v102
	v_perm_b32 v158, v11, s18, v103
	v_perm_b32 v159, v12, s19, v100
	v_perm_b32 v160, v13, s19, v101
	v_perm_b32 v161, v14, s19, v102
	v_perm_b32 v162, v15, s19, v103
	v_mov_b32_e32 v163, v97
	ds_read_b128 v[0:3], v163
	ds_read_b128 v[124:127], v163 offset:32
	ds_read_b128 v[128:131], v163 offset:64
	ds_read_b128 v[186:189], v163 offset:96
	ds_read_b128 v[190:193], v163 offset:128
	ds_read_b128 v[194:197], v163 offset:160
	ds_read_b128 v[198:201], v163 offset:192
	ds_read_b128 v[202:205], v163 offset:224
	s_waitcnt lgkmcnt(7)
	v_mfma_f32_32x32x16_bf16 v[0:15], v[0:3], v[76:79], 0
	s_waitcnt lgkmcnt(6)
	v_mfma_f32_32x32x16_bf16 v[0:15], v[124:127], v[72:75], v[0:15]
	s_waitcnt lgkmcnt(5)
	v_mfma_f32_32x32x16_bf16 v[0:15], v[128:131], v[68:71], v[0:15]
	s_waitcnt lgkmcnt(4)
	v_mfma_f32_32x32x16_bf16 v[0:15], v[186:189], v[64:67], v[0:15]
	s_waitcnt lgkmcnt(3)
	v_mfma_f32_32x32x16_bf16 v[0:15], v[190:193], v[60:63], v[0:15]
	s_waitcnt lgkmcnt(2)
	v_mfma_f32_32x32x16_bf16 v[0:15], v[194:197], v[56:59], v[0:15]
	s_waitcnt lgkmcnt(1)
	v_mfma_f32_32x32x16_bf16 v[0:15], v[198:201], v[52:55], v[0:15]
	s_waitcnt lgkmcnt(0)
	v_mfma_f32_32x32x16_bf16 v[0:15], v[202:205], v[48:51], v[0:15]
	s_nop 11
	v_ashrrev_i32_e32 v124, 31, v0
	v_ashrrev_i32_e32 v125, 31, v1
	v_ashrrev_i32_e32 v126, 31, v2
	v_ashrrev_i32_e32 v127, 31, v3
	v_ashrrev_i32_e32 v128, 31, v4
	v_ashrrev_i32_e32 v129, 31, v5
	v_ashrrev_i32_e32 v130, 31, v6
	v_ashrrev_i32_e32 v131, 31, v7
	v_ashrrev_i32_e32 v163, 31, v8
	v_ashrrev_i32_e32 v164, 31, v9
	v_ashrrev_i32_e32 v165, 31, v10
	v_ashrrev_i32_e32 v166, 31, v11
	v_ashrrev_i32_e32 v167, 31, v12
	v_ashrrev_i32_e32 v168, 31, v13
	v_ashrrev_i32_e32 v169, 31, v14
	v_ashrrev_i32_e32 v170, 31, v15
	v_bitop3_b32 v0, v124, v0, s11 bitop3:0x36
	v_bitop3_b32 v1, v125, v1, s11 bitop3:0x36
	v_bitop3_b32 v2, v126, v2, s11 bitop3:0x36
	v_bitop3_b32 v3, v127, v3, s11 bitop3:0x36
	v_bitop3_b32 v4, v128, v4, s11 bitop3:0x36
	v_bitop3_b32 v5, v129, v5, s11 bitop3:0x36
	v_bitop3_b32 v6, v130, v6, s11 bitop3:0x36
	v_bitop3_b32 v7, v131, v7, s11 bitop3:0x36
	v_bitop3_b32 v8, v163, v8, s11 bitop3:0x36
	v_bitop3_b32 v9, v164, v9, s11 bitop3:0x36
	v_bitop3_b32 v10, v165, v10, s11 bitop3:0x36
	v_bitop3_b32 v11, v166, v11, s11 bitop3:0x36
	v_bitop3_b32 v12, v167, v12, s11 bitop3:0x36
	v_bitop3_b32 v13, v168, v13, s11 bitop3:0x36
	v_bitop3_b32 v14, v169, v14, s11 bitop3:0x36
	v_bitop3_b32 v15, v170, v15, s11 bitop3:0x36
	v_perm_b32 v128, v0, s20, v100
	v_perm_b32 v129, v1, s20, v101
	v_perm_b32 v130, v2, s20, v102
	v_perm_b32 v131, v3, s20, v103
	v_perm_b32 v163, v4, s21, v100
	v_perm_b32 v164, v5, s21, v101
	v_perm_b32 v165, v6, s21, v102
	v_perm_b32 v166, v7, s21, v103
	v_perm_b32 v167, v8, s22, v100
	v_perm_b32 v168, v9, s22, v101
	v_perm_b32 v169, v10, s22, v102
	v_perm_b32 v170, v11, s22, v103
	v_perm_b32 v171, v12, s23, v100
	v_perm_b32 v172, v13, s23, v101
	v_perm_b32 v173, v14, s23, v102
	v_perm_b32 v174, v15, s23, v103
	v_mov_b32_e32 v175, v98
	ds_read_b128 v[0:3], v175
	ds_read_b128 v[124:127], v175 offset:32
	s_waitcnt lgkmcnt(1)
	v_mfma_f32_32x32x16_bf16 v[0:15], v[0:3], v[76:79], 0
	s_waitcnt lgkmcnt(0)
	v_mfma_f32_32x32x16_bf16 v[0:15], v[124:127], v[72:75], v[0:15]
	ds_read_b128 v[72:75], v175 offset:64
	ds_read_b128 v[76:79], v175 offset:96
	s_waitcnt lgkmcnt(1)
	v_mfma_f32_32x32x16_bf16 v[0:15], v[72:75], v[68:71], v[0:15]
	s_waitcnt lgkmcnt(0)
; #define LAS __attribute__((address_space(3)))
; template <int OFF, int TOT> DEVFN void sort16_desc(unsigned (&a)[TOT]) {
; #pragma unroll
;     for (int q = 0; q < OE16_N; ++q) { const int i = OFF + OE16[q][0], l = OFF + OE16[q][1]; const unsigned x = a[i], y = a[l]; a[i] = x > y ? x : y; a[l] = x > y ? y : x; }
; }
; __device__ __forceinline__ void phase_topk(Frame& F, const bf16_t* QP, const bf16_t* K1B, const bf16_t* K2B, unsigned short* EID, float* GATE) {
;     ...
;             for (int nb = 0; nb < 4; ++nb) { f32x16 acc = f32x16{};
;                 LAS const unsigned char* kb = F.lds + half * TK_KSET + (nb * 32 + r32) * TK_KSTRIDE + 16 * hi; asm volatile("" : "+v"(kb));
; #pragma unroll
;                 for (int kk = 0; kk < 8; ++kk) acc = __builtin_amdgcn_mfma_f32_32x32x16_bf16(*(LAS const bf16x8*)(kb + 32 * kk), qf[kk], acc, 0, 0, 0);
; #pragma unroll
;                 for (int r = 0; r < 16; ++r) {
;                     const unsigned x = __float_as_uint(acc[r]), o = x ^ ((unsigned)((int)x >> 31) | 0x80000000u); const int j = r >> 2;
;                     const unsigned pack = (unsigned)(127 - (nb * 32 + 0 + 8 * j)) | ((unsigned)(127 - (nb * 32 + 1 + 8 * j)) << 8) | ((unsigned)(127 - (nb * 32 + 2 + 8 * j)) << 16) | ((unsigned)(127 - (nb * 32 + 3 + 8 * j)) << 24);
;                     K[nb * 16 + r] = __builtin_amdgcn_perm(o, pack, 0x07060500u | (unsigned)(r & 3)); }
;                 __builtin_amdgcn_sched_barrier(0); }
;             __builtin_amdgcn_sched_barrier(0); top16of64(K); __builtin_amdgcn_sched_barrier(0);
	v_mfma_f32_32x32x16_bf16 v[0:15], v[76:79], v[64:67], v[0:15]
	ds_read_b128 v[64:67], v175 offset:128
	ds_read_b128 v[68:71], v175 offset:160
	s_waitcnt lgkmcnt(1)
	v_mfma_f32_32x32x16_bf16 v[0:15], v[64:67], v[60:63], v[0:15]
	s_waitcnt lgkmcnt(0)
	v_mfma_f32_32x32x16_bf16 v[0:15], v[68:71], v[56:59], v[0:15]
	ds_read_b128 v[56:59], v175 offset:192
	ds_read_b128 v[60:63], v175 offset:224
	s_waitcnt lgkmcnt(1)
	v_mfma_f32_32x32x16_bf16 v[0:15], v[56:59], v[52:55], v[0:15]
	s_waitcnt lgkmcnt(0)
	v_mfma_f32_32x32x16_bf16 v[0:15], v[60:63], v[48:51], v[0:15]
	s_nop 11
	v_ashrrev_i32_e32 v48, 31, v0
	v_ashrrev_i32_e32 v49, 31, v1
	v_ashrrev_i32_e32 v50, 31, v2
	v_ashrrev_i32_e32 v51, 31, v3
	v_ashrrev_i32_e32 v52, 31, v4
	v_ashrrev_i32_e32 v53, 31, v5
	v_ashrrev_i32_e32 v54, 31, v6
	v_ashrrev_i32_e32 v55, 31, v7
	v_ashrrev_i32_e32 v56, 31, v8
	v_ashrrev_i32_e32 v57, 31, v9
	v_ashrrev_i32_e32 v58, 31, v10
	v_ashrrev_i32_e32 v59, 31, v11
	v_ashrrev_i32_e32 v60, 31, v12
	v_ashrrev_i32_e32 v61, 31, v13
	v_ashrrev_i32_e32 v62, 31, v14
	v_ashrrev_i32_e32 v63, 31, v15
	v_bitop3_b32 v0, v48, v0, s11 bitop3:0x36
	v_bitop3_b32 v1, v49, v1, s11 bitop3:0x36
	v_bitop3_b32 v2, v50, v2, s11 bitop3:0x36
	v_bitop3_b32 v3, v51, v3, s11 bitop3:0x36
	v_bitop3_b32 v4, v52, v4, s11 bitop3:0x36
	v_bitop3_b32 v5, v53, v5, s11 bitop3:0x36
	v_bitop3_b32 v6, v54, v6, s11 bitop3:0x36
	v_bitop3_b32 v7, v55, v7, s11 bitop3:0x36
	v_bitop3_b32 v8, v56, v8, s11 bitop3:0x36
	v_bitop3_b32 v9, v57, v9, s11 bitop3:0x36
	v_bitop3_b32 v10, v58, v10, s11 bitop3:0x36
	v_bitop3_b32 v11, v59, v11, s11 bitop3:0x36
	v_bitop3_b32 v12, v60, v12, s11 bitop3:0x36
	v_bitop3_b32 v13, v61, v13, s11 bitop3:0x36
	v_bitop3_b32 v14, v62, v14, s11 bitop3:0x36
	v_bitop3_b32 v15, v63, v15, s11 bitop3:0x36
	v_perm_b32 v0, v0, s24, v100
	v_perm_b32 v1, v1, s24, v101
	v_perm_b32 v2, v2, s24, v102
	v_perm_b32 v3, v3, s24, v103
	v_perm_b32 v4, v4, s25, v100
	v_perm_b32 v5, v5, s25, v101
	v_perm_b32 v6, v6, s25, v102
	v_perm_b32 v7, v7, s25, v103
	v_perm_b32 v8, v8, s26, v100
	v_perm_b32 v9, v9, s26, v101
	v_perm_b32 v10, v10, s26, v102
	v_perm_b32 v11, v11, s26, v103
	v_perm_b32 v12, v12, s27, v100
	v_perm_b32 v13, v13, s27, v101
	v_perm_b32 v14, v14, s27, v102
	v_perm_b32 v15, v15, s27, v103
	v_max_u32_e32 v48, v123, v132
	v_min_u32_e32 v49, v123, v132
	v_max_u32_e32 v50, v133, v134
	v_min_u32_e32 v51, v133, v134
	v_max_u32_e32 v52, v48, v50
	v_min_u32_e32 v48, v48, v50
	v_max_u32_e32 v50, v49, v51
	v_min_u32_e32 v49, v49, v51
	v_max_u32_e32 v51, v50, v48
	v_min_u32_e32 v48, v50, v48
	v_max_u32_e32 v50, v135, v136
	v_min_u32_e32 v53, v135, v136
	v_max_u32_e32 v54, v137, v138
	v_min_u32_e32 v55, v137, v138
	v_max_u32_e32 v56, v50, v54
	v_min_u32_e32 v50, v50, v54
	v_max_u32_e32 v54, v53, v55
	v_min_u32_e32 v53, v53, v55
	v_max_u32_e32 v55, v54, v50
	v_min_u32_e32 v50, v54, v50
	v_max_u32_e32 v54, v52, v56
	v_min_u32_e32 v52, v52, v56
	v_max_u32_e32 v56, v48, v50
	v_min_u32_e32 v48, v48, v50
	v_max_u32_e32 v50, v56, v52
	v_min_u32_e32 v52, v56, v52
	v_max_u32_e32 v56, v51, v55
	v_min_u32_e32 v51, v51, v55
	v_max_u32_e32 v55, v49, v53
	v_min_u32_e32 v49, v49, v53
	v_max_u32_e32 v53, v55, v51
	v_min_u32_e32 v51, v55, v51
	v_max_u32_e32 v55, v56, v50
	v_min_u32_e32 v50, v56, v50
	v_max_u32_e32 v56, v53, v52
	v_min_u32_e32 v52, v53, v52
	v_max_u32_e32 v53, v51, v48
	v_min_u32_e32 v48, v51, v48
	v_max_u32_e32 v51, v139, v140
	v_min_u32_e32 v57, v139, v140
	v_max_u32_e32 v58, v141, v142
	v_min_u32_e32 v59, v141, v142
	v_max_u32_e32 v60, v51, v58
	v_min_u32_e32 v51, v51, v58
	v_max_u32_e32 v58, v57, v59
	v_min_u32_e32 v57, v57, v59
	v_max_u32_e32 v59, v58, v51
	v_min_u32_e32 v51, v58, v51
	v_max_u32_e32 v58, v143, v144
	v_min_u32_e32 v61, v143, v144
	v_max_u32_e32 v143, v128, v129
	v_min_u32_e32 v128, v128, v129
	v_max_u32_e32 v129, v130, v131
	v_min_u32_e32 v130, v130, v131
	v_max_u32_e32 v131, v143, v129
	v_min_u32_e32 v129, v143, v129
	v_max_u32_e32 v143, v128, v130
	v_max_u32_e32 v72, v147, v148
	v_min_u32_e32 v73, v147, v148
	v_max_u32_e32 v74, v149, v150
	v_min_u32_e32 v75, v149, v150
	v_min_u32_e32 v128, v128, v130
	v_max_u32_e32 v130, v143, v129
	v_min_u32_e32 v129, v143, v129
	v_max_u32_e32 v143, v163, v164
	v_min_u32_e32 v144, v163, v164
	v_max_u32_e32 v163, v0, v1
	v_min_u32_e32 v0, v0, v1
	v_max_u32_e32 v1, v2, v3
	v_min_u32_e32 v2, v2, v3
	v_max_u32_e32 v76, v72, v74
	v_min_u32_e32 v72, v72, v74
	v_max_u32_e32 v74, v73, v75
	v_max_u32_e32 v3, v163, v1
	v_min_u32_e32 v1, v163, v1
	v_max_u32_e32 v163, v0, v2
	v_max_u32_e32 v62, v145, v146
	v_min_u32_e32 v63, v145, v146
	v_min_u32_e32 v73, v73, v75
	v_max_u32_e32 v75, v74, v72
	v_min_u32_e32 v72, v74, v72
	v_max_u32_e32 v74, v151, v152
	v_min_u32_e32 v77, v151, v152
	v_max_u32_e32 v78, v153, v154
	v_min_u32_e32 v79, v153, v154
	v_max_u32_e32 v145, v165, v166
	v_min_u32_e32 v146, v165, v166
	v_min_u32_e32 v0, v0, v2
	v_max_u32_e32 v2, v163, v1
	v_min_u32_e32 v1, v163, v1
	v_max_u32_e32 v163, v4, v5
	v_min_u32_e32 v4, v4, v5
	v_max_u32_e32 v5, v6, v7
	v_min_u32_e32 v6, v6, v7
	v_max_u32_e32 v123, v74, v78
	v_min_u32_e32 v74, v74, v78
	v_max_u32_e32 v78, v77, v79
	v_max_u32_e32 v147, v143, v145
	v_min_u32_e32 v143, v143, v145
	v_max_u32_e32 v145, v144, v146
	v_max_u32_e32 v7, v163, v5
	v_min_u32_e32 v5, v163, v5
	v_max_u32_e32 v163, v4, v6
	v_min_u32_e32 v77, v77, v79
	v_max_u32_e32 v79, v78, v74
	v_min_u32_e32 v74, v78, v74
	v_min_u32_e32 v144, v144, v146
	v_max_u32_e32 v146, v145, v143
	v_min_u32_e32 v143, v145, v143
	v_min_u32_e32 v4, v4, v6
	v_max_u32_e32 v6, v163, v5
	v_min_u32_e32 v5, v163, v5
	v_max_u32_e32 v78, v76, v123
	v_min_u32_e32 v76, v76, v123
; template <int OFF, int TOT> DEVFN void sort16_desc(unsigned (&a)[TOT]) {
; #pragma unroll
;     for (int q = 0; q < OE16_N; ++q) { const int i = OFF + OE16[q][0], l = OFF + OE16[q][1]; const unsigned x = a[i], y = a[l]; a[i] = x > y ? x : y; a[l] = x > y ? y : x; }
; }
	v_max_u32_e32 v123, v72, v74
	v_max_u32_e32 v145, v131, v147
	v_min_u32_e32 v131, v131, v147
	v_max_u32_e32 v147, v129, v143
	v_max_u32_e32 v163, v3, v7
	v_min_u32_e32 v3, v3, v7
	v_max_u32_e32 v7, v1, v5
	v_min_u32_e32 v72, v72, v74
	v_max_u32_e32 v74, v123, v76
	v_min_u32_e32 v76, v123, v76
	v_max_u32_e32 v123, v75, v79
	v_min_u32_e32 v75, v75, v79
	v_max_u32_e32 v79, v73, v77
	v_min_u32_e32 v129, v129, v143
	v_max_u32_e32 v143, v147, v131
	v_min_u32_e32 v131, v147, v131
	v_max_u32_e32 v147, v130, v146
	v_min_u32_e32 v130, v130, v146
	v_max_u32_e32 v146, v128, v144
	v_min_u32_e32 v1, v1, v5
	v_max_u32_e32 v5, v7, v3
	v_min_u32_e32 v3, v7, v3
	v_max_u32_e32 v7, v2, v6
	v_min_u32_e32 v2, v2, v6
	v_max_u32_e32 v6, v0, v4
	v_min_u32_e32 v73, v73, v77
	v_max_u32_e32 v77, v79, v75
	v_min_u32_e32 v75, v79, v75
	v_min_u32_e32 v128, v128, v144
	v_max_u32_e32 v144, v146, v130
	v_min_u32_e32 v130, v146, v130
	v_min_u32_e32 v0, v0, v4
	v_max_u32_e32 v4, v6, v2
	v_min_u32_e32 v2, v6, v2
	v_max_u32_e32 v79, v123, v74
	v_min_u32_e32 v74, v123, v74
	v_max_u32_e32 v123, v77, v76
	v_min_u32_e32 v76, v77, v76
	v_max_u32_e32 v77, v75, v72
	v_min_u32_e32 v72, v75, v72
	v_max_u32_e32 v75, v155, v156
	v_min_u32_e32 v124, v155, v156
	v_max_u32_e32 v125, v157, v158
	v_min_u32_e32 v126, v157, v158
	v_max_u32_e32 v146, v147, v143
	v_min_u32_e32 v143, v147, v143
	v_max_u32_e32 v147, v144, v131
	v_min_u32_e32 v131, v144, v131
	v_max_u32_e32 v144, v130, v129
	v_min_u32_e32 v129, v130, v129
	v_max_u32_e32 v130, v167, v168
	v_min_u32_e32 v148, v167, v168
	v_max_u32_e32 v149, v169, v170
	v_min_u32_e32 v150, v169, v170
	v_max_u32_e32 v6, v7, v5
	v_min_u32_e32 v5, v7, v5
	v_max_u32_e32 v7, v4, v3
	v_min_u32_e32 v3, v4, v3
	v_max_u32_e32 v4, v2, v1
	v_min_u32_e32 v1, v2, v1
	v_max_u32_e32 v2, v8, v9
	v_min_u32_e32 v8, v8, v9
	v_max_u32_e32 v9, v10, v11
	v_min_u32_e32 v10, v10, v11
	v_max_u32_e32 v127, v75, v125
	v_min_u32_e32 v75, v75, v125
	v_max_u32_e32 v125, v124, v126
	v_max_u32_e32 v151, v130, v149
	v_min_u32_e32 v130, v130, v149
	v_max_u32_e32 v149, v148, v150
	v_max_u32_e32 v11, v2, v9
	v_min_u32_e32 v2, v2, v9
	v_max_u32_e32 v9, v8, v10
	v_min_u32_e32 v124, v124, v126
	v_max_u32_e32 v126, v125, v75
	v_min_u32_e32 v75, v125, v75
	v_max_u32_e32 v125, v159, v160
	v_min_u32_e32 v132, v159, v160
	v_max_u32_e32 v133, v161, v162
	v_min_u32_e32 v134, v161, v162
	v_min_u32_e32 v148, v148, v150
	v_max_u32_e32 v150, v149, v130
	v_min_u32_e32 v130, v149, v130
	v_max_u32_e32 v149, v171, v172
	v_min_u32_e32 v152, v171, v172
	v_max_u32_e32 v153, v173, v174
	v_min_u32_e32 v154, v173, v174
	v_min_u32_e32 v8, v8, v10
	v_max_u32_e32 v10, v9, v2
	v_min_u32_e32 v2, v9, v2
	v_max_u32_e32 v9, v12, v13
	v_min_u32_e32 v12, v12, v13
	v_max_u32_e32 v13, v14, v15
	v_min_u32_e32 v14, v14, v15
	v_max_u32_e32 v64, v58, v62
	v_min_u32_e32 v58, v58, v62
	v_max_u32_e32 v62, v61, v63
	v_max_u32_e32 v135, v125, v133
	v_min_u32_e32 v125, v125, v133
	v_max_u32_e32 v133, v132, v134
	v_max_u32_e32 v155, v149, v153
	v_min_u32_e32 v149, v149, v153
	v_max_u32_e32 v153, v152, v154
	v_max_u32_e32 v15, v9, v13
	v_min_u32_e32 v9, v9, v13
	v_max_u32_e32 v13, v12, v14
	v_min_u32_e32 v61, v61, v63
	v_max_u32_e32 v63, v62, v58
	v_min_u32_e32 v58, v62, v58
	v_min_u32_e32 v132, v132, v134
	v_max_u32_e32 v134, v133, v125
	v_min_u32_e32 v125, v133, v125
	v_min_u32_e32 v152, v152, v154
	v_max_u32_e32 v154, v153, v149
	v_min_u32_e32 v149, v153, v149
	v_min_u32_e32 v12, v12, v14
	v_max_u32_e32 v14, v13, v9
	v_min_u32_e32 v9, v13, v9
	v_max_u32_e32 v62, v60, v64
	v_min_u32_e32 v60, v60, v64
	v_max_u32_e32 v64, v51, v58
	v_max_u32_e32 v133, v127, v135
	v_min_u32_e32 v127, v127, v135
	v_max_u32_e32 v135, v75, v125
	v_max_u32_e32 v153, v151, v155
	v_min_u32_e32 v151, v151, v155
	v_max_u32_e32 v155, v130, v149
	v_max_u32_e32 v13, v11, v15
	v_min_u32_e32 v11, v11, v15
	v_max_u32_e32 v15, v2, v9
	v_min_u32_e32 v51, v51, v58
	v_max_u32_e32 v58, v64, v60
	v_min_u32_e32 v60, v64, v60
	v_max_u32_e32 v64, v59, v63
	v_min_u32_e32 v59, v59, v63
	v_max_u32_e32 v63, v57, v61
	v_min_u32_e32 v75, v75, v125
	v_max_u32_e32 v125, v135, v127
	v_min_u32_e32 v127, v135, v127
	v_max_u32_e32 v135, v126, v134
	v_min_u32_e32 v126, v126, v134
	v_max_u32_e32 v134, v124, v132
	v_min_u32_e32 v130, v130, v149
	v_max_u32_e32 v149, v155, v151
	v_min_u32_e32 v151, v155, v151
	v_max_u32_e32 v155, v150, v154
	v_min_u32_e32 v150, v150, v154
	v_max_u32_e32 v154, v148, v152
	v_min_u32_e32 v2, v2, v9
	v_max_u32_e32 v9, v15, v11
	v_min_u32_e32 v11, v15, v11
	v_max_u32_e32 v15, v10, v14
	v_min_u32_e32 v10, v10, v14
	v_max_u32_e32 v14, v8, v12
	v_min_u32_e32 v57, v57, v61
	v_max_u32_e32 v61, v63, v59
	v_min_u32_e32 v124, v124, v132
	v_max_u32_e32 v132, v134, v126
	v_min_u32_e32 v148, v148, v152
	v_max_u32_e32 v152, v154, v150
	v_min_u32_e32 v8, v8, v12
	v_max_u32_e32 v12, v14, v10
	v_min_u32_e32 v59, v63, v59
	v_max_u32_e32 v63, v64, v58
	v_min_u32_e32 v58, v64, v58
	v_max_u32_e32 v64, v61, v60
	v_min_u32_e32 v60, v61, v60
	v_min_u32_e32 v126, v134, v126
	v_max_u32_e32 v134, v135, v125
	v_min_u32_e32 v125, v135, v125
	v_max_u32_e32 v135, v132, v127
	v_min_u32_e32 v127, v132, v127
	v_min_u32_e32 v150, v154, v150
	v_max_u32_e32 v154, v155, v149
	v_min_u32_e32 v149, v155, v149
	v_max_u32_e32 v155, v152, v151
	v_min_u32_e32 v151, v152, v151
	v_min_u32_e32 v10, v14, v10
	v_max_u32_e32 v14, v15, v9
	v_min_u32_e32 v9, v15, v9
	v_max_u32_e32 v15, v12, v11
	v_min_u32_e32 v11, v12, v11
	v_max_u32_e32 v61, v59, v51
	v_min_u32_e32 v51, v59, v51
	v_min_u32_e32 v59, v54, v62
	v_max_u32_e32 v65, v52, v60
	v_max_u32_e32 v132, v126, v75
	v_min_u32_e32 v75, v126, v75
; template <int OFF, int TOT> DEVFN void sort16_desc(unsigned (&a)[TOT]) {
; #pragma unroll
;     for (int q = 0; q < OE16_N; ++q) { const int i = OFF + OE16[q][0], l = OFF + OE16[q][1]; const unsigned x = a[i], y = a[l]; a[i] = x > y ? x : y; a[l] = x > y ? y : x; }
; }
; template <int OFF, int TOT> DEVFN void bitonic_merge16_desc(unsigned (&a)[TOT]) {
; #pragma unroll
;     for (int j = 8; j > 0; j >>= 1)
; #pragma unroll
;         for (int i = 0; i < 16; ++i) { const int l = i ^ j; if (l > i) { const unsigned x = a[OFF + i], y = a[OFF + l]; a[OFF + i] = x > y ? x : y; a[OFF + l] = x > y ? y : x; } }
; }
; template <int A, int B, int TOT> DEVFN void merge_top16(unsigned (&a)[TOT]) {
; #pragma unroll
;     for (int i = 0; i < 16; ++i) { const unsigned x = a[A + i], y = a[B + 15 - i]; a[A + i] = x > y ? x : y; }
;     bitonic_merge16_desc<A, TOT>(a);
; }
; DEVFN void top16of64(unsigned (&a)[64]) {
;     sort16_desc<0, 64>(a); sort16_desc<16, 64>(a); sort16_desc<32, 64>(a); sort16_desc<48, 64>(a);
;     merge_top16<0, 16, 64>(a); merge_top16<32, 48, 64>(a); merge_top16<0, 32, 64>(a);
	v_min_u32_e32 v126, v78, v133
	v_max_u32_e32 v136, v76, v127
	v_max_u32_e32 v152, v150, v130
	v_min_u32_e32 v130, v150, v130
	v_min_u32_e32 v150, v145, v153
	v_max_u32_e32 v156, v131, v151
	v_max_u32_e32 v12, v10, v2
	v_min_u32_e32 v2, v10, v2
	v_min_u32_e32 v10, v163, v13
	v_max_u32_e32 v164, v3, v11
	v_min_u32_e32 v52, v52, v60
	v_max_u32_e32 v60, v65, v59
	v_min_u32_e32 v59, v65, v59
	v_max_u32_e32 v65, v50, v58
	v_min_u32_e32 v50, v50, v58
	v_max_u32_e32 v58, v48, v51
	v_min_u32_e32 v76, v76, v127
	v_max_u32_e32 v127, v136, v126
	v_min_u32_e32 v126, v136, v126
	v_max_u32_e32 v136, v74, v125
	v_min_u32_e32 v74, v74, v125
	v_max_u32_e32 v125, v72, v75
	v_min_u32_e32 v131, v131, v151
	v_max_u32_e32 v151, v156, v150
	v_min_u32_e32 v150, v156, v150
	v_max_u32_e32 v156, v143, v149
	v_min_u32_e32 v143, v143, v149
	v_max_u32_e32 v149, v129, v130
	v_min_u32_e32 v3, v3, v11
	v_max_u32_e32 v11, v164, v10
	v_min_u32_e32 v10, v164, v10
	v_max_u32_e32 v164, v5, v9
	v_min_u32_e32 v5, v5, v9
	v_max_u32_e32 v9, v1, v2
	v_min_u32_e32 v48, v48, v51
	v_max_u32_e32 v51, v58, v50
	v_min_u32_e32 v50, v58, v50
	v_min_u32_e32 v72, v72, v75
	v_max_u32_e32 v75, v125, v74
	v_min_u32_e32 v74, v125, v74
	v_min_u32_e32 v129, v129, v130
	v_max_u32_e32 v130, v149, v143
	v_min_u32_e32 v143, v149, v143
	v_min_u32_e32 v1, v1, v2
	v_max_u32_e32 v2, v9, v5
	v_min_u32_e32 v5, v9, v5
	v_max_u32_e32 v58, v65, v60
	v_min_u32_e32 v60, v65, v60
	v_max_u32_e32 v65, v51, v59
	v_min_u32_e32 v51, v51, v59
	v_max_u32_e32 v59, v50, v52
	v_min_u32_e32 v50, v50, v52
	v_max_u32_e32 v52, v55, v63
	v_min_u32_e32 v55, v55, v63
	v_max_u32_e32 v63, v53, v61
	v_max_u32_e32 v125, v136, v127
	v_min_u32_e32 v127, v136, v127
	v_max_u32_e32 v136, v75, v126
	v_min_u32_e32 v75, v75, v126
	v_max_u32_e32 v126, v74, v76
	v_min_u32_e32 v74, v74, v76
	v_max_u32_e32 v76, v79, v134
	v_min_u32_e32 v79, v79, v134
	v_max_u32_e32 v134, v77, v132
	v_max_u32_e32 v149, v156, v151
	v_min_u32_e32 v151, v156, v151
	v_max_u32_e32 v156, v130, v150
	v_min_u32_e32 v130, v130, v150
	v_max_u32_e32 v150, v143, v131
	v_min_u32_e32 v131, v143, v131
	v_max_u32_e32 v143, v146, v154
	v_min_u32_e32 v146, v146, v154
	v_max_u32_e32 v154, v144, v152
	v_max_u32_e32 v9, v164, v11
	v_min_u32_e32 v11, v164, v11
	v_max_u32_e32 v164, v2, v10
	v_min_u32_e32 v2, v2, v10
	v_max_u32_e32 v10, v5, v3
	v_min_u32_e32 v3, v5, v3
	v_max_u32_e32 v5, v6, v14
	v_min_u32_e32 v6, v6, v14
	v_max_u32_e32 v14, v4, v12
	v_min_u32_e32 v53, v53, v61
	v_max_u32_e32 v61, v63, v55
	v_min_u32_e32 v55, v63, v55
	v_max_u32_e32 v63, v56, v64
	v_min_u32_e32 v56, v56, v64
	v_max_u32_e32 v64, v49, v57
	v_min_u32_e32 v77, v77, v132
	v_max_u32_e32 v132, v134, v79
	v_min_u32_e32 v79, v134, v79
	v_max_u32_e32 v134, v123, v135
	v_min_u32_e32 v123, v123, v135
	v_max_u32_e32 v135, v73, v124
	v_min_u32_e32 v144, v144, v152
	v_max_u32_e32 v152, v154, v146
	v_min_u32_e32 v146, v154, v146
	v_max_u32_e32 v154, v147, v155
	v_min_u32_e32 v147, v147, v155
	v_max_u32_e32 v155, v128, v148
	v_min_u32_e32 v4, v4, v12
	v_max_u32_e32 v12, v14, v6
	v_min_u32_e32 v6, v14, v6
	v_max_u32_e32 v14, v7, v15
	v_min_u32_e32 v7, v7, v15
	v_max_u32_e32 v15, v0, v8
	v_min_u32_e32 v49, v49, v57
	v_max_u32_e32 v57, v64, v56
	v_min_u32_e32 v56, v64, v56
	v_min_u32_e32 v73, v73, v124
	v_max_u32_e32 v124, v135, v123
	v_min_u32_e32 v123, v135, v123
	v_min_u32_e32 v128, v128, v148
	v_max_u32_e32 v148, v155, v147
	v_min_u32_e32 v147, v155, v147
	v_min_u32_e32 v0, v0, v8
	v_max_u32_e32 v8, v15, v7
	v_min_u32_e32 v7, v15, v7
	v_max_u32_e32 v64, v63, v61
	v_min_u32_e32 v61, v63, v61
	v_max_u32_e32 v63, v57, v55
	v_min_u32_e32 v55, v57, v55
	v_max_u32_e32 v57, v56, v53
	v_min_u32_e32 v53, v56, v53
	v_max_u32_e32 v135, v134, v132
	v_min_u32_e32 v132, v134, v132
	v_max_u32_e32 v134, v124, v79
	v_min_u32_e32 v79, v124, v79
	v_max_u32_e32 v124, v123, v77
	v_min_u32_e32 v77, v123, v77
	v_max_u32_e32 v155, v154, v152
	v_min_u32_e32 v152, v154, v152
	v_max_u32_e32 v154, v148, v146
	v_min_u32_e32 v146, v148, v146
	v_max_u32_e32 v148, v147, v144
	v_min_u32_e32 v144, v147, v144
	v_max_u32_e32 v15, v14, v12
	v_min_u32_e32 v12, v14, v12
	v_max_u32_e32 v14, v8, v6
	v_min_u32_e32 v6, v8, v6
	v_max_u32_e32 v8, v7, v4
	v_min_u32_e32 v4, v7, v4
	v_min_u32_e32 v56, v52, v58
	v_min_u32_e32 v66, v64, v60
	v_min_u32_e32 v67, v61, v65
	v_min_u32_e32 v68, v63, v51
	v_min_u32_e32 v69, v55, v59
	v_min_u32_e32 v70, v57, v50
	v_min_u32_e32 v71, v53, v48
	v_min_u32_e32 v123, v76, v125
	v_min_u32_e32 v137, v135, v127
	v_min_u32_e32 v138, v132, v136
	v_min_u32_e32 v139, v134, v75
	v_min_u32_e32 v140, v79, v126
	v_min_u32_e32 v141, v124, v74
	v_min_u32_e32 v142, v77, v72
	v_min_u32_e32 v147, v143, v149
	v_min_u32_e32 v157, v155, v151
	v_min_u32_e32 v158, v152, v156
	v_min_u32_e32 v159, v154, v130
	v_min_u32_e32 v160, v146, v150
	v_min_u32_e32 v161, v148, v131
	v_min_u32_e32 v162, v144, v129
	v_min_u32_e32 v7, v5, v9
	v_min_u32_e32 v165, v15, v11
	v_min_u32_e32 v166, v12, v164
	v_min_u32_e32 v167, v14, v2
	v_min_u32_e32 v168, v6, v10
	v_min_u32_e32 v169, v8, v3
	v_min_u32_e32 v170, v4, v1
	v_max3_u32 v54, v54, v62, v73
	v_max3_u32 v52, v52, v58, v142
	v_max3_u32 v56, v56, v77, v72
	v_max3_u32 v58, v64, v60, v141
	v_max3_u32 v60, v66, v124, v74
	v_max3_u32 v61, v61, v65, v140
	v_max3_u32 v62, v67, v79, v126
	v_max3_u32 v51, v63, v51, v139
	v_max3_u32 v63, v68, v134, v75
	v_max3_u32 v55, v55, v59, v138
	v_max3_u32 v59, v69, v132, v136
	v_max3_u32 v50, v57, v50, v137
	v_max3_u32 v57, v70, v135, v127
	v_max3_u32 v48, v53, v48, v123
	v_max3_u32 v53, v71, v76, v125
	v_max3_u32 v49, v49, v78, v133
	v_max3_u32 v0, v145, v153, v0
; template <int A, int B, int TOT> DEVFN void merge_top16(unsigned (&a)[TOT]) {
; #pragma unroll
;     for (int i = 0; i < 16; ++i) { const unsigned x = a[A + i], y = a[B + 15 - i]; a[A + i] = x > y ? x : y; }
;     bitonic_merge16_desc<A, TOT>(a);
; }
; DEVFN void top16of64(unsigned (&a)[64]) {
;     sort16_desc<0, 64>(a); sort16_desc<16, 64>(a); sort16_desc<32, 64>(a); sort16_desc<48, 64>(a);
;     merge_top16<0, 16, 64>(a); merge_top16<32, 48, 64>(a); merge_top16<0, 32, 64>(a);
; __device__ __forceinline__ void phase_topk(Frame& F, const bf16_t* QP, const bf16_t* K1B, const bf16_t* K2B, unsigned short* EID, float* GATE) {
;     ...
;             for (int i = 0; i < 16; ++i) K[i] ^= h4;
;             unsigned C[16];
; #pragma unroll
;             for (int i = 0; i < 16; ++i) { const unsigned y = (unsigned)__shfl_xor((int)K[15 - i], 32); C[i] = K[i] > y ? K[i] : y; }
;             bitonic_merge16_desc<0, 16>(C);
	v_max3_u32 v72, v143, v149, v170
	v_max3_u32 v1, v147, v4, v1
	v_max3_u32 v4, v155, v151, v169
	v_max3_u32 v3, v157, v8, v3
	v_max3_u32 v8, v152, v156, v168
	v_max3_u32 v6, v158, v6, v10
	v_max3_u32 v10, v154, v130, v167
	v_max3_u32 v2, v159, v14, v2
	v_max3_u32 v14, v146, v150, v166
	v_max3_u32 v12, v160, v12, v164
	v_max3_u32 v73, v148, v131, v165
	v_max3_u32 v11, v161, v15, v11
	v_max3_u32 v7, v144, v129, v7
	v_max3_u32 v5, v162, v5, v9
	v_max3_u32 v9, v128, v163, v13
	v_max_u32_e32 v64, v54, v63
	v_min_u32_e32 v54, v54, v63
	v_max_u32_e32 v63, v52, v55
	v_min_u32_e32 v52, v52, v55
	v_max_u32_e32 v55, v56, v59
	v_min_u32_e32 v56, v56, v59
	v_max_u32_e32 v59, v58, v50
	v_min_u32_e32 v50, v58, v50
	v_max_u32_e32 v58, v60, v57
	v_min_u32_e32 v57, v60, v57
	v_max_u32_e32 v60, v61, v48
	v_min_u32_e32 v48, v61, v48
	v_max_u32_e32 v61, v62, v53
	v_min_u32_e32 v53, v62, v53
	v_max_u32_e32 v62, v51, v49
	v_min_u32_e32 v49, v51, v49
	v_max_u32_e32 v13, v0, v2
	v_min_u32_e32 v0, v0, v2
	v_max_u32_e32 v2, v72, v14
	v_min_u32_e32 v14, v72, v14
	v_max_u32_e32 v15, v1, v12
	v_min_u32_e32 v1, v1, v12
	v_max_u32_e32 v12, v4, v73
	v_min_u32_e32 v4, v4, v73
	v_max_u32_e32 v72, v3, v11
	v_min_u32_e32 v3, v3, v11
	v_max_u32_e32 v11, v8, v7
	v_min_u32_e32 v7, v8, v7
	v_max_u32_e32 v8, v6, v5
	v_min_u32_e32 v5, v6, v5
	v_max_u32_e32 v6, v10, v9
	v_min_u32_e32 v9, v10, v9
	v_max_u32_e32 v51, v64, v58
	v_min_u32_e32 v58, v64, v58
	v_max_u32_e32 v64, v63, v60
	v_min_u32_e32 v60, v63, v60
	v_max_u32_e32 v63, v55, v61
	v_min_u32_e32 v55, v55, v61
	v_max_u32_e32 v61, v59, v62
	v_min_u32_e32 v59, v59, v62
	v_max_u32_e32 v62, v54, v57
	v_min_u32_e32 v54, v54, v57
	v_max_u32_e32 v57, v52, v48
	v_min_u32_e32 v48, v52, v48
	v_max_u32_e32 v52, v56, v53
	v_min_u32_e32 v53, v56, v53
	v_max_u32_e32 v56, v50, v49
	v_min_u32_e32 v49, v50, v49
	v_max_u32_e32 v10, v13, v72
	v_min_u32_e32 v13, v13, v72
	v_max_u32_e32 v72, v2, v11
	v_min_u32_e32 v2, v2, v11
	v_max_u32_e32 v11, v15, v8
	v_min_u32_e32 v8, v15, v8
	v_max_u32_e32 v15, v12, v6
	v_min_u32_e32 v6, v12, v6
	v_max_u32_e32 v12, v0, v3
	v_min_u32_e32 v0, v0, v3
	v_max_u32_e32 v3, v14, v7
	v_min_u32_e32 v7, v14, v7
	v_max_u32_e32 v14, v1, v5
	v_min_u32_e32 v1, v1, v5
	v_max_u32_e32 v5, v4, v9
	v_min_u32_e32 v4, v4, v9
	v_max_u32_e32 v50, v51, v63
	v_min_u32_e32 v51, v51, v63
	v_max_u32_e32 v63, v64, v61
	v_min_u32_e32 v61, v64, v61
	v_max_u32_e32 v64, v58, v55
	v_min_u32_e32 v55, v58, v55
	v_max_u32_e32 v58, v60, v59
	v_min_u32_e32 v59, v60, v59
	v_max_u32_e32 v60, v62, v52
	v_min_u32_e32 v52, v62, v52
	v_max_u32_e32 v62, v57, v56
	v_min_u32_e32 v56, v57, v56
	v_max_u32_e32 v57, v54, v53
	v_min_u32_e32 v53, v54, v53
	v_max_u32_e32 v54, v48, v49
	v_min_u32_e32 v48, v48, v49
	v_max_u32_e32 v9, v10, v11
	v_min_u32_e32 v10, v10, v11
	v_max_u32_e32 v11, v72, v15
	v_min_u32_e32 v15, v72, v15
	v_max_u32_e32 v72, v13, v8
	v_min_u32_e32 v8, v13, v8
	v_max_u32_e32 v13, v2, v6
	v_min_u32_e32 v2, v2, v6
	v_max_u32_e32 v6, v12, v14
	v_min_u32_e32 v12, v12, v14
	v_max_u32_e32 v14, v3, v5
	v_min_u32_e32 v3, v3, v5
	v_max_u32_e32 v5, v0, v1
	v_min_u32_e32 v0, v0, v1
	v_max_u32_e32 v1, v7, v4
	v_min_u32_e32 v4, v7, v4
	v_min_u32_e32 v49, v50, v63
	v_min_u32_e32 v65, v51, v61
	v_min_u32_e32 v66, v64, v58
	v_min_u32_e32 v67, v55, v59
	v_min_u32_e32 v68, v60, v62
	v_min_u32_e32 v69, v52, v56
	v_min_u32_e32 v70, v57, v54
	v_min_u32_e32 v71, v53, v48
	v_min_u32_e32 v7, v9, v11
	v_min_u32_e32 v73, v10, v15
	v_min_u32_e32 v74, v72, v13
	v_min_u32_e32 v75, v8, v2
	v_min_u32_e32 v76, v6, v14
	v_min_u32_e32 v77, v12, v3
	v_min_u32_e32 v78, v5, v1
	v_min_u32_e32 v79, v0, v4
	v_max3_u32 v50, v50, v63, v79
	v_max3_u32 v0, v49, v0, v4
	v_max3_u32 v4, v51, v61, v78
	v_max3_u32 v1, v65, v5, v1
	v_max3_u32 v5, v64, v58, v77
	v_max3_u32 v3, v66, v12, v3
	v_max3_u32 v12, v55, v59, v76
	v_max3_u32 v6, v67, v6, v14
	v_max3_u32 v14, v60, v62, v75
	v_max3_u32 v2, v68, v8, v2
	v_max3_u32 v8, v52, v56, v74
	v_max3_u32 v13, v69, v72, v13
	v_max3_u32 v49, v57, v54, v73
	v_max3_u32 v10, v70, v10, v15
	v_max3_u32 v7, v53, v48, v7
	v_max3_u32 v9, v71, v9, v11
	v_max_u32_e32 v11, v50, v14
	v_min_u32_e32 v14, v50, v14
	v_max_u32_e32 v15, v0, v2
	v_min_u32_e32 v0, v0, v2
	v_max_u32_e32 v2, v4, v8
	v_min_u32_e32 v4, v4, v8
	v_max_u32_e32 v8, v1, v13
	v_min_u32_e32 v1, v1, v13
	v_max_u32_e32 v13, v5, v49
	v_min_u32_e32 v5, v5, v49
	v_max_u32_e32 v48, v3, v10
	v_min_u32_e32 v3, v3, v10
	v_max_u32_e32 v10, v12, v7
	v_min_u32_e32 v7, v12, v7
	v_max_u32_e32 v12, v6, v9
	v_min_u32_e32 v6, v6, v9
	v_max_u32_e32 v9, v11, v13
	v_min_u32_e32 v11, v11, v13
	v_max_u32_e32 v13, v15, v48
	v_min_u32_e32 v15, v15, v48
	v_max_u32_e32 v48, v2, v10
	v_min_u32_e32 v2, v2, v10
	v_max_u32_e32 v10, v8, v12
	v_min_u32_e32 v8, v8, v12
	v_max_u32_e32 v12, v14, v5
	v_min_u32_e32 v5, v14, v5
	v_max_u32_e32 v14, v0, v3
	v_min_u32_e32 v0, v0, v3
	v_max_u32_e32 v3, v4, v7
	v_min_u32_e32 v4, v4, v7
	v_max_u32_e32 v7, v1, v6
	v_min_u32_e32 v1, v1, v6
	v_max_u32_e32 v6, v9, v48
	v_min_u32_e32 v9, v9, v48
	v_max_u32_e32 v48, v13, v10
	v_min_u32_e32 v10, v13, v10
	v_max_u32_e32 v13, v11, v2
	v_min_u32_e32 v2, v11, v2
	v_max_u32_e32 v11, v15, v8
	v_min_u32_e32 v8, v15, v8
	v_max_u32_e32 v15, v12, v3
	v_min_u32_e32 v3, v12, v3
	v_max_u32_e32 v12, v14, v7
	v_min_u32_e32 v7, v14, v7
	v_max_u32_e32 v14, v5, v4
	v_min_u32_e32 v4, v5, v4
	v_max_u32_e32 v5, v0, v1
	v_min_u32_e32 v0, v0, v1
	v_max_u32_e32 v1, v6, v48
	v_min_u32_e32 v6, v6, v48
	v_max_u32_e32 v48, v9, v10
	v_min_u32_e32 v9, v9, v10
	v_max_u32_e32 v10, v13, v11
	v_min_u32_e32 v11, v13, v11
	v_max_u32_e32 v13, v2, v8
	v_min_u32_e32 v2, v2, v8
	v_max_u32_e32 v8, v15, v12
	v_min_u32_e32 v12, v15, v12
	v_max_u32_e32 v15, v3, v7
	v_min_u32_e32 v3, v3, v7
	v_max_u32_e32 v7, v14, v5
	v_min_u32_e32 v5, v14, v5
	v_max_u32_e32 v14, v4, v0
	v_min_u32_e32 v0, v4, v0
	v_xor_b32_e32 v15, v15, v105
	v_xor_b32_e32 v0, v0, v105
	v_xor_b32_e32 v3, v3, v105
	v_xor_b32_e32 v7, v7, v105
	v_xor_b32_e32 v5, v5, v105
	v_xor_b32_e32 v14, v14, v105
	v_xor_b32_e32 v4, v6, v105
	v_xor_b32_e32 v6, v48, v105
	ds_bpermute_b32 v48, v119, v0
	ds_bpermute_b32 v49, v119, v14
	ds_bpermute_b32 v50, v119, v5
	ds_bpermute_b32 v51, v119, v7
	ds_bpermute_b32 v52, v119, v3
	ds_bpermute_b32 v53, v119, v15
	v_xor_b32_e32 v1, v1, v105
	v_xor_b32_e32 v9, v9, v105
	v_xor_b32_e32 v10, v10, v105
	v_xor_b32_e32 v11, v11, v105
	v_xor_b32_e32 v13, v13, v105
	v_xor_b32_e32 v2, v2, v105
	v_xor_b32_e32 v8, v8, v105
	v_xor_b32_e32 v12, v12, v105
	s_waitcnt lgkmcnt(5)
; __device__ __forceinline__ float ord2f(unsigned o) { return __uint_as_float(o ^ (~(unsigned)((int)o >> 31) | 0x80000000u)); }
; __device__ __forceinline__ void phase_topk(Frame& F, const bf16_t* QP, const bf16_t* K1B, const bf16_t* K2B, unsigned short* EID, float* GATE) {
;     ...
;             for (int i = 0; i < 16; ++i) { const unsigned y = (unsigned)__shfl_xor((int)K[15 - i], 32); C[i] = K[i] > y ? K[i] : y; }
;             bitonic_merge16_desc<0, 16>(C);
; #pragma unroll
;             for (int i = 0; i < 16; ++i) { if (half == 0) V1[i] = C[i]; else V2[i] = C[i]; }
;             __builtin_amdgcn_sched_barrier(0);
;         }
;         float f1[16], f2[16];
; #pragma unroll
;         for (int a = 0; a < 16; ++a) { I1s[a * 64 + lane] = 127u - (V1[a] & 127u); I2s[a * 64 + lane] = 127u - (V2[a] & 127u); f1[a] = ord2f(V1[a] & ~127u); f2[a] = ord2f(V2[a] & ~127u); }
	v_max_u32_e32 v48, v1, v48
	s_waitcnt lgkmcnt(4)
	v_max_u32_e32 v49, v4, v49
	s_waitcnt lgkmcnt(3)
	v_max_u32_e32 v50, v6, v50
	s_waitcnt lgkmcnt(2)
	v_max_u32_e32 v51, v9, v51
	s_waitcnt lgkmcnt(1)
	v_max_u32_e32 v52, v10, v52
	s_waitcnt lgkmcnt(0)
	v_max_u32_e32 v53, v11, v53
	ds_bpermute_b32 v54, v119, v12
	ds_bpermute_b32 v55, v119, v8
	ds_bpermute_b32 v56, v119, v2
	ds_bpermute_b32 v57, v119, v13
	ds_bpermute_b32 v11, v119, v11
	ds_bpermute_b32 v10, v119, v10
	ds_bpermute_b32 v9, v119, v9
	ds_bpermute_b32 v6, v119, v6
	ds_bpermute_b32 v4, v119, v4
	ds_bpermute_b32 v1, v119, v1
	s_waitcnt lgkmcnt(9)
	v_max_u32_e32 v13, v13, v54
	s_waitcnt lgkmcnt(8)
	v_max_u32_e32 v2, v2, v55
	s_waitcnt lgkmcnt(7)
	v_max_u32_e32 v8, v8, v56
	s_waitcnt lgkmcnt(6)
	v_max_u32_e32 v12, v12, v57
	s_waitcnt lgkmcnt(5)
	v_max_u32_e32 v11, v15, v11
	s_waitcnt lgkmcnt(4)
	v_max_u32_e32 v3, v3, v10
	s_waitcnt lgkmcnt(3)
	v_max_u32_e32 v7, v7, v9
	s_waitcnt lgkmcnt(2)
	v_max_u32_e32 v5, v5, v6
	s_waitcnt lgkmcnt(1)
	v_max_u32_e32 v4, v14, v4
	s_waitcnt lgkmcnt(0)
	v_max_u32_e32 v0, v0, v1
	v_max_u32_e32 v1, v48, v8
	v_min_u32_e32 v6, v48, v8
	v_max_u32_e32 v8, v49, v12
	v_min_u32_e32 v9, v49, v12
	v_max_u32_e32 v10, v50, v11
	v_min_u32_e32 v11, v50, v11
	v_max_u32_e32 v12, v51, v3
	v_min_u32_e32 v3, v51, v3
	v_max_u32_e32 v14, v52, v7
	v_min_u32_e32 v7, v52, v7
	v_max_u32_e32 v15, v53, v5
	v_min_u32_e32 v5, v53, v5
	v_max_u32_e32 v48, v13, v4
	v_min_u32_e32 v4, v13, v4
	v_max_u32_e32 v13, v2, v0
	v_min_u32_e32 v0, v2, v0
	v_max_u32_e32 v2, v1, v14
	v_min_u32_e32 v1, v1, v14
	v_max_u32_e32 v14, v8, v15
	v_min_u32_e32 v8, v8, v15
	v_max_u32_e32 v15, v10, v48
	v_min_u32_e32 v10, v10, v48
	v_max_u32_e32 v48, v12, v13
	v_min_u32_e32 v12, v12, v13
	v_max_u32_e32 v13, v6, v7
	v_min_u32_e32 v6, v6, v7
	v_max_u32_e32 v7, v9, v5
	v_min_u32_e32 v5, v9, v5
	v_max_u32_e32 v9, v11, v4
	v_min_u32_e32 v4, v11, v4
	v_max_u32_e32 v11, v3, v0
	v_min_u32_e32 v0, v3, v0
	v_max_u32_e32 v3, v2, v15
	v_min_u32_e32 v2, v2, v15
	v_max_u32_e32 v15, v14, v48
	v_min_u32_e32 v14, v14, v48
	v_max_u32_e32 v48, v1, v10
	v_min_u32_e32 v1, v1, v10
	v_max_u32_e32 v10, v8, v12
	v_min_u32_e32 v8, v8, v12
	v_max_u32_e32 v12, v13, v9
	v_min_u32_e32 v9, v13, v9
	v_max_u32_e32 v13, v7, v11
	v_min_u32_e32 v7, v7, v11
	v_max_u32_e32 v11, v6, v4
	v_min_u32_e32 v4, v6, v4
	v_max_u32_e32 v6, v5, v0
	v_min_u32_e32 v0, v5, v0
	v_max_u32_e32 v5, v3, v15
	v_min_u32_e32 v3, v3, v15
	v_max_u32_e32 v15, v2, v14
	v_min_u32_e32 v2, v2, v14
	v_max_u32_e32 v14, v48, v10
	v_min_u32_e32 v10, v48, v10
	v_max_u32_e32 v48, v1, v8
	v_min_u32_e32 v1, v1, v8
	v_max_u32_e32 v8, v12, v13
	v_min_u32_e32 v12, v12, v13
	v_max_u32_e32 v13, v9, v7
	v_min_u32_e32 v7, v9, v7
	v_max_u32_e32 v9, v11, v6
	v_min_u32_e32 v6, v11, v6
	v_max_u32_e32 v11, v4, v0
	v_min_u32_e32 v0, v4, v0
	v_cmp_lt_i32_e32 vcc, -1, v122
	v_bitop3_b32 v4, v122, s28, v122 bitop3:0xc
	v_bitop3_b32 v49, v5, s28, v5 bitop3:0xc
	v_cndmask_b32_e64 v50, v104, -1, vcc
	v_cmp_lt_i32_e32 vcc, -1, v5
	v_bitop3_b32 v50, v50, v122, s29 bitop3:0x78
	s_nop 0
	v_cndmask_b32_e64 v51, v104, -1, vcc
	v_bitop3_b32 v5, v51, v5, s29 bitop3:0x78
	v_bitop3_b32 v51, v121, s28, v121 bitop3:0xc
	ds_write2st64_b32 v90, v4, v51 offset1:1
	v_bitop3_b32 v4, v3, s28, v3 bitop3:0xc
	v_cmp_lt_i32_e32 vcc, -1, v121
	ds_write2st64_b32 v90, v49, v4 offset0:16 offset1:17
	v_bitop3_b32 v51, v15, s28, v15 bitop3:0xc
	v_cndmask_b32_e64 v4, v104, -1, vcc
	v_cmp_lt_i32_e32 vcc, -1, v3
	v_bitop3_b32 v4, v4, v121, s29 bitop3:0x78
	s_nop 0
	v_cndmask_b32_e64 v49, v104, -1, vcc
	v_cmp_lt_i32_e32 vcc, -1, v120
	v_bitop3_b32 v3, v49, v3, s29 bitop3:0x78
	v_bitop3_b32 v49, v120, s28, v120 bitop3:0xc
	v_cndmask_b32_e64 v52, v104, -1, vcc
	v_cmp_lt_i32_e32 vcc, -1, v15
	v_bitop3_b32 v52, v52, v120, s29 bitop3:0x78
	s_nop 0
	v_cndmask_b32_e64 v53, v104, -1, vcc
	v_bitop3_b32 v15, v53, v15, s29 bitop3:0x78
	v_bitop3_b32 v53, v118, s28, v118 bitop3:0xc
	ds_write2st64_b32 v90, v49, v53 offset0:2 offset1:3
	v_bitop3_b32 v49, v2, s28, v2 bitop3:0xc
	v_cmp_lt_i32_e32 vcc, -1, v118
	ds_write2st64_b32 v90, v51, v49 offset0:18 offset1:19
	v_bitop3_b32 v53, v14, s28, v14 bitop3:0xc
	v_cndmask_b32_e64 v49, v104, -1, vcc
	v_cmp_lt_i32_e32 vcc, -1, v2
	v_bitop3_b32 v49, v49, v118, s29 bitop3:0x78
	s_nop 0
	v_cndmask_b32_e64 v51, v104, -1, vcc
	v_cmp_lt_i32_e32 vcc, -1, v117
	v_bitop3_b32 v2, v51, v2, s29 bitop3:0x78
	v_bitop3_b32 v51, v117, s28, v117 bitop3:0xc
	v_cndmask_b32_e64 v54, v104, -1, vcc
	v_cmp_lt_i32_e32 vcc, -1, v14
	v_bitop3_b32 v54, v54, v117, s29 bitop3:0x78
	s_nop 0
	v_cndmask_b32_e64 v55, v104, -1, vcc
	v_bitop3_b32 v14, v55, v14, s29 bitop3:0x78
	v_bitop3_b32 v55, v116, s28, v116 bitop3:0xc
	ds_write2st64_b32 v90, v51, v55 offset0:4 offset1:5
	v_bitop3_b32 v51, v10, s28, v10 bitop3:0xc
	v_cmp_lt_i32_e32 vcc, -1, v116
	ds_write2st64_b32 v90, v53, v51 offset0:20 offset1:21
	v_bitop3_b32 v55, v48, s28, v48 bitop3:0xc
	v_cndmask_b32_e64 v51, v104, -1, vcc
	v_cmp_lt_i32_e32 vcc, -1, v10
	v_bitop3_b32 v51, v51, v116, s29 bitop3:0x78
	s_nop 0
	v_cndmask_b32_e64 v53, v104, -1, vcc
	v_cmp_lt_i32_e32 vcc, -1, v115
	v_bitop3_b32 v10, v53, v10, s29 bitop3:0x78
	v_bitop3_b32 v53, v115, s28, v115 bitop3:0xc
	v_cndmask_b32_e64 v56, v104, -1, vcc
	v_cmp_lt_i32_e32 vcc, -1, v48
	v_bitop3_b32 v56, v56, v115, s29 bitop3:0x78
	s_nop 0
	v_cndmask_b32_e64 v57, v104, -1, vcc
	v_bitop3_b32 v48, v57, v48, s29 bitop3:0x78
	v_bitop3_b32 v57, v114, s28, v114 bitop3:0xc
	ds_write2st64_b32 v90, v53, v57 offset0:6 offset1:7
	v_bitop3_b32 v53, v1, s28, v1 bitop3:0xc
	v_cmp_lt_i32_e32 vcc, -1, v114
	ds_write2st64_b32 v90, v55, v53 offset0:22 offset1:23
; __device__ __forceinline__ unsigned f2ord(float f) { const unsigned u = __float_as_uint(f); return u ^ ((unsigned)((int)u >> 31) | 0x80000000u); }
; __device__ __forceinline__ void phase_topk(Frame& F, const bf16_t* QP, const bf16_t* K1B, const bf16_t* K2B, unsigned short* EID, float* GATE) {
;     ...
;         for (int a = 0; a < 16; ++a) { I1s[a * 64 + lane] = 127u - (V1[a] & 127u); I2s[a * 64 + lane] = 127u - (V2[a] & 127u); f1[a] = ord2f(V1[a] & ~127u); f2[a] = ord2f(V2[a] & ~127u); }
;         __builtin_amdgcn_sched_barrier(0);
;         unsigned Cd[64];
;     Cd[0] = (f2ord(f1[0] + f2[0]) & ~255u) | 255u;
;     Cd[1] = (f2ord(f1[0] + f2[1]) & ~255u) | 254u;
;     Cd[2] = (f2ord(f1[0] + f2[2]) & ~255u) | 253u;
;     Cd[3] = (f2ord(f1[0] + f2[3]) & ~255u) | 252u;
;     Cd[4] = (f2ord(f1[0] + f2[4]) & ~255u) | 251u;
;     Cd[5] = (f2ord(f1[0] + f2[5]) & ~255u) | 250u;
;     Cd[6] = (f2ord(f1[0] + f2[6]) & ~255u) | 249u;
;     Cd[7] = (f2ord(f1[0] + f2[7]) & ~255u) | 248u;
;     Cd[8] = (f2ord(f1[0] + f2[8]) & ~255u) | 247u;
;     Cd[9] = (f2ord(f1[0] + f2[9]) & ~255u) | 246u;
;     Cd[10] = (f2ord(f1[0] + f2[10]) & ~255u) | 245u;
;     Cd[11] = (f2ord(f1[0] + f2[11]) & ~255u) | 244u;
;     Cd[12] = (f2ord(f1[0] + f2[12]) & ~255u) | 243u;
;     Cd[13] = (f2ord(f1[0] + f2[13]) & ~255u) | 242u;
;     Cd[14] = (f2ord(f1[0] + f2[14]) & ~255u) | 241u;
;     Cd[15] = (f2ord(f1[0] + f2[15]) & ~255u) | 240u;
;     Cd[16] = (f2ord(f1[1] + f2[0]) & ~255u) | 239u;
;     Cd[17] = (f2ord(f1[1] + f2[1]) & ~255u) | 238u;
;     Cd[18] = (f2ord(f1[1] + f2[2]) & ~255u) | 237u;
;     Cd[19] = (f2ord(f1[1] + f2[3]) & ~255u) | 236u;
;     Cd[20] = (f2ord(f1[1] + f2[4]) & ~255u) | 235u;
;     Cd[21] = (f2ord(f1[1] + f2[5]) & ~255u) | 234u;
;     Cd[22] = (f2ord(f1[1] + f2[6]) & ~255u) | 233u;
;     Cd[23] = (f2ord(f1[1] + f2[7]) & ~255u) | 232u;
;     Cd[24] = (f2ord(f1[2] + f2[0]) & ~255u) | 223u;
;     Cd[25] = (f2ord(f1[2] + f2[1]) & ~255u) | 222u;
;     Cd[26] = (f2ord(f1[2] + f2[2]) & ~255u) | 221u;
;     Cd[27] = (f2ord(f1[2] + f2[3]) & ~255u) | 220u;
;     Cd[28] = (f2ord(f1[2] + f2[4]) & ~255u) | 219u;
;     Cd[29] = (f2ord(f1[3] + f2[0]) & ~255u) | 207u;
;     Cd[30] = (f2ord(f1[3] + f2[1]) & ~255u) | 206u;
;     Cd[31] = (f2ord(f1[3] + f2[2]) & ~255u) | 205u;
;     Cd[32] = (f2ord(f1[3] + f2[3]) & ~255u) | 204u;
	v_bitop3_b32 v57, v8, s28, v8 bitop3:0xc
	v_cndmask_b32_e64 v53, v104, -1, vcc
	v_cmp_lt_i32_e32 vcc, -1, v1
	v_bitop3_b32 v53, v53, v114, s29 bitop3:0x78
	s_nop 0
	v_cndmask_b32_e64 v55, v104, -1, vcc
	v_cmp_lt_i32_e32 vcc, -1, v113
	v_bitop3_b32 v1, v55, v1, s29 bitop3:0x78
	v_bitop3_b32 v55, v113, s28, v113 bitop3:0xc
	v_cndmask_b32_e64 v58, v104, -1, vcc
	v_cmp_lt_i32_e32 vcc, -1, v8
	v_bitop3_b32 v58, v58, v113, s29 bitop3:0x78
	s_nop 0
	v_cndmask_b32_e64 v59, v104, -1, vcc
	v_bitop3_b32 v8, v59, v8, s29 bitop3:0x78
	v_bitop3_b32 v59, v112, s28, v112 bitop3:0xc
	ds_write2st64_b32 v90, v55, v59 offset0:8 offset1:9
	v_bitop3_b32 v55, v12, s28, v12 bitop3:0xc
	v_cmp_lt_i32_e32 vcc, -1, v112
	ds_write2st64_b32 v90, v57, v55 offset0:24 offset1:25
	v_bitop3_b32 v59, v13, s28, v13 bitop3:0xc
	v_cndmask_b32_e64 v55, v104, -1, vcc
	v_cmp_lt_i32_e32 vcc, -1, v12
	v_bitop3_b32 v55, v55, v112, s29 bitop3:0x78
	s_nop 0
	v_cndmask_b32_e64 v57, v104, -1, vcc
	v_cmp_lt_i32_e32 vcc, -1, v111
	v_bitop3_b32 v12, v57, v12, s29 bitop3:0x78
	v_bitop3_b32 v57, v111, s28, v111 bitop3:0xc
	v_cndmask_b32_e64 v60, v104, -1, vcc
	v_cmp_lt_i32_e32 vcc, -1, v13
	v_bitop3_b32 v60, v60, v111, s29 bitop3:0x78
	s_nop 0
	v_cndmask_b32_e64 v61, v104, -1, vcc
	v_bitop3_b32 v13, v61, v13, s29 bitop3:0x78
	v_bitop3_b32 v61, v110, s28, v110 bitop3:0xc
	ds_write2st64_b32 v90, v57, v61 offset0:10 offset1:11
	v_bitop3_b32 v57, v7, s28, v7 bitop3:0xc
	v_cmp_lt_i32_e32 vcc, -1, v110
	ds_write2st64_b32 v90, v59, v57 offset0:26 offset1:27
	v_bitop3_b32 v61, v9, s28, v9 bitop3:0xc
	v_cndmask_b32_e64 v57, v104, -1, vcc
	v_cmp_lt_i32_e32 vcc, -1, v7
	v_bitop3_b32 v57, v57, v110, s29 bitop3:0x78
	s_nop 0
	v_cndmask_b32_e64 v59, v104, -1, vcc
	v_cmp_lt_i32_e32 vcc, -1, v109
	v_bitop3_b32 v7, v59, v7, s29 bitop3:0x78
	v_bitop3_b32 v59, v109, s28, v109 bitop3:0xc
	v_cndmask_b32_e64 v62, v104, -1, vcc
	v_cmp_lt_i32_e32 vcc, -1, v9
	v_bitop3_b32 v62, v62, v109, s29 bitop3:0x78
	s_nop 0
	v_cndmask_b32_e64 v63, v104, -1, vcc
	v_bitop3_b32 v9, v63, v9, s29 bitop3:0x78
	v_bitop3_b32 v63, v108, s28, v108 bitop3:0xc
	ds_write2st64_b32 v90, v59, v63 offset0:12 offset1:13
	v_bitop3_b32 v59, v6, s28, v6 bitop3:0xc
	v_cmp_lt_i32_e32 vcc, -1, v108
	ds_write2st64_b32 v90, v61, v59 offset0:28 offset1:29
	v_bitop3_b32 v63, v11, s28, v11 bitop3:0xc
	v_cndmask_b32_e64 v59, v104, -1, vcc
	v_cmp_lt_i32_e32 vcc, -1, v6
	v_bitop3_b32 v59, v59, v108, s29 bitop3:0x78
	s_nop 0
	v_cndmask_b32_e64 v61, v104, -1, vcc
	v_cmp_lt_i32_e32 vcc, -1, v107
	v_bitop3_b32 v6, v61, v6, s29 bitop3:0x78
	v_bitop3_b32 v61, v107, s28, v107 bitop3:0xc
	v_cndmask_b32_e64 v64, v104, -1, vcc
	v_cmp_lt_i32_e32 vcc, -1, v11
	v_bitop3_b32 v64, v64, v107, s29 bitop3:0x78
	s_nop 0
	v_cndmask_b32_e64 v65, v104, -1, vcc
	v_bitop3_b32 v11, v65, v11, s29 bitop3:0x78
	v_bitop3_b32 v65, v106, s28, v106 bitop3:0xc
	ds_write2st64_b32 v90, v61, v65 offset0:14 offset1:15
	v_bitop3_b32 v61, v0, s28, v0 bitop3:0xc
	v_cmp_lt_i32_e32 vcc, -1, v106
	ds_write2st64_b32 v90, v63, v61 offset0:30 offset1:31
	s_nop 0
	v_cndmask_b32_e64 v61, v104, -1, vcc
	v_cmp_lt_i32_e32 vcc, -1, v0
	v_bitop3_b32 v61, v61, v106, s29 bitop3:0x78
	s_nop 0
	v_cndmask_b32_e64 v63, v104, -1, vcc
	v_bitop3_b32 v0, v63, v0, s29 bitop3:0x78
	v_add_f32_e32 v63, v50, v5
	v_ashrrev_i32_e32 v65, 31, v63
	v_or_b32_e32 v65, 0x80000000, v65
	v_bitop3_b32 v63, v65, s30, v63 bitop3:0xde
	v_add_f32_e32 v65, v50, v3
	v_ashrrev_i32_e32 v66, 31, v65
	v_or_b32_e32 v66, 0x80000000, v66
	v_bitop3_b32 v65, v66, s9, v65 bitop3:0x48
	v_add_f32_e32 v66, v50, v15
	v_ashrrev_i32_e32 v67, 31, v66
	v_or_b32_e32 v67, 0x80000000, v67
	v_bitop3_b32 v66, v67, s9, v66 bitop3:0x48
	v_add_f32_e32 v67, v50, v2
	v_ashrrev_i32_e32 v68, 31, v67
	v_or_b32_e32 v68, 0x80000000, v68
	v_bitop3_b32 v67, v68, s9, v67 bitop3:0x48
	v_add_f32_e32 v68, v50, v14
	v_ashrrev_i32_e32 v69, 31, v68
	v_or_b32_e32 v69, 0x80000000, v69
	v_bitop3_b32 v68, v69, s9, v68 bitop3:0x48
	v_add_f32_e32 v69, v50, v10
	v_ashrrev_i32_e32 v70, 31, v69
	v_or_b32_e32 v70, 0x80000000, v70
	v_bitop3_b32 v69, v70, s9, v69 bitop3:0x48
	v_add_f32_e32 v70, v50, v48
	v_ashrrev_i32_e32 v71, 31, v70
	v_or_b32_e32 v71, 0x80000000, v71
	v_bitop3_b32 v70, v71, s9, v70 bitop3:0x48
	v_add_f32_e32 v71, v50, v1
	v_ashrrev_i32_e32 v72, 31, v71
	v_or_b32_e32 v72, 0x80000000, v72
	v_add_f32_e32 v8, v50, v8
	v_bitop3_b32 v71, v72, s9, v71 bitop3:0x48
	v_ashrrev_i32_e32 v72, 31, v8
	v_or_b32_e32 v72, 0x80000000, v72
	v_add_f32_e32 v12, v50, v12
	v_bitop3_b32 v8, v72, s9, v8 bitop3:0x48
	v_ashrrev_i32_e32 v72, 31, v12
	v_or_b32_e32 v72, 0x80000000, v72
	v_add_f32_e32 v13, v50, v13
	v_bitop3_b32 v12, v72, s9, v12 bitop3:0x48
	v_ashrrev_i32_e32 v72, 31, v13
	v_or_b32_e32 v72, 0x80000000, v72
	v_add_f32_e32 v7, v50, v7
	v_bitop3_b32 v13, v72, s9, v13 bitop3:0x48
	v_ashrrev_i32_e32 v72, 31, v7
	v_or_b32_e32 v72, 0x80000000, v72
	v_add_f32_e32 v9, v50, v9
	v_bitop3_b32 v7, v72, s9, v7 bitop3:0x48
	v_ashrrev_i32_e32 v72, 31, v9
	v_or_b32_e32 v72, 0x80000000, v72
	v_add_f32_e32 v6, v50, v6
	v_bitop3_b32 v9, v72, s9, v9 bitop3:0x48
	v_ashrrev_i32_e32 v72, 31, v6
	v_add_f32_e32 v0, v50, v0
	v_or_b32_e32 v72, 0x80000000, v72
	v_add_f32_e32 v11, v50, v11
	v_ashrrev_i32_e32 v50, 31, v0
	v_bitop3_b32 v6, v72, s9, v6 bitop3:0x48
	v_ashrrev_i32_e32 v72, 31, v11
	v_or_b32_e32 v50, 0x80000000, v50
	v_or_b32_e32 v72, 0x80000000, v72
	v_bitop3_b32 v0, v50, s9, v0 bitop3:0x48
	v_add_f32_e32 v50, v4, v5
	v_bitop3_b32 v11, v72, s9, v11 bitop3:0x48
	v_ashrrev_i32_e32 v72, 31, v50
	v_or_b32_e32 v72, 0x80000000, v72
	v_bitop3_b32 v50, v72, s9, v50 bitop3:0x48
	v_add_f32_e32 v72, v4, v3
; __device__ __forceinline__ void phase_topk(Frame& F, const bf16_t* QP, const bf16_t* K1B, const bf16_t* K2B, unsigned short* EID, float* GATE) {
;     ...
;     Cd[0] = (f2ord(f1[0] + f2[0]) & ~255u) | 255u;
;     Cd[1] = (f2ord(f1[0] + f2[1]) & ~255u) | 254u;
;     Cd[2] = (f2ord(f1[0] + f2[2]) & ~255u) | 253u;
;     Cd[3] = (f2ord(f1[0] + f2[3]) & ~255u) | 252u;
;     Cd[4] = (f2ord(f1[0] + f2[4]) & ~255u) | 251u;
;     Cd[5] = (f2ord(f1[0] + f2[5]) & ~255u) | 250u;
;     Cd[6] = (f2ord(f1[0] + f2[6]) & ~255u) | 249u;
;     Cd[7] = (f2ord(f1[0] + f2[7]) & ~255u) | 248u;
;     Cd[8] = (f2ord(f1[0] + f2[8]) & ~255u) | 247u;
;     Cd[9] = (f2ord(f1[0] + f2[9]) & ~255u) | 246u;
;     Cd[10] = (f2ord(f1[0] + f2[10]) & ~255u) | 245u;
;     Cd[11] = (f2ord(f1[0] + f2[11]) & ~255u) | 244u;
;     Cd[12] = (f2ord(f1[0] + f2[12]) & ~255u) | 243u;
;     Cd[13] = (f2ord(f1[0] + f2[13]) & ~255u) | 242u;
;     Cd[14] = (f2ord(f1[0] + f2[14]) & ~255u) | 241u;
;     Cd[15] = (f2ord(f1[0] + f2[15]) & ~255u) | 240u;
;     Cd[16] = (f2ord(f1[1] + f2[0]) & ~255u) | 239u;
;     Cd[17] = (f2ord(f1[1] + f2[1]) & ~255u) | 238u;
;     Cd[18] = (f2ord(f1[1] + f2[2]) & ~255u) | 237u;
;     Cd[19] = (f2ord(f1[1] + f2[3]) & ~255u) | 236u;
;     Cd[20] = (f2ord(f1[1] + f2[4]) & ~255u) | 235u;
;     Cd[21] = (f2ord(f1[1] + f2[5]) & ~255u) | 234u;
;     Cd[22] = (f2ord(f1[1] + f2[6]) & ~255u) | 233u;
;     Cd[23] = (f2ord(f1[1] + f2[7]) & ~255u) | 232u;
;     Cd[24] = (f2ord(f1[2] + f2[0]) & ~255u) | 223u;
;     Cd[25] = (f2ord(f1[2] + f2[1]) & ~255u) | 222u;
;     Cd[26] = (f2ord(f1[2] + f2[2]) & ~255u) | 221u;
;     Cd[27] = (f2ord(f1[2] + f2[3]) & ~255u) | 220u;
;     Cd[28] = (f2ord(f1[2] + f2[4]) & ~255u) | 219u;
;     Cd[29] = (f2ord(f1[3] + f2[0]) & ~255u) | 207u;
;     Cd[30] = (f2ord(f1[3] + f2[1]) & ~255u) | 206u;
;     Cd[31] = (f2ord(f1[3] + f2[2]) & ~255u) | 205u;
;     Cd[32] = (f2ord(f1[3] + f2[3]) & ~255u) | 204u;
;     Cd[33] = (f2ord(f1[4] + f2[0]) & ~255u) | 191u;
;     Cd[34] = (f2ord(f1[4] + f2[1]) & ~255u) | 190u;
;     Cd[35] = (f2ord(f1[4] + f2[2]) & ~255u) | 189u;
;     Cd[36] = (f2ord(f1[5] + f2[0]) & ~255u) | 175u;
;     Cd[37] = (f2ord(f1[5] + f2[1]) & ~255u) | 174u;
;     Cd[38] = (f2ord(f1[6] + f2[0]) & ~255u) | 159u;
;     Cd[39] = (f2ord(f1[6] + f2[1]) & ~255u) | 158u;
;     Cd[40] = (f2ord(f1[7] + f2[0]) & ~255u) | 143u;
	v_ashrrev_i32_e32 v73, 31, v72
	v_or_b32_e32 v73, 0x80000000, v73
	v_bitop3_b32 v72, v73, s9, v72 bitop3:0x48
	v_add_f32_e32 v73, v4, v15
	v_ashrrev_i32_e32 v74, 31, v73
	v_or_b32_e32 v74, 0x80000000, v74
	v_bitop3_b32 v73, v74, s9, v73 bitop3:0x48
	v_add_f32_e32 v74, v4, v2
	v_ashrrev_i32_e32 v75, 31, v74
	v_or_b32_e32 v75, 0x80000000, v75
	v_bitop3_b32 v74, v75, s9, v74 bitop3:0x48
	v_add_f32_e32 v75, v4, v14
	v_ashrrev_i32_e32 v76, 31, v75
	v_or_b32_e32 v76, 0x80000000, v76
	v_add_f32_e32 v10, v4, v10
	v_bitop3_b32 v75, v76, s9, v75 bitop3:0x48
	v_ashrrev_i32_e32 v76, 31, v10
	v_add_f32_e32 v1, v4, v1
	v_or_b32_e32 v76, 0x80000000, v76
	v_add_f32_e32 v48, v4, v48
	v_ashrrev_i32_e32 v4, 31, v1
	v_bitop3_b32 v10, v76, s9, v10 bitop3:0x48
	v_ashrrev_i32_e32 v76, 31, v48
	v_or_b32_e32 v4, 0x80000000, v4
	v_or_b32_e32 v76, 0x80000000, v76
	v_bitop3_b32 v1, v4, s9, v1 bitop3:0x48
	v_add_f32_e32 v4, v52, v5
	v_bitop3_b32 v48, v76, s9, v48 bitop3:0x48
	v_ashrrev_i32_e32 v76, 31, v4
	v_or_b32_e32 v76, 0x80000000, v76
	v_bitop3_b32 v4, v76, s9, v4 bitop3:0x48
	v_add_f32_e32 v76, v52, v3
	v_ashrrev_i32_e32 v77, 31, v76
	v_or_b32_e32 v77, 0x80000000, v77
	v_bitop3_b32 v76, v77, s9, v76 bitop3:0x48
	v_add_f32_e32 v77, v52, v15
	v_ashrrev_i32_e32 v78, 31, v77
	v_or_b32_e32 v78, 0x80000000, v78
	v_add_f32_e32 v14, v52, v14
	v_bitop3_b32 v77, v78, s9, v77 bitop3:0x48
	v_add_f32_e32 v78, v52, v2
	v_ashrrev_i32_e32 v52, 31, v14
	v_ashrrev_i32_e32 v79, 31, v78
	v_or_b32_e32 v52, 0x80000000, v52
	v_or_b32_e32 v79, 0x80000000, v79
	v_bitop3_b32 v14, v52, s9, v14 bitop3:0x48
	v_add_f32_e32 v52, v49, v5
	v_bitop3_b32 v78, v79, s9, v78 bitop3:0x48
	v_ashrrev_i32_e32 v79, 31, v52
	v_or_b32_e32 v79, 0x80000000, v79
	v_bitop3_b32 v52, v79, s9, v52 bitop3:0x48
	v_add_f32_e32 v79, v49, v3
	v_ashrrev_i32_e32 v105, 31, v79
	v_or_b32_e32 v105, 0x80000000, v105
	v_add_f32_e32 v2, v49, v2
	v_bitop3_b32 v79, v105, s9, v79 bitop3:0x48
	v_add_f32_e32 v105, v49, v15
	v_ashrrev_i32_e32 v49, 31, v2
	v_ashrrev_i32_e32 v106, 31, v105
	v_or_b32_e32 v49, 0x80000000, v49
	v_or_b32_e32 v106, 0x80000000, v106
	v_bitop3_b32 v2, v49, s9, v2 bitop3:0x48
	v_add_f32_e32 v49, v54, v5
	v_bitop3_b32 v105, v106, s9, v105 bitop3:0x48
	v_ashrrev_i32_e32 v106, 31, v49
	v_or_b32_e32 v106, 0x80000000, v106
	v_add_f32_e32 v15, v54, v15
	v_bitop3_b32 v49, v106, s9, v49 bitop3:0x48
	v_add_f32_e32 v106, v54, v3
	v_ashrrev_i32_e32 v54, 31, v15
	v_ashrrev_i32_e32 v107, 31, v106
	v_or_b32_e32 v54, 0x80000000, v54
	v_or_b32_e32 v107, 0x80000000, v107
	v_bitop3_b32 v15, v54, s9, v15 bitop3:0x48
	v_add_f32_e32 v54, v51, v5
	v_bitop3_b32 v106, v107, s9, v106 bitop3:0x48
	v_ashrrev_i32_e32 v107, 31, v54
	v_or_b32_e32 v107, 0x80000000, v107
	v_add_f32_e32 v51, v51, v3
	v_bitop3_b32 v54, v107, s9, v54 bitop3:0x48
	v_ashrrev_i32_e32 v107, 31, v51
	v_or_b32_e32 v107, 0x80000000, v107
	v_bitop3_b32 v51, v107, s9, v51 bitop3:0x48
	v_add_f32_e32 v107, v56, v5
	v_ashrrev_i32_e32 v108, 31, v107
	v_or_b32_e32 v108, 0x80000000, v108
	v_add_f32_e32 v56, v56, v3
	v_bitop3_b32 v107, v108, s9, v107 bitop3:0x48
	v_ashrrev_i32_e32 v108, 31, v56
	v_or_b32_e32 v108, 0x80000000, v108
	v_add_f32_e32 v3, v53, v3
	v_bitop3_b32 v56, v108, s9, v56 bitop3:0x48
	v_add_f32_e32 v108, v53, v5
	v_ashrrev_i32_e32 v53, 31, v3
	v_or_b32_e32 v53, 0x80000000, v53
	v_bitop3_b32 v3, v53, s9, v3 bitop3:0x48
	v_add_f32_e32 v53, v58, v5
	v_ashrrev_i32_e32 v58, 31, v53
	v_or_b32_e32 v58, 0x80000000, v58
	v_add_f32_e32 v55, v55, v5
	v_bitop3_b32 v53, v58, s9, v53 bitop3:0x48
	v_ashrrev_i32_e32 v58, 31, v55
	v_or_b32_e32 v58, 0x80000000, v58
	v_bitop3_b32 v55, v58, s9, v55 bitop3:0x48
	v_add_f32_e32 v58, v60, v5
	v_ashrrev_i32_e32 v60, 31, v58
	v_or_b32_e32 v60, 0x80000000, v60
	v_add_f32_e32 v57, v57, v5
	v_bitop3_b32 v58, v60, s9, v58 bitop3:0x48
	v_ashrrev_i32_e32 v60, 31, v57
	v_or_b32_e32 v60, 0x80000000, v60
	v_bitop3_b32 v57, v60, s9, v57 bitop3:0x48
	v_add_f32_e32 v60, v62, v5
	v_ashrrev_i32_e32 v62, 31, v60
	v_add_f32_e32 v59, v59, v5
	v_bitop3_b32 v60, v62, v60, s11 bitop3:0x36
	v_ashrrev_i32_e32 v62, 31, v59
	v_ashrrev_i32_e32 v109, 31, v108
	v_bitop3_b32 v59, v62, v59, s11 bitop3:0x36
	v_add_f32_e32 v62, v64, v5
	v_add_f32_e32 v5, v61, v5
	v_or_b32_e32 v109, 0x80000000, v109
	v_ashrrev_i32_e32 v64, 31, v62
	v_ashrrev_i32_e32 v61, 31, v5
	v_bitop3_b32 v108, v109, s9, v108 bitop3:0x48
	v_bitop3_b32 v62, v64, v62, s11 bitop3:0x36
	v_bitop3_b32 v5, v61, v5, s11 bitop3:0x36
	v_or_b32_e32 v65, 0xfe, v65
	v_or_b32_e32 v66, 0xfd, v66
	v_or_b32_e32 v67, 0xfc, v67
	v_or_b32_e32 v68, 0xfb, v68
	v_or_b32_e32 v69, 0xfa, v69
	v_or_b32_e32 v70, 0xf9, v70
	v_or_b32_e32 v71, 0xf8, v71
	v_or_b32_e32 v8, 0xf7, v8
	v_or_b32_e32 v12, 0xf6, v12
	v_or_b32_e32 v13, 0xf5, v13
	v_or_b32_e32 v7, 0xf4, v7
	v_or_b32_e32 v9, 0xf3, v9
	v_or_b32_e32 v6, 0xf2, v6
	v_or_b32_e32 v11, 0xf1, v11
	v_or_b32_e32 v0, 0xf0, v0
	v_or_b32_e32 v50, 0xef, v50
	v_or_b32_e32 v72, 0xee, v72
	v_or_b32_e32 v73, 0xed, v73
	v_or_b32_e32 v74, 0xec, v74
	v_or_b32_e32 v75, 0xeb, v75
	v_or_b32_e32 v10, 0xea, v10
	v_or_b32_e32 v48, 0xe9, v48
	v_or_b32_e32 v1, 0xe8, v1
	v_or_b32_e32 v4, 0xdf, v4
	v_or_b32_e32 v76, 0xde, v76
	v_or_b32_e32 v77, 0xdd, v77
	v_or_b32_e32 v78, 0xdc, v78
	v_or_b32_e32 v14, 0xdb, v14
	v_or_b32_e32 v52, 0xcf, v52
	v_or_b32_e32 v79, 0xce, v79
	v_or_b32_e32 v105, 0xcd, v105
	v_or_b32_e32 v2, 0xcc, v2
	v_or_b32_e32 v49, 0xbf, v49
	v_or_b32_e32 v106, 0xbe, v106
	v_or_b32_e32 v15, 0xbd, v15
	v_or_b32_e32 v54, 0xaf, v54
	v_or_b32_e32 v51, 0xae, v51
	v_or_b32_e32 v107, 0x9f, v107
	v_or_b32_e32 v56, 0x9e, v56
	v_or_b32_e32 v108, 0x8f, v108
	v_or_b32_e32 v3, 0x8e, v3
; __device__ __forceinline__ unsigned f2ord(float f) { const unsigned u = __float_as_uint(f); return u ^ ((unsigned)((int)u >> 31) | 0x80000000u); }
; template <int OFF, int TOT> DEVFN void sort16_desc(unsigned (&a)[TOT]) {
; #pragma unroll
;     for (int q = 0; q < OE16_N; ++q) { const int i = OFF + OE16[q][0], l = OFF + OE16[q][1]; const unsigned x = a[i], y = a[l]; a[i] = x > y ? x : y; a[l] = x > y ? y : x; }
; }
; template <int OFF, int TOT> DEVFN void bitonic_merge16_desc(unsigned (&a)[TOT]) {
; #pragma unroll
;     for (int j = 8; j > 0; j >>= 1)
; #pragma unroll
;         for (int i = 0; i < 16; ++i) { const int l = i ^ j; if (l > i) { const unsigned x = a[OFF + i], y = a[OFF + l]; a[OFF + i] = x > y ? x : y; a[OFF + l] = x > y ? y : x; } }
; }
; template <int A, int B, int TOT> DEVFN void merge_top16(unsigned (&a)[TOT]) {
; #pragma unroll
;     for (int i = 0; i < 16; ++i) { const unsigned x = a[A + i], y = a[B + 15 - i]; a[A + i] = x > y ? x : y; }
;     bitonic_merge16_desc<A, TOT>(a);
; }
; DEVFN void top16of64(unsigned (&a)[64]) {
;     sort16_desc<0, 64>(a); sort16_desc<16, 64>(a); sort16_desc<32, 64>(a); sort16_desc<48, 64>(a);
;     merge_top16<0, 16, 64>(a); merge_top16<32, 48, 64>(a); merge_top16<0, 32, 64>(a);
; }
; __device__ __forceinline__ void phase_topk(Frame& F, const bf16_t* QP, const bf16_t* K1B, const bf16_t* K2B, unsigned short* EID, float* GATE) {
;     ...
;     Cd[42] = (f2ord(f1[8] + f2[0]) & ~255u) | 127u;
;     Cd[43] = (f2ord(f1[9] + f2[0]) & ~255u) | 111u;
;     Cd[44] = (f2ord(f1[10] + f2[0]) & ~255u) | 95u;
;     Cd[45] = (f2ord(f1[11] + f2[0]) & ~255u) | 79u;
;     Cd[46] = (f2ord(f1[12] + f2[0]) & ~255u) | 63u;
;     Cd[47] = (f2ord(f1[13] + f2[0]) & ~255u) | 47u;
;     Cd[48] = (f2ord(f1[14] + f2[0]) & ~255u) | 31u;
;     Cd[49] = (f2ord(f1[15] + f2[0]) & ~255u) | 15u;
;     Cd[50] = 0u;
;     Cd[51] = 0u;
;     Cd[52] = 0u;
;     Cd[53] = 0u;
;     Cd[54] = 0u;
;     Cd[55] = 0u;
;     Cd[56] = 0u;
;     Cd[57] = 0u;
;     Cd[58] = 0u;
;     Cd[59] = 0u;
;     Cd[60] = 0u;
;     Cd[61] = 0u;
;     Cd[62] = 0u;
;     Cd[63] = 0u;
	v_or_b32_e32 v53, 0x7f, v53
	v_or_b32_e32 v55, 0x6f, v55
	v_or_b32_e32 v58, 0x5f, v58
	v_or_b32_e32 v57, 0x4f, v57
	v_and_or_b32 v60, v60, s9, 63
	v_and_or_b32 v59, v59, s9, 47
	v_and_or_b32 v62, v62, s9, 31
	v_and_or_b32 v5, v5, s9, 15
	v_max_u32_e32 v61, v63, v65
	v_min_u32_e32 v63, v63, v65
	v_max_u32_e32 v64, v66, v67
	v_min_u32_e32 v65, v66, v67
	v_max_u32_e32 v115, v50, v72
	v_min_u32_e32 v50, v50, v72
	v_max_u32_e32 v72, v73, v74
	v_min_u32_e32 v73, v73, v74
	v_max_u32_e32 v123, v2, v49
	v_min_u32_e32 v2, v2, v49
	v_max_u32_e32 v49, v106, v15
	v_min_u32_e32 v15, v106, v15
	v_max_u32_e32 v66, v61, v64
	v_min_u32_e32 v61, v61, v64
	v_max_u32_e32 v64, v63, v65
	v_max_u32_e32 v74, v115, v72
	v_min_u32_e32 v72, v115, v72
	v_max_u32_e32 v115, v50, v73
	v_max_u32_e32 v106, v123, v49
	v_min_u32_e32 v49, v123, v49
	v_max_u32_e32 v123, v2, v15
	v_min_u32_e32 v63, v63, v65
	v_max_u32_e32 v65, v64, v61
	v_min_u32_e32 v61, v64, v61
	v_max_u32_e32 v64, v68, v69
	v_min_u32_e32 v67, v68, v69
	v_max_u32_e32 v68, v70, v71
	v_min_u32_e32 v69, v70, v71
	v_min_u32_e32 v50, v50, v73
	v_max_u32_e32 v73, v115, v72
	v_min_u32_e32 v72, v115, v72
	v_max_u32_e32 v115, v75, v10
	v_min_u32_e32 v10, v75, v10
	v_max_u32_e32 v75, v48, v1
	v_min_u32_e32 v1, v48, v1
	v_min_u32_e32 v2, v2, v15
	v_max_u32_e32 v15, v123, v49
	v_min_u32_e32 v49, v123, v49
	v_max_u32_e32 v123, v54, v51
	v_min_u32_e32 v51, v54, v51
	v_max_u32_e32 v54, v107, v56
	v_min_u32_e32 v56, v107, v56
	v_max_u32_e32 v70, v64, v68
	v_min_u32_e32 v64, v64, v68
	v_max_u32_e32 v68, v67, v69
	v_max_u32_e32 v48, v115, v75
	v_min_u32_e32 v75, v115, v75
	v_max_u32_e32 v115, v10, v1
	v_max_u32_e32 v107, v123, v54
	v_min_u32_e32 v54, v123, v54
	v_max_u32_e32 v123, v51, v56
	v_min_u32_e32 v67, v67, v69
	v_max_u32_e32 v69, v68, v64
	v_min_u32_e32 v64, v68, v64
	v_min_u32_e32 v1, v10, v1
	v_max_u32_e32 v10, v115, v75
	v_min_u32_e32 v75, v115, v75
	v_min_u32_e32 v51, v51, v56
	v_max_u32_e32 v56, v123, v54
	v_min_u32_e32 v54, v123, v54
	v_max_u32_e32 v68, v66, v70
	v_min_u32_e32 v66, v66, v70
	v_max_u32_e32 v70, v61, v64
	v_max_u32_e32 v115, v74, v48
	v_min_u32_e32 v48, v74, v48
	v_max_u32_e32 v74, v72, v75
	v_max_u32_e32 v123, v106, v107
	v_min_u32_e32 v106, v106, v107
	v_max_u32_e32 v107, v49, v54
	v_min_u32_e32 v61, v61, v64
	v_max_u32_e32 v64, v70, v66
	v_min_u32_e32 v66, v70, v66
	v_max_u32_e32 v70, v65, v69
	v_min_u32_e32 v65, v65, v69
	v_max_u32_e32 v69, v63, v67
	v_min_u32_e32 v72, v72, v75
	v_max_u32_e32 v75, v74, v48
	v_min_u32_e32 v48, v74, v48
	v_max_u32_e32 v74, v73, v10
	v_min_u32_e32 v10, v73, v10
	v_max_u32_e32 v73, v50, v1
	v_min_u32_e32 v49, v49, v54
	v_max_u32_e32 v54, v107, v106
	v_min_u32_e32 v106, v107, v106
	v_max_u32_e32 v107, v15, v56
	v_min_u32_e32 v15, v15, v56
	v_max_u32_e32 v56, v2, v51
	v_min_u32_e32 v63, v63, v67
	v_max_u32_e32 v67, v69, v65
	v_min_u32_e32 v65, v69, v65
	v_min_u32_e32 v1, v50, v1
	v_max_u32_e32 v50, v73, v10
	v_min_u32_e32 v10, v73, v10
	v_min_u32_e32 v2, v2, v51
	v_max_u32_e32 v51, v56, v15
	v_min_u32_e32 v15, v56, v15
	v_max_u32_e32 v69, v70, v64
	v_min_u32_e32 v64, v70, v64
	v_max_u32_e32 v70, v67, v66
	v_min_u32_e32 v66, v67, v66
	v_max_u32_e32 v67, v65, v61
	v_min_u32_e32 v61, v65, v61
	v_max_u32_e32 v65, v8, v12
	v_min_u32_e32 v8, v8, v12
	v_max_u32_e32 v12, v13, v7
	v_min_u32_e32 v7, v13, v7
	v_max_u32_e32 v73, v74, v75
	v_min_u32_e32 v74, v74, v75
	v_max_u32_e32 v75, v50, v48
	v_min_u32_e32 v48, v50, v48
	v_max_u32_e32 v50, v10, v72
	v_min_u32_e32 v10, v10, v72
	v_max_u32_e32 v72, v4, v76
	v_min_u32_e32 v4, v4, v76
	v_max_u32_e32 v76, v77, v78
	v_min_u32_e32 v77, v77, v78
	v_max_u32_e32 v56, v107, v54
	v_min_u32_e32 v54, v107, v54
	v_max_u32_e32 v107, v51, v106
	v_min_u32_e32 v51, v51, v106
	v_max_u32_e32 v106, v15, v49
	v_min_u32_e32 v15, v15, v49
	v_max_u32_e32 v49, v108, v3
	v_min_u32_e32 v3, v108, v3
	v_max_u32_e32 v108, v53, v55
	v_min_u32_e32 v53, v53, v55
	v_max_u32_e32 v13, v65, v12
	v_min_u32_e32 v12, v65, v12
	v_max_u32_e32 v65, v8, v7
	v_max_u32_e32 v78, v72, v76
	v_min_u32_e32 v72, v72, v76
	v_max_u32_e32 v76, v4, v77
	v_max_u32_e32 v55, v49, v108
	v_min_u32_e32 v49, v49, v108
	v_max_u32_e32 v108, v3, v53
	v_min_u32_e32 v7, v8, v7
	v_max_u32_e32 v8, v65, v12
	v_min_u32_e32 v12, v65, v12
	v_max_u32_e32 v65, v9, v6
	v_min_u32_e32 v6, v9, v6
	v_max_u32_e32 v9, v11, v0
	v_min_u32_e32 v0, v11, v0
	v_min_u32_e32 v4, v4, v77
	v_max_u32_e32 v77, v76, v72
	v_min_u32_e32 v72, v76, v72
	v_max_u32_e32 v76, v14, v52
	v_min_u32_e32 v14, v14, v52
	v_max_u32_e32 v52, v79, v105
	v_min_u32_e32 v79, v79, v105
	v_min_u32_e32 v3, v3, v53
	v_max_u32_e32 v53, v108, v49
	v_min_u32_e32 v49, v108, v49
	v_max_u32_e32 v108, v58, v57
	v_min_u32_e32 v57, v58, v57
	v_max_u32_e32 v58, v60, v59
	v_min_u32_e32 v59, v60, v59
	v_max_u32_e32 v11, v65, v9
	v_min_u32_e32 v9, v65, v9
	v_max_u32_e32 v65, v6, v0
	v_max_u32_e32 v105, v76, v52
	v_min_u32_e32 v52, v76, v52
	v_max_u32_e32 v76, v14, v79
	v_max_u32_e32 v60, v108, v58
	v_min_u32_e32 v58, v108, v58
	v_max_u32_e32 v108, v57, v59
	v_min_u32_e32 v0, v6, v0
	v_max_u32_e32 v6, v65, v9
	v_min_u32_e32 v9, v65, v9
	v_min_u32_e32 v14, v14, v79
	v_max_u32_e32 v79, v76, v52
	v_min_u32_e32 v52, v76, v52
	v_min_u32_e32 v57, v57, v59
	v_max_u32_e32 v59, v108, v58
	v_min_u32_e32 v58, v108, v58
	v_max_u32_e32 v65, v13, v11
	v_min_u32_e32 v11, v13, v11
	v_max_u32_e32 v13, v12, v9
	v_max_u32_e32 v76, v78, v105
	v_min_u32_e32 v78, v78, v105
	v_max_u32_e32 v105, v72, v52
	v_max_u32_e32 v108, v55, v60
	v_min_u32_e32 v55, v55, v60
	v_max_u32_e32 v60, v49, v58
	v_min_u32_e32 v9, v12, v9
	v_max_u32_e32 v12, v13, v11
	v_min_u32_e32 v11, v13, v11
; template <int OFF, int TOT> DEVFN void sort16_desc(unsigned (&a)[TOT]) {
; #pragma unroll
;     for (int q = 0; q < OE16_N; ++q) { const int i = OFF + OE16[q][0], l = OFF + OE16[q][1]; const unsigned x = a[i], y = a[l]; a[i] = x > y ? x : y; a[l] = x > y ? y : x; }
; }
; template <int OFF, int TOT> DEVFN void bitonic_merge16_desc(unsigned (&a)[TOT]) {
; #pragma unroll
;     for (int j = 8; j > 0; j >>= 1)
; #pragma unroll
;         for (int i = 0; i < 16; ++i) { const int l = i ^ j; if (l > i) { const unsigned x = a[OFF + i], y = a[OFF + l]; a[OFF + i] = x > y ? x : y; a[OFF + l] = x > y ? y : x; } }
; }
; template <int A, int B, int TOT> DEVFN void merge_top16(unsigned (&a)[TOT]) {
; #pragma unroll
;     for (int i = 0; i < 16; ++i) { const unsigned x = a[A + i], y = a[B + 15 - i]; a[A + i] = x > y ? x : y; }
;     bitonic_merge16_desc<A, TOT>(a);
; }
; DEVFN void top16of64(unsigned (&a)[64]) {
;     sort16_desc<0, 64>(a); sort16_desc<16, 64>(a); sort16_desc<32, 64>(a); sort16_desc<48, 64>(a);
;     merge_top16<0, 16, 64>(a); merge_top16<32, 48, 64>(a); merge_top16<0, 32, 64>(a);
; }
	v_max_u32_e32 v13, v8, v6
	v_min_u32_e32 v6, v8, v6
	v_max_u32_e32 v8, v7, v0
	v_min_u32_e32 v52, v72, v52
	v_max_u32_e32 v72, v105, v78
	v_min_u32_e32 v78, v105, v78
	v_max_u32_e32 v105, v77, v79
	v_min_u32_e32 v77, v77, v79
	v_max_u32_e32 v79, v4, v14
	v_min_u32_e32 v49, v49, v58
	v_max_u32_e32 v58, v60, v55
	v_min_u32_e32 v55, v60, v55
	v_max_u32_e32 v60, v53, v59
	v_min_u32_e32 v53, v53, v59
	v_max_u32_e32 v59, v3, v57
	v_min_u32_e32 v0, v7, v0
	v_max_u32_e32 v7, v8, v6
	v_min_u32_e32 v4, v4, v14
	v_max_u32_e32 v14, v79, v77
	v_min_u32_e32 v3, v3, v57
	v_max_u32_e32 v57, v59, v53
	v_min_u32_e32 v6, v8, v6
	v_max_u32_e32 v8, v13, v12
	v_min_u32_e32 v12, v13, v12
	v_max_u32_e32 v13, v7, v11
	v_min_u32_e32 v7, v7, v11
	v_min_u32_e32 v77, v79, v77
	v_max_u32_e32 v79, v105, v72
	v_min_u32_e32 v72, v105, v72
	v_max_u32_e32 v105, v14, v78
	v_min_u32_e32 v14, v14, v78
	v_min_u32_e32 v53, v59, v53
	v_max_u32_e32 v59, v60, v58
	v_min_u32_e32 v58, v60, v58
	v_max_u32_e32 v60, v57, v55
	v_min_u32_e32 v55, v57, v55
	v_max_u32_e32 v11, v6, v9
	v_min_u32_e32 v6, v6, v9
	v_min_u32_e32 v9, v68, v65
	v_max_u32_e32 v71, v66, v7
	v_max_u32_e32 v78, v77, v52
	v_min_u32_e32 v52, v77, v52
	v_min_u32_e32 v77, v115, v76
	v_max_u32_e32 v116, v48, v14
	v_max_u32_e32 v57, v53, v49
	v_min_u32_e32 v49, v53, v49
	v_max_u32_e32 v53, v123, v108
	v_min_u32_e32 v108, v123, v108
	v_max_u32_e32 v123, v51, v55
	v_min_u32_e32 v7, v66, v7
	v_max_u32_e32 v66, v71, v9
	v_min_u32_e32 v9, v71, v9
	v_max_u32_e32 v71, v64, v12
	v_min_u32_e32 v12, v64, v12
	v_max_u32_e32 v64, v61, v6
	v_min_u32_e32 v14, v48, v14
	v_max_u32_e32 v48, v116, v77
	v_min_u32_e32 v77, v116, v77
	v_max_u32_e32 v116, v74, v72
	v_min_u32_e32 v72, v74, v72
	v_max_u32_e32 v74, v10, v52
	v_min_u32_e32 v51, v51, v55
	v_max_u32_e32 v55, v123, v108
	v_min_u32_e32 v108, v123, v108
	v_max_u32_e32 v123, v54, v58
	v_min_u32_e32 v54, v54, v58
	v_max_u32_e32 v58, v15, v49
	v_min_u32_e32 v6, v61, v6
	v_max_u32_e32 v61, v64, v12
	v_min_u32_e32 v12, v64, v12
	v_min_u32_e32 v10, v10, v52
	v_max_u32_e32 v52, v74, v72
	v_min_u32_e32 v72, v74, v72
	v_min_u32_e32 v15, v15, v49
	v_max_u32_e32 v49, v58, v54
	v_min_u32_e32 v54, v58, v54
	v_max_u32_e32 v64, v71, v66
	v_min_u32_e32 v66, v71, v66
	v_max_u32_e32 v71, v61, v9
	v_min_u32_e32 v9, v61, v9
	v_max_u32_e32 v61, v12, v7
	v_min_u32_e32 v7, v12, v7
	v_max_u32_e32 v12, v69, v8
	v_min_u32_e32 v8, v69, v8
	v_max_u32_e32 v69, v67, v11
	v_max_u32_e32 v74, v116, v48
	v_min_u32_e32 v48, v116, v48
	v_max_u32_e32 v116, v52, v77
	v_min_u32_e32 v52, v52, v77
	v_max_u32_e32 v77, v72, v14
	v_min_u32_e32 v14, v72, v14
	v_max_u32_e32 v72, v73, v79
	v_min_u32_e32 v73, v73, v79
	v_max_u32_e32 v79, v50, v78
	v_max_u32_e32 v58, v123, v55
	v_min_u32_e32 v55, v123, v55
	v_max_u32_e32 v123, v49, v108
	v_min_u32_e32 v49, v49, v108
	v_max_u32_e32 v108, v54, v51
	v_min_u32_e32 v51, v54, v51
	v_max_u32_e32 v54, v56, v59
	v_min_u32_e32 v56, v56, v59
	v_max_u32_e32 v59, v106, v57
	v_min_u32_e32 v11, v67, v11
	v_max_u32_e32 v67, v69, v8
	v_min_u32_e32 v8, v69, v8
	v_max_u32_e32 v69, v70, v13
	v_min_u32_e32 v13, v70, v13
	v_max_u32_e32 v70, v63, v0
	v_min_u32_e32 v50, v50, v78
	v_max_u32_e32 v78, v79, v73
	v_min_u32_e32 v73, v79, v73
	v_max_u32_e32 v79, v75, v105
	v_min_u32_e32 v75, v75, v105
	v_max_u32_e32 v105, v1, v4
	v_min_u32_e32 v57, v106, v57
	v_max_u32_e32 v106, v59, v56
	v_min_u32_e32 v56, v59, v56
	v_max_u32_e32 v59, v107, v60
	v_min_u32_e32 v60, v107, v60
	v_max_u32_e32 v107, v2, v3
	v_min_u32_e32 v0, v63, v0
	v_max_u32_e32 v63, v70, v13
	v_min_u32_e32 v13, v70, v13
	v_min_u32_e32 v1, v1, v4
	v_max_u32_e32 v4, v105, v75
	v_min_u32_e32 v75, v105, v75
	v_min_u32_e32 v2, v2, v3
	v_max_u32_e32 v3, v107, v60
	v_min_u32_e32 v60, v107, v60
	v_max_u32_e32 v70, v69, v67
	v_min_u32_e32 v67, v69, v67
	v_max_u32_e32 v69, v63, v8
	v_min_u32_e32 v8, v63, v8
	v_max_u32_e32 v63, v13, v11
	v_min_u32_e32 v11, v13, v11
	v_max_u32_e32 v105, v79, v78
	v_min_u32_e32 v78, v79, v78
	v_max_u32_e32 v79, v4, v73
	v_min_u32_e32 v4, v4, v73
	v_max_u32_e32 v73, v75, v50
	v_min_u32_e32 v50, v75, v50
	v_max_u32_e32 v107, v59, v106
	v_min_u32_e32 v59, v59, v106
	v_max_u32_e32 v106, v3, v56
	v_min_u32_e32 v3, v3, v56
	v_max_u32_e32 v56, v60, v57
	v_min_u32_e32 v57, v60, v57
	v_min_u32_e32 v13, v12, v64
	v_min_u32_e32 v109, v70, v66
	v_min_u32_e32 v110, v67, v71
	v_min_u32_e32 v111, v69, v9
	v_min_u32_e32 v112, v8, v61
	v_min_u32_e32 v113, v63, v7
	v_min_u32_e32 v114, v11, v6
	v_min_u32_e32 v75, v72, v74
	v_min_u32_e32 v117, v105, v48
	v_min_u32_e32 v118, v78, v116
	v_min_u32_e32 v119, v79, v52
	v_min_u32_e32 v120, v4, v77
	v_min_u32_e32 v121, v73, v14
	v_min_u32_e32 v122, v50, v10
	v_max_u32_e32 v60, v54, v58
	v_min_u32_e32 v54, v54, v58
	v_max_u32_e32 v58, v107, v55
	v_min_u32_e32 v55, v107, v55
	v_max_u32_e32 v107, v59, v123
	v_min_u32_e32 v59, v59, v123
	v_max_u32_e32 v123, v106, v49
	v_min_u32_e32 v49, v106, v49
	v_max_u32_e32 v106, v3, v108
	v_min_u32_e32 v3, v3, v108
	v_max_u32_e32 v108, v56, v51
	v_min_u32_e32 v51, v56, v51
	v_max_u32_e32 v56, v57, v15
	v_min_u32_e32 v15, v57, v15
	v_min_u32_e32 v57, v62, v5
	v_max3_u32 v1, v68, v65, v1
	v_max3_u32 v12, v12, v64, v122
	v_max3_u32 v10, v13, v50, v10
	v_max3_u32 v13, v70, v66, v121
	v_max3_u32 v14, v109, v73, v14
	v_max3_u32 v50, v67, v71, v120
	v_max3_u32 v4, v110, v4, v77
	v_max3_u32 v9, v69, v9, v119
	v_max3_u32 v52, v111, v79, v52
	v_max3_u32 v8, v8, v61, v118
	v_max3_u32 v61, v112, v78, v116
	v_max3_u32 v7, v63, v7, v117
	v_max3_u32 v48, v113, v105, v48
	v_max3_u32 v6, v11, v6, v75
	v_max3_u32 v11, v114, v72, v74
	v_max3_u32 v0, v0, v115, v76
	v_max_u32_e32 v15, v15, v57
; #define LDS_WAIT() asm volatile("s_waitcnt lgkmcnt(0)" ::: "memory")
; __device__ __forceinline__ float ord2f(unsigned o) { return __uint_as_float(o ^ (~(unsigned)((int)o >> 31) | 0x80000000u)); }
; template <int A, int B, int TOT> DEVFN void merge_top16(unsigned (&a)[TOT]) {
; #pragma unroll
;     for (int i = 0; i < 16; ++i) { const unsigned x = a[A + i], y = a[B + 15 - i]; a[A + i] = x > y ? x : y; }
;     bitonic_merge16_desc<A, TOT>(a);
; }
; DEVFN void top16of64(unsigned (&a)[64]) {
;     sort16_desc<0, 64>(a); sort16_desc<16, 64>(a); sort16_desc<32, 64>(a); sort16_desc<48, 64>(a);
;     merge_top16<0, 16, 64>(a); merge_top16<32, 48, 64>(a); merge_top16<0, 32, 64>(a);
; }
; __device__ __forceinline__ void phase_topk(Frame& F, const bf16_t* QP, const bf16_t* K1B, const bf16_t* K2B, unsigned short* EID, float* GATE) {
;     ...
;         __builtin_amdgcn_sched_barrier(0); top16of64(Cd); __builtin_amdgcn_sched_barrier(0);
;         LDS_WAIT();
;         unsigned eid[16]; float e[16]; float sum = 0.f; const float v0 = ord2f(Cd[0] & ~255u);
; #pragma unroll
;         for (int r = 0; r < 16; ++r) { const unsigned c = 255u - (Cd[r] & 255u); eid[r] = I1s[(c >> 4) * 64 + lane] * 128u + I2s[(c & 15u) * 64 + lane];
	v_max3_u32 v2, v2, v62, v5
	v_max_u32_e32 v63, v1, v52
	v_min_u32_e32 v1, v1, v52
	v_max_u32_e32 v52, v12, v8
	v_min_u32_e32 v8, v12, v8
	v_max_u32_e32 v12, v10, v61
	v_min_u32_e32 v10, v10, v61
	v_max_u32_e32 v61, v13, v7
	v_min_u32_e32 v7, v13, v7
	v_max_u32_e32 v13, v14, v48
	v_min_u32_e32 v14, v14, v48
	v_max_u32_e32 v48, v50, v6
	v_min_u32_e32 v6, v50, v6
	v_max_u32_e32 v50, v4, v11
	v_min_u32_e32 v4, v4, v11
	v_max_u32_e32 v11, v9, v0
	v_min_u32_e32 v0, v9, v0
	v_max_u32_e32 v5, v53, v49
	v_min_u32_e32 v49, v53, v49
	v_max_u32_e32 v53, v60, v106
	v_min_u32_e32 v57, v60, v106
	v_max_u32_e32 v60, v54, v3
	v_min_u32_e32 v3, v54, v3
	v_max_u32_e32 v54, v58, v108
	v_min_u32_e32 v58, v58, v108
	v_max_u32_e32 v62, v55, v51
	v_min_u32_e32 v51, v55, v51
	v_max_u32_e32 v55, v107, v56
	v_min_u32_e32 v56, v107, v56
	v_max_u32_e32 v71, v59, v15
	v_min_u32_e32 v15, v59, v15
	v_max_u32_e32 v59, v123, v2
	v_min_u32_e32 v2, v123, v2
	v_max_u32_e32 v9, v63, v13
	v_min_u32_e32 v13, v63, v13
	v_max_u32_e32 v63, v52, v48
	v_min_u32_e32 v48, v52, v48
	v_max_u32_e32 v52, v12, v50
	v_min_u32_e32 v12, v12, v50
	v_max_u32_e32 v50, v61, v11
	v_min_u32_e32 v11, v61, v11
	v_max_u32_e32 v61, v1, v14
	v_min_u32_e32 v1, v1, v14
	v_max_u32_e32 v14, v8, v6
	v_min_u32_e32 v6, v8, v6
	v_max_u32_e32 v8, v10, v4
	v_min_u32_e32 v4, v10, v4
	v_max_u32_e32 v10, v7, v0
	v_min_u32_e32 v0, v7, v0
	v_max_u32_e32 v72, v5, v62
	v_min_u32_e32 v5, v5, v62
	v_max_u32_e32 v62, v53, v55
	v_min_u32_e32 v53, v53, v55
	v_max_u32_e32 v55, v60, v71
	v_min_u32_e32 v60, v60, v71
	v_max_u32_e32 v71, v54, v59
	v_min_u32_e32 v54, v54, v59
	v_max_u32_e32 v59, v49, v51
	v_min_u32_e32 v49, v49, v51
	v_max_u32_e32 v51, v57, v56
	v_min_u32_e32 v56, v57, v56
	v_max_u32_e32 v57, v3, v15
	v_min_u32_e32 v3, v3, v15
	v_max_u32_e32 v15, v58, v2
	v_min_u32_e32 v2, v58, v2
	v_max_u32_e32 v7, v9, v52
	v_min_u32_e32 v9, v9, v52
	v_max_u32_e32 v52, v63, v50
	v_min_u32_e32 v50, v63, v50
	v_max_u32_e32 v63, v13, v12
	v_min_u32_e32 v12, v13, v12
	v_max_u32_e32 v13, v48, v11
	v_min_u32_e32 v11, v48, v11
	v_max_u32_e32 v48, v61, v8
	v_min_u32_e32 v8, v61, v8
	v_max_u32_e32 v61, v14, v10
	v_min_u32_e32 v10, v14, v10
	v_max_u32_e32 v14, v1, v4
	v_min_u32_e32 v1, v1, v4
	v_max_u32_e32 v4, v6, v0
	v_min_u32_e32 v0, v6, v0
	v_max_u32_e32 v58, v72, v55
	v_min_u32_e32 v55, v72, v55
	v_max_u32_e32 v72, v62, v71
	v_min_u32_e32 v62, v62, v71
	v_max_u32_e32 v71, v5, v60
	v_min_u32_e32 v5, v5, v60
	v_max_u32_e32 v60, v53, v54
	v_min_u32_e32 v53, v53, v54
	v_max_u32_e32 v54, v59, v57
	v_min_u32_e32 v57, v59, v57
	v_max_u32_e32 v59, v51, v15
	v_min_u32_e32 v15, v51, v15
	v_max_u32_e32 v51, v49, v3
	v_min_u32_e32 v3, v49, v3
	v_max_u32_e32 v49, v56, v2
	v_min_u32_e32 v2, v56, v2
	v_min_u32_e32 v6, v7, v52
	v_min_u32_e32 v64, v9, v50
	v_min_u32_e32 v65, v63, v13
	v_min_u32_e32 v66, v12, v11
	v_min_u32_e32 v67, v48, v61
	v_min_u32_e32 v68, v8, v10
	v_min_u32_e32 v69, v14, v4
	v_min_u32_e32 v70, v1, v0
	v_min_u32_e32 v56, v58, v72
	v_min_u32_e32 v73, v55, v62
	v_min_u32_e32 v74, v71, v60
	v_min_u32_e32 v75, v5, v53
	v_min_u32_e32 v76, v54, v59
	v_min_u32_e32 v77, v57, v15
	v_min_u32_e32 v78, v51, v49
	v_min_u32_e32 v79, v3, v2
	v_max3_u32 v7, v7, v52, v79
	v_max3_u32 v2, v6, v3, v2
	v_max3_u32 v3, v9, v50, v78
	v_max3_u32 v6, v64, v51, v49
	v_max3_u32 v9, v63, v13, v77
	v_max3_u32 v13, v65, v57, v15
	v_max3_u32 v11, v12, v11, v76
	v_max3_u32 v12, v66, v54, v59
	v_max3_u32 v15, v48, v61, v75
	v_max3_u32 v5, v67, v5, v53
	v_max3_u32 v8, v8, v10, v74
	v_max3_u32 v10, v68, v71, v60
	v_max3_u32 v4, v14, v4, v73
	v_max3_u32 v14, v69, v55, v62
	v_max3_u32 v0, v1, v0, v56
	v_max3_u32 v1, v70, v58, v72
	v_max_u32_e32 v48, v7, v15
	v_min_u32_e32 v7, v7, v15
	v_max_u32_e32 v15, v2, v5
	v_min_u32_e32 v2, v2, v5
	v_max_u32_e32 v5, v3, v8
	v_min_u32_e32 v3, v3, v8
	v_max_u32_e32 v8, v6, v10
	v_min_u32_e32 v6, v6, v10
	v_max_u32_e32 v10, v9, v4
	v_min_u32_e32 v4, v9, v4
	v_max_u32_e32 v9, v13, v14
	v_min_u32_e32 v13, v13, v14
	v_max_u32_e32 v14, v11, v0
	v_min_u32_e32 v0, v11, v0
	v_max_u32_e32 v11, v12, v1
	v_min_u32_e32 v1, v12, v1
	v_max_u32_e32 v12, v48, v10
	v_min_u32_e32 v10, v48, v10
	v_max_u32_e32 v48, v15, v9
	v_min_u32_e32 v9, v15, v9
	v_max_u32_e32 v15, v5, v14
	v_min_u32_e32 v5, v5, v14
	v_max_u32_e32 v14, v8, v11
	v_min_u32_e32 v8, v8, v11
	v_max_u32_e32 v11, v7, v4
	v_min_u32_e32 v4, v7, v4
	v_max_u32_e32 v7, v2, v13
	v_min_u32_e32 v2, v2, v13
	v_max_u32_e32 v13, v3, v0
	v_min_u32_e32 v0, v3, v0
	v_max_u32_e32 v3, v6, v1
	v_min_u32_e32 v1, v6, v1
	v_max_u32_e32 v6, v12, v15
	v_min_u32_e32 v12, v12, v15
	v_max_u32_e32 v15, v48, v14
	v_min_u32_e32 v14, v48, v14
	v_max_u32_e32 v48, v10, v5
	v_min_u32_e32 v5, v10, v5
	v_max_u32_e32 v10, v9, v8
	v_min_u32_e32 v8, v9, v8
	v_max_u32_e32 v9, v11, v13
	v_min_u32_e32 v11, v11, v13
	v_max_u32_e32 v13, v7, v3
	v_min_u32_e32 v3, v7, v3
	v_max_u32_e32 v7, v4, v0
	v_min_u32_e32 v0, v4, v0
	v_max_u32_e32 v4, v2, v1
	v_min_u32_e32 v1, v2, v1
	v_max_u32_e32 v2, v6, v15
	v_min_u32_e32 v6, v6, v15
	v_max_u32_e32 v50, v12, v14
	v_min_u32_e32 v12, v12, v14
	v_max_u32_e32 v52, v48, v10
	v_min_u32_e32 v10, v48, v10
	v_max_u32_e32 v54, v5, v8
	v_min_u32_e32 v5, v5, v8
	v_max_u32_e32 v56, v9, v13
	v_min_u32_e32 v9, v9, v13
	v_max_u32_e32 v58, v11, v3
	v_min_u32_e32 v3, v11, v3
	v_max_u32_e32 v60, v7, v4
	v_min_u32_e32 v4, v7, v4
	v_max_u32_e32 v62, v0, v1
	v_min_u32_e32 v0, v0, v1
	v_not_b32_e32 v49, v2
	v_not_b32_e32 v15, v6
	v_not_b32_e32 v51, v50
	v_not_b32_e32 v14, v12
	v_not_b32_e32 v53, v52
	v_not_b32_e32 v48, v10
	v_not_b32_e32 v55, v54
	v_not_b32_e32 v8, v5
	v_not_b32_e32 v57, v56
	v_not_b32_e32 v13, v9
	v_not_b32_e32 v59, v58
	v_not_b32_e32 v11, v3
	v_not_b32_e32 v61, v60
	v_not_b32_e32 v7, v4
	v_not_b32_e32 v63, v62
	v_not_b32_e32 v1, v0
	v_lshlrev_b32_e32 v64, 4, v49
	v_lshlrev_b32_e32 v49, 8, v49
	v_lshlrev_b32_e32 v65, 4, v15
	v_lshlrev_b32_e32 v15, 8, v15
	v_lshlrev_b32_e32 v66, 4, v51
	v_lshlrev_b32_e32 v51, 8, v51
	v_lshlrev_b32_e32 v67, 4, v14
	v_lshlrev_b32_e32 v14, 8, v14
	v_and_b32_e32 v64, 0xf00, v64
	v_and_b32_e32 v49, 0xf00, v49
	v_and_b32_e32 v65, 0xf00, v65
	v_and_b32_e32 v15, 0xf00, v15
	v_and_b32_e32 v66, 0xf00, v66
	v_and_b32_e32 v51, 0xf00, v51
	v_and_b32_e32 v67, 0xf00, v67
	v_and_b32_e32 v14, 0xf00, v14
	s_waitcnt lgkmcnt(0)
; #define LDS_WAIT() asm volatile("s_waitcnt lgkmcnt(0)" ::: "memory")
; __device__ __forceinline__ float ord2f(unsigned o) { return __uint_as_float(o ^ (~(unsigned)((int)o >> 31) | 0x80000000u)); }
; __device__ __forceinline__ void phase_topk(Frame& F, const bf16_t* QP, const bf16_t* K1B, const bf16_t* K2B, unsigned short* EID, float* GATE) {
;     ...
;         LDS_WAIT();
;         unsigned eid[16]; float e[16]; float sum = 0.f; const float v0 = ord2f(Cd[0] & ~255u);
; #pragma unroll
;         for (int r = 0; r < 16; ++r) { const unsigned c = 255u - (Cd[r] & 255u); eid[r] = I1s[(c >> 4) * 64 + lane] * 128u + I2s[(c & 15u) * 64 + lane];
;             e[r] = __builtin_amdgcn_exp2f((ord2f(Cd[r] & ~255u) - v0) * LOG2E); sum += e[r]; }
	v_add_u32_e32 v64, v90, v64
	v_add_u32_e32 v49, v90, v49
	v_add_u32_e32 v65, v90, v65
	v_add_u32_e32 v15, v90, v15
	v_add_u32_e32 v66, v90, v66
	v_add_u32_e32 v51, v90, v51
	v_add_u32_e32 v67, v90, v67
	v_add_u32_e32 v14, v90, v14
	ds_read_b32 v64, v64
	ds_read_b32 v49, v49 offset:4096
	ds_read_b32 v65, v65
	ds_read_b32 v15, v15 offset:4096
	ds_read_b32 v66, v66
	ds_read_b32 v51, v51 offset:4096
	ds_read_b32 v67, v67
	ds_read_b32 v14, v14 offset:4096
	v_cmp_lt_i32_e32 vcc, -1, v6
	s_waitcnt lgkmcnt(6)
	v_lshl_add_u32 v49, v64, 7, v49
	s_waitcnt lgkmcnt(4)
	v_lshl_add_u32 v15, v65, 7, v15
	v_cndmask_b32_e64 v64, v104, -1, vcc
	v_cmp_lt_i32_e32 vcc, -1, v50
	v_bitop3_b32 v6, v64, v6, s9 bitop3:0x78
	s_waitcnt lgkmcnt(2)
	v_lshl_add_u32 v51, v66, 7, v51
	v_cndmask_b32_e64 v64, v104, -1, vcc
	v_cmp_lt_i32_e32 vcc, -1, v12
	v_bitop3_b32 v50, v64, v50, s9 bitop3:0x78
	s_waitcnt lgkmcnt(0)
	v_lshl_add_u32 v14, v67, 7, v14
	v_cndmask_b32_e64 v64, v104, -1, vcc
	v_bitop3_b32 v12, v64, v12, s9 bitop3:0x78
	v_lshlrev_b32_e32 v64, 4, v53
	v_lshlrev_b32_e32 v53, 8, v53
	v_lshlrev_b32_e32 v65, 4, v48
	v_lshlrev_b32_e32 v48, 8, v48
	v_lshlrev_b32_e32 v66, 4, v55
	v_lshlrev_b32_e32 v55, 8, v55
	v_lshlrev_b32_e32 v67, 4, v8
	v_lshlrev_b32_e32 v8, 8, v8
	v_and_b32_e32 v64, 0xf00, v64
	v_and_b32_e32 v53, 0xf00, v53
	v_and_b32_e32 v65, 0xf00, v65
	v_and_b32_e32 v48, 0xf00, v48
	v_and_b32_e32 v66, 0xf00, v66
	v_and_b32_e32 v55, 0xf00, v55
	v_and_b32_e32 v67, 0xf00, v67
	v_and_b32_e32 v8, 0xf00, v8
	v_add_u32_e32 v64, v90, v64
	v_add_u32_e32 v53, v90, v53
	v_add_u32_e32 v65, v90, v65
	v_add_u32_e32 v48, v90, v48
	v_add_u32_e32 v66, v90, v66
	v_add_u32_e32 v55, v90, v55
	v_add_u32_e32 v67, v90, v67
	v_add_u32_e32 v8, v90, v8
	ds_read_b32 v64, v64
	ds_read_b32 v53, v53 offset:4096
	ds_read_b32 v65, v65
	ds_read_b32 v48, v48 offset:4096
	ds_read_b32 v66, v66
	ds_read_b32 v55, v55 offset:4096
	ds_read_b32 v67, v67
	ds_read_b32 v8, v8 offset:4096
	v_cmp_lt_i32_e32 vcc, -1, v52
	s_waitcnt lgkmcnt(6)
	v_lshl_add_u32 v53, v64, 7, v53
	s_waitcnt lgkmcnt(4)
	v_lshl_add_u32 v48, v65, 7, v48
	v_cndmask_b32_e64 v64, v104, -1, vcc
	v_cmp_lt_i32_e32 vcc, -1, v10
	v_bitop3_b32 v52, v64, v52, s9 bitop3:0x78
	v_and_b32_e32 v65, 0xffffff00, v5
	v_cndmask_b32_e64 v64, v104, -1, vcc
	v_cmp_lt_i32_e32 vcc, -1, v54
	v_bitop3_b32 v10, v64, v10, s9 bitop3:0x78
	s_waitcnt lgkmcnt(0)
	v_lshl_add_u32 v8, v67, 7, v8
	v_cndmask_b32_e64 v64, v104, -1, vcc
	v_cmp_lt_i32_e32 vcc, -1, v2
	v_bitop3_b32 v54, v64, v54, s9 bitop3:0x78
	v_and_b32_e32 v64, 0xffffff00, v2
	v_cndmask_b32_e64 v2, v104, -1, vcc
	v_xor_b32_e32 v2, v2, v64
	v_sub_f32_e32 v64, v2, v2
	v_mul_f32_e32 v64, 0x3fb8aa3b, v64
	v_sub_f32_e32 v6, v6, v2
	v_exp_f32_e32 v64, v64
	v_mul_f32_e32 v6, 0x3fb8aa3b, v6
	v_sub_f32_e32 v50, v50, v2
	v_exp_f32_e32 v6, v6
	v_mul_f32_e32 v50, 0x3fb8aa3b, v50
	v_sub_f32_e32 v12, v12, v2
	v_cmp_lt_i32_e32 vcc, -1, v5
	v_exp_f32_e32 v50, v50
	v_mul_f32_e32 v12, 0x3fb8aa3b, v12
	v_sub_f32_e32 v52, v52, v2
	v_cndmask_b32_e64 v5, v104, -1, vcc
	v_exp_f32_e32 v12, v12
	v_mul_f32_e32 v52, 0x3fb8aa3b, v52
	v_xor_b32_e32 v5, v5, v65
	v_add_f32_e32 v65, 0, v64
	v_exp_f32_e32 v52, v52
	v_add_f32_e32 v65, v6, v65
	v_cmp_lt_i32_e32 vcc, -1, v56
	v_add_f32_e32 v65, v50, v65
	v_sub_f32_e32 v5, v5, v2
	v_cndmask_b32_e64 v67, v104, -1, vcc
	v_cmp_lt_i32_e32 vcc, -1, v9
	v_add_f32_e32 v65, v12, v65
	v_mul_f32_e32 v5, 0x3fb8aa3b, v5
	v_cndmask_b32_e64 v68, v104, -1, vcc
	v_lshl_add_u32 v55, v66, 7, v55
	v_exp_f32_e32 v66, v5
	v_add_f32_e32 v5, v52, v65
	v_lshlrev_b32_e32 v65, 4, v57
	v_lshlrev_b32_e32 v57, 8, v57
	v_bitop3_b32 v56, v67, v56, s9 bitop3:0x78
	v_lshlrev_b32_e32 v67, 4, v13
	v_lshlrev_b32_e32 v13, 8, v13
	v_bitop3_b32 v9, v68, v9, s9 bitop3:0x78
	v_lshlrev_b32_e32 v68, 4, v59
	v_lshlrev_b32_e32 v59, 8, v59
	v_lshlrev_b32_e32 v69, 4, v11
	v_lshlrev_b32_e32 v11, 8, v11
	v_and_b32_e32 v65, 0xf00, v65
	v_and_b32_e32 v57, 0xf00, v57
	v_and_b32_e32 v67, 0xf00, v67
	v_and_b32_e32 v13, 0xf00, v13
	v_and_b32_e32 v68, 0xf00, v68
	v_and_b32_e32 v59, 0xf00, v59
	v_and_b32_e32 v69, 0xf00, v69
	v_and_b32_e32 v11, 0xf00, v11
	v_add_u32_e32 v65, v90, v65
	v_add_u32_e32 v57, v90, v57
	v_add_u32_e32 v67, v90, v67
	v_add_u32_e32 v13, v90, v13
	v_add_u32_e32 v68, v90, v68
	v_add_u32_e32 v59, v90, v59
	v_add_u32_e32 v69, v90, v69
	v_add_u32_e32 v11, v90, v11
	ds_read_b32 v65, v65
	ds_read_b32 v57, v57 offset:4096
	ds_read_b32 v67, v67
	ds_read_b32 v13, v13 offset:4096
	ds_read_b32 v68, v68
	ds_read_b32 v59, v59 offset:4096
	ds_read_b32 v69, v69
	ds_read_b32 v11, v11 offset:4096
	v_cmp_lt_i32_e32 vcc, -1, v58
	s_waitcnt lgkmcnt(6)
	v_lshl_add_u32 v57, v65, 7, v57
	s_waitcnt lgkmcnt(4)
; #define LDS_WAIT() asm volatile("s_waitcnt lgkmcnt(0)" ::: "memory")
; __device__ __forceinline__ float ord2f(unsigned o) { return __uint_as_float(o ^ (~(unsigned)((int)o >> 31) | 0x80000000u)); }
; __device__ __forceinline__ void phase_topk(Frame& F, const bf16_t* QP, const bf16_t* K1B, const bf16_t* K2B, unsigned short* EID, float* GATE) {
;     ...
;         for (int r = 0; r < 16; ++r) { const unsigned c = 255u - (Cd[r] & 255u); eid[r] = I1s[(c >> 4) * 64 + lane] * 128u + I2s[(c & 15u) * 64 + lane];
;             e[r] = __builtin_amdgcn_exp2f((ord2f(Cd[r] & ~255u) - v0) * LOG2E); sum += e[r]; }
;         const float inv = 1.f / sum;
;         u32x4 ew; ew.x = (hi ? eid[8] : eid[0]) | ((hi ? eid[9] : eid[1]) << 16); ew.y = (hi ? eid[10] : eid[2]) | ((hi ? eid[11] : eid[3]) << 16);
;         ew.z = (hi ? eid[12] : eid[4]) | ((hi ? eid[13] : eid[5]) << 16); ew.w = (hi ? eid[14] : eid[6]) | ((hi ? eid[15] : eid[7]) << 16);
;         *(u32x4*)(EID + (size_t)t * 128 + h * 16 + 8 * hi) = ew;
;         const f32x4 g0 = {(hi ? e[8] : e[0]) * inv, (hi ? e[9] : e[1]) * inv, (hi ? e[10] : e[2]) * inv, (hi ? e[11] : e[3]) * inv};
;         const f32x4 g1 = {(hi ? e[12] : e[4]) * inv, (hi ? e[13] : e[5]) * inv, (hi ? e[14] : e[6]) * inv, (hi ? e[15] : e[7]) * inv};
;         *(f32x4*)(GATE + (size_t)t * 128 + h * 16 + 8 * hi) = g0; *(f32x4*)(GATE + (size_t)t * 128 + h * 16 + 8 * hi + 4) = g1;
;         LDS_WAIT();
	v_lshl_add_u32 v13, v67, 7, v13
	v_cndmask_b32_e64 v65, v104, -1, vcc
	v_cmp_lt_i32_e32 vcc, -1, v3
	v_bitop3_b32 v58, v65, v58, s9 bitop3:0x78
	s_waitcnt lgkmcnt(0)
	v_lshl_add_u32 v11, v69, 7, v11
	v_cndmask_b32_e64 v65, v104, -1, vcc
	v_bitop3_b32 v3, v65, v3, s9 bitop3:0x78
	v_sub_f32_e32 v3, v3, v2
	v_mul_f32_e32 v3, 0x3fb8aa3b, v3
	v_exp_f32_e32 v65, v3
	v_lshl_add_u32 v3, v68, 7, v59
	v_lshlrev_b32_e32 v59, 4, v61
	v_lshlrev_b32_e32 v61, 8, v61
	v_lshlrev_b32_e32 v67, 4, v7
	v_lshlrev_b32_e32 v7, 8, v7
	v_lshlrev_b32_e32 v68, 4, v63
	v_lshlrev_b32_e32 v63, 8, v63
	v_lshlrev_b32_e32 v69, 4, v1
	v_lshlrev_b32_e32 v1, 8, v1
	v_and_b32_e32 v59, 0xf00, v59
	v_and_b32_e32 v61, 0xf00, v61
	v_and_b32_e32 v67, 0xf00, v67
	v_and_b32_e32 v7, 0xf00, v7
	v_and_b32_e32 v68, 0xf00, v68
	v_and_b32_e32 v63, 0xf00, v63
	v_and_b32_e32 v69, 0xf00, v69
	v_and_b32_e32 v1, 0xf00, v1
	v_add_u32_e32 v59, v90, v59
	v_add_u32_e32 v61, v90, v61
	v_add_u32_e32 v67, v90, v67
	v_add_u32_e32 v7, v90, v7
	v_add_u32_e32 v68, v90, v68
	v_add_u32_e32 v63, v90, v63
	v_add_u32_e32 v69, v90, v69
	v_add_u32_e32 v1, v90, v1
	ds_read_b32 v59, v59
	ds_read_b32 v61, v61 offset:4096
	ds_read_b32 v67, v67
	ds_read_b32 v7, v7 offset:4096
	ds_read_b32 v68, v68
	ds_read_b32 v63, v63 offset:4096
	ds_read_b32 v69, v69
	ds_read_b32 v1, v1 offset:4096
	v_cmp_lt_i32_e32 vcc, -1, v60
	s_waitcnt lgkmcnt(6)
	v_lshl_add_u32 v59, v59, 7, v61
	v_sub_f32_e32 v10, v10, v2
	v_cndmask_b32_e64 v61, v104, -1, vcc
	v_cmp_lt_i32_e32 vcc, -1, v4
	v_bitop3_b32 v60, v61, v60, s9 bitop3:0x78
	v_mul_f32_e32 v10, 0x3fb8aa3b, v10
	v_cndmask_b32_e64 v61, v104, -1, vcc
	v_sub_f32_e32 v54, v54, v2
	v_bitop3_b32 v4, v61, v4, s9 bitop3:0x78
	v_exp_f32_e32 v10, v10
	v_mul_f32_e32 v54, 0x3fb8aa3b, v54
	v_sub_f32_e32 v4, v4, v2
	v_exp_f32_e32 v54, v54
	v_sub_f32_e32 v56, v56, v2
	v_mul_f32_e32 v4, 0x3fb8aa3b, v4
	v_cmp_lt_i32_e32 vcc, -1, v62
	v_mul_f32_e32 v56, 0x3fb8aa3b, v56
	v_sub_f32_e32 v9, v9, v2
	v_exp_f32_e32 v61, v4
	v_cndmask_b32_e64 v4, v104, -1, vcc
	v_exp_f32_e32 v56, v56
	v_mul_f32_e32 v9, 0x3fb8aa3b, v9
	v_sub_f32_e32 v58, v58, v2
	v_bitop3_b32 v4, v4, v62, s9 bitop3:0x78
	v_add_f32_e32 v5, v10, v5
	v_exp_f32_e32 v9, v9
	v_mul_f32_e32 v58, 0x3fb8aa3b, v58
	v_sub_f32_e32 v4, v4, v2
	v_add_f32_e32 v5, v54, v5
	v_exp_f32_e32 v58, v58
	v_sub_f32_e32 v60, v60, v2
	v_mul_f32_e32 v4, 0x3fb8aa3b, v4
	v_cmp_lt_i32_e32 vcc, -1, v0
	v_add_f32_e32 v5, v66, v5
	v_mul_f32_e32 v60, 0x3fb8aa3b, v60
	v_exp_f32_e32 v62, v4
	v_cndmask_b32_e64 v4, v104, -1, vcc
	v_add_f32_e32 v5, v56, v5
	v_exp_f32_e32 v60, v60
	v_bitop3_b32 v0, v4, v0, s9 bitop3:0x78
	v_add_f32_e32 v5, v9, v5
	v_sub_f32_e32 v0, v0, v2
	v_add_f32_e32 v5, v58, v5
	v_mul_f32_e32 v0, 0x3fb8aa3b, v0
	v_add_f32_e32 v5, v65, v5
	v_exp_f32_e32 v70, v0
	v_add_f32_e32 v0, v60, v5
	v_add_f32_e32 v0, v61, v0
	v_add_f32_e32 v0, v62, v0
	v_add_f32_e32 v0, v70, v0
	v_div_scale_f32 v2, s[34:35], v0, v0, 1.0
	v_rcp_f32_e32 v4, v2
	s_waitcnt lgkmcnt(4)
	v_lshl_add_u32 v5, v67, 7, v7
	s_waitcnt lgkmcnt(2)
	v_lshl_add_u32 v7, v68, 7, v63
	s_waitcnt lgkmcnt(0)
	v_lshl_add_u32 v63, v69, 7, v1
	v_fma_f32 v1, -v2, v4, 1.0
	v_fmac_f32_e32 v4, v1, v4
	v_div_scale_f32 v1, vcc, 1.0, v0, 1.0
	v_mul_f32_e32 v67, v1, v4
	v_fma_f32 v68, -v2, v67, v1
	v_fmac_f32_e32 v67, v68, v4
	v_fma_f32 v1, -v2, v67, v1
	v_div_fmas_f32 v1, v1, v4, v67
	v_div_fixup_f32 v67, v1, v0, 1.0
	v_cndmask_b32_e64 v0, v57, v49, s[2:3]
	v_cndmask_b32_e64 v1, v13, v15, s[2:3]
	v_lshl_or_b32 v0, v1, 16, v0
	v_cndmask_b32_e64 v1, v3, v51, s[2:3]
	v_cndmask_b32_e64 v2, v11, v14, s[2:3]
	v_lshl_or_b32 v1, v2, 16, v1
	v_cndmask_b32_e64 v2, v59, v53, s[2:3]
	v_cndmask_b32_e64 v3, v5, v48, s[2:3]
	v_lshl_or_b32 v2, v3, 16, v2
	v_cndmask_b32_e64 v3, v7, v55, s[2:3]
	v_cndmask_b32_e64 v4, v63, v8, s[2:3]
	v_lshl_or_b32 v3, v4, 16, v3
	v_lshlrev_b64 v[4:5], 8, v[80:81]
	v_lshl_add_u64 v[4:5], v[82:83], 0, v[4:5]
	global_store_dwordx4 v[4:5], v[0:3], off
	v_cndmask_b32_e64 v4, v60, v52, s[2:3]
	v_cndmask_b32_e64 v5, v61, v10, s[2:3]
	v_cndmask_b32_e64 v0, v56, v64, s[2:3]
	v_cndmask_b32_e64 v1, v9, v6, s[2:3]
	v_cndmask_b32_e64 v2, v58, v50, s[2:3]
	v_cndmask_b32_e64 v3, v65, v12, s[2:3]
	v_lshlrev_b64 v[8:9], 9, v[80:81]
	v_mul_f32_e32 v0, v0, v67
	v_mul_f32_e32 v1, v1, v67
	v_mul_f32_e32 v2, v2, v67
	v_mul_f32_e32 v3, v3, v67
	v_cndmask_b32_e64 v6, v62, v54, s[2:3]
	v_cndmask_b32_e64 v7, v70, v66, s[2:3]
	v_lshl_add_u64 v[8:9], v[84:85], 0, v[8:9]
	v_mul_f32_e32 v4, v4, v67
	v_mul_f32_e32 v5, v5, v67
	v_mul_f32_e32 v6, v6, v67
	v_mul_f32_e32 v7, v7, v67
	global_store_dwordx4 v[8:9], v[0:3], off
	global_store_dwordx4 v[8:9], v[4:7], off offset:16
	s_waitcnt lgkmcnt(0)
	v_add_u32_e32 v80, s10, v80
	s_and_b64 vcc, exec, s[4:5]
	s_mov_b32 s33, s31
	s_cbranch_vccnz .LBB0_822
